# ph3: LayerNorm gamma/beta hoisted out of the batch loop, row prefetch a full trip ahead; all xor-16 butterfly steps via v_permlane16_swap instead of ds_swizzle
# speedup vs baseline: 1.0577x; 1.0048x over previous
; __device__ __forceinline__ float wave_max(float v) { v = fmaxf(v, dpp_f<0xB1>(v)); v = fmaxf(v, dpp_f<0x4E>(v)); v = fmaxf(v, dpp_f<0x141>(v)); v = fmaxf(v, dpp_f<0x140>(v)); v = fmaxf(v, xor_sw<16>(v)); return max_x32(v); }
; __device__ __forceinline__ float q8_row16(const float (&o)[16], unsigned char* qrow, int lane) {
;     float am = 0.f;
; #pragma unroll
;     for (int i = 0; i < 16; ++i) am = fmaxf(am, fabsf(o[i]));
;     am = wave_max(am);
;     const float qs = am > 0.f ? am * (1.0f / 127.0f) : 1.0f, qinv = 1.0f / qs;
; #pragma unroll
;     for (int hf = 0; hf < 2; ++hf) { u32x2 q; q.x = q8x4(o[8 * hf], o[8 * hf + 1], o[8 * hf + 2], o[8 * hf + 3], qinv); q.y = q8x4(o[8 * hf + 4], o[8 * hf + 5], o[8 * hf + 6], o[8 * hf + 7], qinv);
;         *(u32x2*)(qrow + 512 * hf + 8 * lane) = q; }
;     return qs;
; }
; __global__ void __launch_bounds__(NWAVES * 64, 2) mk_fwd(Args args) {
;     ...
;         const float* x = args.in[0];
;         for (int t = gw; t < T; t += NGW) {
;             float o[16];
; #pragma unroll
;             for (int hf = 0; hf < 2; ++hf) { const f32x4 a = *(const f32x4*)(x + (size_t)t * D + 512 * hf + 8 * lane), b = *(const f32x4*)(x + (size_t)t * D + 512 * hf + 8 * lane + 4);
; #pragma unroll
;                 for (int i = 0; i < 4; ++i) { o[8 * hf + i] = a[i]; o[8 * hf + 4 + i] = b[i]; } }
;             store_bf16_row16(o, XB + (size_t)t * D, lane);
;             const float qs = q8_row16(o, ws + WS_XQ + (size_t)t * D, lane);
;             if (lane == 0) ((float*)(ws + WS_SX))[t] = qs;
;         }
.LBB0_32:
	global_load_dwordx4 v[8:11], v[4:5], off
	global_load_dwordx4 v[12:15], v[4:5], off offset:16
	global_load_dwordx4 v[16:19], v[4:5], off offset:2048
	global_load_dwordx4 v[20:23], v[4:5], off offset:2064
	v_lshl_add_u64 v[24:25], s[84:85], 0, v[0:1]
	v_lshl_add_u64 v[26:27], s[84:85], 0, v[2:3]
	v_add_co_u32_e32 v32, vcc, s14, v24
	v_add_co_u32_e64 v34, s[2:3], s17, v26
	s_nop 0
	v_addc_co_u32_e32 v33, vcc, 0, v25, vcc
	v_addc_co_u32_e64 v35, s[2:3], 0, v27, s[2:3]
	s_waitcnt vmcnt(3)
	v_max3_f32 v7, |v8|, 0, |v9|
	v_max3_f32 v7, v7, |v10|, |v11|
	s_waitcnt vmcnt(2)
	v_max3_f32 v7, v7, |v12|, |v13|
	v_max3_f32 v7, v7, |v14|, |v15|
	s_waitcnt vmcnt(1)
	v_max3_f32 v7, v7, |v16|, |v17|
	v_max3_f32 v7, v7, |v18|, |v19|
	s_waitcnt vmcnt(0)
	v_max3_f32 v7, v7, |v20|, |v21|
	v_max3_f32 v7, v7, |v22|, |v23|
	v_cvt_pk_bf16_f32 v24, v8, v9
	v_cvt_pk_bf16_f32 v25, v10, v11
	v_mov_b32_dpp v29, v7 quad_perm:[1,0,3,2] row_mask:0xf bank_mask:0xf bound_ctrl:1
	v_max_f32_e32 v29, v29, v29
	v_max_f32_e32 v7, v7, v29
	v_cvt_pk_bf16_f32 v26, v12, v13
	v_cvt_pk_bf16_f32 v27, v14, v15
	v_mov_b32_dpp v29, v7 quad_perm:[2,3,0,1] row_mask:0xf bank_mask:0xf bound_ctrl:1
	v_max_f32_e32 v29, v29, v29
	v_max_f32_e32 v7, v7, v29
	global_store_dwordx4 v[32:33], v[24:27], off
	v_cvt_pk_bf16_f32 v28, v16, v17
	v_mov_b32_dpp v29, v7 row_half_mirror row_mask:0xf bank_mask:0xf bound_ctrl:1
	v_max_f32_e32 v29, v29, v29
	v_max_f32_e32 v7, v7, v29
	v_cvt_pk_bf16_f32 v30, v20, v21
	v_cvt_pk_bf16_f32 v31, v22, v23
	v_mov_b32_dpp v29, v7 row_mirror row_mask:0xf bank_mask:0xf bound_ctrl:1
	v_max_f32_e32 v29, v29, v29
	v_max_f32_e32 v7, v7, v29
	v_cvt_pk_bf16_f32 v29, v18, v19
	global_store_dwordx4 v[32:33], v[28:31], off offset:1024
	s_waitcnt lgkmcnt(0)
	v_mov_b32_e32 v36, v7
	s_nop 1
	v_permlane16_swap_b32_e32 v7, v36
	v_max_f32_e32 v24, v36, v36
	v_max_f32_e32 v7, v7, v24
	v_mov_b32_e32 v24, v7
	s_nop 1
	v_permlane32_swap_b32_e32 v7, v24
	v_max_f32_e32 v24, v24, v24
	v_max_f32_e32 v7, v7, v7
	v_max_f32_e32 v7, v7, v24
	v_mul_f32_e32 v24, 0x3c010204, v7
	v_cmp_lt_f32_e32 vcc, 0, v7
	s_nop 1
	v_cndmask_b32_e32 v7, 1.0, v24, vcc
	v_div_scale_f32 v24, s[2:3], v7, v7, 1.0
	v_rcp_f32_e32 v25, v24
	v_div_scale_f32 v26, vcc, 1.0, v7, 1.0
	v_fma_f32 v27, -v24, v25, 1.0
	v_fmac_f32_e32 v25, v27, v25
	v_mul_f32_e32 v27, v26, v25
	v_fma_f32 v28, -v24, v27, v26
	v_fmac_f32_e32 v27, v28, v25
	v_fma_f32 v24, -v24, v27, v26
	v_div_fmas_f32 v24, v24, v25, v27
	v_div_fixup_f32 v24, v24, v7, 1.0
	v_fmaak_f32 v8, v8, v24, 0x4b400000
	v_fmaak_f32 v9, v9, v24, 0x4b400000
	v_fmaak_f32 v10, v10, v24, 0x4b400000
	v_fmaak_f32 v11, v11, v24, 0x4b400000
	v_fmaak_f32 v12, v12, v24, 0x4b400000
	v_fmaak_f32 v13, v13, v24, 0x4b400000
	v_fmaak_f32 v14, v14, v24, 0x4b400000
	v_fmaak_f32 v15, v15, v24, 0x4b400000
	v_fmaak_f32 v16, v16, v24, 0x4b400000
	v_fmaak_f32 v17, v17, v24, 0x4b400000
	v_fmaak_f32 v18, v18, v24, 0x4b400000
	v_fmaak_f32 v19, v19, v24, 0x4b400000
	v_fmaak_f32 v20, v20, v24, 0x4b400000
	v_fmaak_f32 v21, v21, v24, 0x4b400000
	v_fmaak_f32 v22, v22, v24, 0x4b400000
	v_fmaak_f32 v23, v23, v24, 0x4b400000
	v_perm_b32 v10, v11, v10, s15
	v_perm_b32 v8, v9, v8, s15
	v_perm_b32 v9, v15, v14, s15
	v_perm_b32 v11, v13, v12, s15
	v_perm_b32 v12, v19, v18, s15
	v_perm_b32 v13, v17, v16, s15
	v_perm_b32 v14, v23, v22, s15
	v_perm_b32 v15, v21, v20, s15
	v_perm_b32 v8, v10, v8, s16
	v_perm_b32 v9, v9, v11, s16
	v_perm_b32 v10, v12, v13, s16
	v_perm_b32 v11, v14, v15, s16
	global_store_dwordx2 v[34:35], v[8:9], off
	global_store_dwordx2 v[34:35], v[10:11], off offset:512
	s_and_saveexec_b64 s[2:3], s[0:1]
	s_cbranch_execz .LBB0_31
	s_add_u32 s20, s84, s12
	s_addc_u32 s21, s85, s13
	global_store_dword v6, v7, s[20:21]
	s_branch .LBB0_31

; #define LAS __attribute__((address_space(3)))
; __device__ __forceinline__ unsigned cvt_pk_bf16(float lo, float hi) { const f32x2_t v = {lo, hi}; const bf16x2_t b = __builtin_convertvector(v, bf16x2_t); return __builtin_bit_cast(unsigned, b); }
; template <int O> __device__ __forceinline__ float xor_sw(float v) { return __int_as_float(__builtin_amdgcn_ds_swizzle(__float_as_int(v), 0x1f | (O << 10))); }
; __device__ __forceinline__ float sum_x32(float v) { const auto r = __builtin_amdgcn_permlane32_swap(__float_as_uint(v), __float_as_uint(v), false, false); return __uint_as_float(r[0]) + __uint_as_float(r[1]); }
; __global__ void __launch_bounds__(NWAVES * 64, 2) mk_fwd(Args args) {
;     ...
;                             for (int sl = 0; sl < 2; ++sl) { const int pp = 32 * wave + 16 * sl + c, sw = (2 * wave + sl) & 15;
;                                 float lt = l[sl]; lt += xor_sw<16>(lt); lt = sum_x32(lt);
;                                 const float mc = PARK[pp * 68 + 64], lc = PARK[pp * 68 + 65];
;                                 const float mn = fmaxf(m[sl], mc), fa = __builtin_amdgcn_exp2f(m[sl] - mn), fb = __builtin_amdgcn_exp2f(mc - mn);
;                                 const float inv = 1.0f / (lt * fa + lc * fb);
;                                 bf16_t* orow = CAT + (size_t)(b * SEQ + 256 * ib + pp) * D + h * 64;
; #pragma unroll
;                                 for (int mt = 0; mt < 4; ++mt) { const f32x4 oc = *(const LAS f32x4*)(PARK + pp * 68 + 4 * ((4 * mt + g) ^ sw)); const f32x4 v = (O[sl][mt] * fa + oc * fb) * inv;
;                                     u32x2 w; w.x = cvt_pk_bf16(v[0], v[1]); w.y = cvt_pk_bf16(v[2], v[3]); *(u32x2*)(orow + 16 * mt + 4 * g) = w; } }
.LBB0_229:
	v_readlane_b32 s8, v253, 18
	v_lshlrev_b32_e32 v16, 2, v192
	v_ashrrev_i32_e32 v17, 31, v16
	s_waitcnt vmcnt(1)
	v_add_u32_e32 v22, s8, v193
	s_lshl_b32 s8, s28, 11
	s_or_b32 s10, s8, s29
	s_add_u32 s8, s80, s68
	s_waitcnt lgkmcnt(0)
	v_mov_b32_e32 v18, v91
	s_nop 1
	v_permlane16_swap_b32_e32 v91, v18
	v_add_f32_e32 v18, v91, v18
	s_addc_u32 s9, s81, 0
	v_mov_b32_e32 v19, v18
	v_lshl_add_u64 v[16:17], v[16:17], 1, s[8:9]
	s_nop 0
	v_permlane32_swap_b32_e32 v18, v19
	s_movk_i32 s8, 0x110
	v_add_f32_e32 v18, v18, v19
	v_mul_lo_u32 v19, v22, s8
	s_waitcnt vmcnt(0)
	v_add_u32_e32 v27, 0, v19
	ds_read_b64 v[20:21], v27 offset:256
	v_max_f32_e32 v23, v101, v101
	s_waitcnt lgkmcnt(0)
	v_max_f32_e32 v19, v20, v20
	v_max_f32_e32 v19, v23, v19
	v_sub_f32_e32 v23, v101, v19
	v_sub_f32_e32 v19, v20, v19
	v_exp_f32_e32 v24, v23
	v_exp_f32_e32 v25, v19
	v_mov_b32_e32 v19, v21
	v_pk_mul_f32 v[18:19], v[18:19], v[24:25]
	s_nop 0
	v_add_f32_e32 v18, v18, v19
	v_div_scale_f32 v19, s[8:9], v18, v18, 1.0
	v_rcp_f32_e32 v20, v19
	v_readlane_b32 s8, v253, 62
	v_pk_mul_f32 v[30:31], v[24:25], v[56:57] op_sel_hi:[0,1]
	v_pk_mul_f32 v[34:35], v[24:25], v[54:55] op_sel_hi:[0,1]
	v_fma_f32 v21, -v19, v20, 1.0
	v_fmac_f32_e32 v20, v21, v20
	v_div_scale_f32 v21, vcc, 1.0, v18, 1.0
	v_mul_f32_e32 v23, v21, v20
	v_fma_f32 v26, -v19, v23, v21
	v_fmac_f32_e32 v23, v26, v20
	v_fma_f32 v19, -v19, v23, v21
	v_div_fmas_f32 v19, v19, v20, v23
	v_div_fixup_f32 v26, v19, v18, 1.0
	v_add_u32_e32 v18, s10, v22
	v_ashrrev_i32_e32 v19, 31, v18
	v_lshlrev_b64 v[20:21], 11, v[18:19]
	v_xor_b32_e32 v19, s8, v192
	v_lshl_add_u32 v19, v19, 4, v27
	v_lshl_add_u64 v[28:29], v[16:17], 0, v[20:21]
	ds_read_b128 v[20:23], v19
	v_mov_b32_e32 v32, v25
	v_xor_b32_e32 v19, s8, v98
	v_lshl_add_u32 v19, v19, 4, v27
	s_waitcnt lgkmcnt(0)
	v_pk_fma_f32 v[20:21], v[32:33], v[20:21], v[34:35] op_sel_hi:[0,1,1]
	v_pk_fma_f32 v[22:23], v[32:33], v[22:23], v[30:31] op_sel_hi:[0,1,1]
	v_pk_mul_f32 v[22:23], v[26:27], v[22:23] op_sel_hi:[0,1]
	v_pk_mul_f32 v[20:21], v[26:27], v[20:21] op_sel_hi:[0,1]
	v_cvt_pk_bf16_f32 v20, v20, v21
	v_cvt_pk_bf16_f32 v21, v22, v23
	global_store_dwordx2 v[28:29], v[20:21], off
	ds_read_b128 v[20:23], v19
	v_pk_mul_f32 v[30:31], v[24:25], v[52:53] op_sel_hi:[0,1]
	v_pk_mul_f32 v[34:35], v[24:25], v[50:51] op_sel_hi:[0,1]
	v_xor_b32_e32 v19, s8, v97
	v_lshl_add_u32 v19, v19, 4, v27
	s_waitcnt lgkmcnt(0)
	v_pk_fma_f32 v[20:21], v[32:33], v[20:21], v[34:35] op_sel_hi:[0,1,1]
	v_pk_fma_f32 v[22:23], v[32:33], v[22:23], v[30:31] op_sel_hi:[0,1,1]
	v_pk_mul_f32 v[22:23], v[26:27], v[22:23] op_sel_hi:[0,1]
	v_pk_mul_f32 v[20:21], v[26:27], v[20:21] op_sel_hi:[0,1]
	v_cvt_pk_bf16_f32 v20, v20, v21
	v_cvt_pk_bf16_f32 v21, v22, v23
	global_store_dwordx2 v[28:29], v[20:21], off offset:32
	ds_read_b128 v[20:23], v19
	v_pk_mul_f32 v[30:31], v[24:25], v[48:49] op_sel_hi:[0,1]
	v_pk_mul_f32 v[34:35], v[24:25], v[46:47] op_sel_hi:[0,1]
	v_xor_b32_e32 v19, s8, v96
	v_lshl_add_u32 v19, v19, 4, v27
	s_waitcnt lgkmcnt(0)
	v_pk_fma_f32 v[20:21], v[32:33], v[20:21], v[34:35] op_sel_hi:[0,1,1]
	v_pk_fma_f32 v[22:23], v[32:33], v[22:23], v[30:31] op_sel_hi:[0,1,1]
	v_pk_mul_f32 v[22:23], v[26:27], v[22:23] op_sel_hi:[0,1]
	v_pk_mul_f32 v[20:21], v[26:27], v[20:21] op_sel_hi:[0,1]
	v_cvt_pk_bf16_f32 v20, v20, v21
	v_cvt_pk_bf16_f32 v21, v22, v23
	global_store_dwordx2 v[28:29], v[20:21], off offset:64
	ds_read_b128 v[20:23], v19
	v_pk_mul_f32 v[30:31], v[24:25], v[44:45] op_sel_hi:[0,1]
	v_pk_mul_f32 v[24:25], v[24:25], v[42:43] op_sel_hi:[0,1]
	s_waitcnt lgkmcnt(0)
; #define LAS __attribute__((address_space(3)))
; __device__ __forceinline__ unsigned cvt_pk_bf16(float lo, float hi) { const f32x2_t v = {lo, hi}; const bf16x2_t b = __builtin_convertvector(v, bf16x2_t); return __builtin_bit_cast(unsigned, b); }
; template <int O> __device__ __forceinline__ float xor_sw(float v) { return __int_as_float(__builtin_amdgcn_ds_swizzle(__float_as_int(v), 0x1f | (O << 10))); }
; __device__ __forceinline__ float sum_x32(float v) { const auto r = __builtin_amdgcn_permlane32_swap(__float_as_uint(v), __float_as_uint(v), false, false); return __uint_as_float(r[0]) + __uint_as_float(r[1]); }
; __global__ void __launch_bounds__(NWAVES * 64, 2) mk_fwd(Args args) {
;     ...
;                             for (int sl = 0; sl < 2; ++sl) { const int pp = 32 * wave + 16 * sl + c, sw = (2 * wave + sl) & 15;
;                                 float lt = l[sl]; lt += xor_sw<16>(lt); lt = sum_x32(lt);
;                                 const float mc = PARK[pp * 68 + 64], lc = PARK[pp * 68 + 65];
;                                 const float mn = fmaxf(m[sl], mc), fa = __builtin_amdgcn_exp2f(m[sl] - mn), fb = __builtin_amdgcn_exp2f(mc - mn);
;                                 const float inv = 1.0f / (lt * fa + lc * fb);
;                                 bf16_t* orow = CAT + (size_t)(b * SEQ + 256 * ib + pp) * D + h * 64;
; #pragma unroll
;                                 for (int mt = 0; mt < 4; ++mt) { const f32x4 oc = *(const LAS f32x4*)(PARK + pp * 68 + 4 * ((4 * mt + g) ^ sw)); const f32x4 v = (O[sl][mt] * fa + oc * fb) * inv;
;                                     u32x2 w; w.x = cvt_pk_bf16(v[0], v[1]); w.y = cvt_pk_bf16(v[2], v[3]); *(u32x2*)(orow + 16 * mt + 4 * g) = w; } }
	v_pk_fma_f32 v[20:21], v[32:33], v[20:21], v[24:25] op_sel_hi:[0,1,1]
	v_pk_fma_f32 v[22:23], v[32:33], v[22:23], v[30:31] op_sel_hi:[0,1,1]
	v_pk_mul_f32 v[22:23], v[26:27], v[22:23] op_sel_hi:[0,1]
	v_pk_mul_f32 v[20:21], v[26:27], v[20:21] op_sel_hi:[0,1]
	v_cvt_pk_bf16_f32 v20, v20, v21
	v_cvt_pk_bf16_f32 v21, v22, v23
	ds_read_b64 v[22:23], v27 offset:4608
	global_store_dwordx2 v[28:29], v[20:21], off offset:96
	v_max_f32_e32 v24, v99, v99
	s_waitcnt lgkmcnt(1)
	v_mov_b32_e32 v19, v90
	s_nop 1
	v_permlane16_swap_b32_e32 v90, v19
	v_add_f32_e32 v19, v90, v19
	v_mov_b32_e32 v20, v19
	s_waitcnt lgkmcnt(0)
	v_max_f32_e32 v21, v22, v22
	v_max_f32_e32 v21, v24, v21
	v_sub_f32_e32 v24, v99, v21
	v_sub_f32_e32 v21, v22, v21
	v_exp_f32_e32 v24, v24
	v_exp_f32_e32 v25, v21
	v_permlane32_swap_b32_e32 v19, v20
	v_add_f32_e32 v20, v19, v20
	v_mov_b32_e32 v21, v23
	v_pk_mul_f32 v[20:21], v[20:21], v[24:25]
	v_add_u32_e32 v19, 0x1100, v27
	v_add_f32_e32 v20, v20, v21
	v_div_scale_f32 v21, s[8:9], v20, v20, 1.0
	v_rcp_f32_e32 v22, v21
	v_readlane_b32 s8, v253, 63
	v_pk_mul_f32 v[14:15], v[24:25], v[14:15] op_sel_hi:[0,1]
	v_pk_mul_f32 v[12:13], v[24:25], v[12:13] op_sel_hi:[0,1]
	v_fma_f32 v23, -v21, v22, 1.0
	v_fmac_f32_e32 v22, v23, v22
	v_div_scale_f32 v23, vcc, 1.0, v20, 1.0
	v_mul_f32_e32 v26, v23, v22
	v_fma_f32 v27, -v21, v26, v23
	v_fmac_f32_e32 v26, v27, v22
	v_fma_f32 v21, -v21, v26, v23
	v_div_fmas_f32 v21, v21, v22, v26
	v_div_fixup_f32 v26, v21, v20, 1.0
	v_add_u32_e32 v20, 16, v18
	v_ashrrev_i32_e32 v21, 31, v20
	v_xor_b32_e32 v18, s8, v192
	v_lshlrev_b64 v[20:21], 11, v[20:21]
	v_lshl_add_u32 v18, v18, 4, v19
	v_lshl_add_u64 v[16:17], v[16:17], 0, v[20:21]
	ds_read_b128 v[20:23], v18
	v_mov_b32_e32 v18, v25
	v_pk_mul_f32 v[10:11], v[24:25], v[10:11] op_sel_hi:[0,1]
	v_pk_mul_f32 v[8:9], v[24:25], v[8:9] op_sel_hi:[0,1]
	v_pk_mul_f32 v[6:7], v[24:25], v[6:7] op_sel_hi:[0,1]
	s_waitcnt lgkmcnt(0)
	v_pk_fma_f32 v[12:13], v[18:19], v[20:21], v[12:13] op_sel_hi:[0,1,1]
	v_pk_fma_f32 v[14:15], v[18:19], v[22:23], v[14:15] op_sel_hi:[0,1,1]
	v_pk_mul_f32 v[14:15], v[26:27], v[14:15] op_sel_hi:[0,1]
	v_pk_mul_f32 v[12:13], v[26:27], v[12:13] op_sel_hi:[0,1]
	v_cvt_pk_bf16_f32 v12, v12, v13
	v_cvt_pk_bf16_f32 v13, v14, v15
	global_store_dwordx2 v[16:17], v[12:13], off
	v_xor_b32_e32 v12, s8, v98
	v_lshl_add_u32 v12, v12, 4, v19
	ds_read_b128 v[12:15], v12
	v_pk_mul_f32 v[4:5], v[24:25], v[4:5] op_sel_hi:[0,1]
	v_pk_mul_f32 v[2:3], v[24:25], v[2:3] op_sel_hi:[0,1]
	v_pk_mul_f32 v[0:1], v[24:25], v[0:1] op_sel_hi:[0,1]
	s_waitcnt lgkmcnt(0)
	v_pk_fma_f32 v[8:9], v[18:19], v[12:13], v[8:9] op_sel_hi:[0,1,1]
	v_pk_fma_f32 v[10:11], v[18:19], v[14:15], v[10:11] op_sel_hi:[0,1,1]
	v_pk_mul_f32 v[10:11], v[26:27], v[10:11] op_sel_hi:[0,1]
	v_pk_mul_f32 v[8:9], v[26:27], v[8:9] op_sel_hi:[0,1]
	v_cvt_pk_bf16_f32 v8, v8, v9
	v_cvt_pk_bf16_f32 v9, v10, v11
	global_store_dwordx2 v[16:17], v[8:9], off offset:32
	v_xor_b32_e32 v8, s8, v97
	v_lshl_add_u32 v8, v8, 4, v19
	ds_read_b128 v[8:11], v8
	s_waitcnt lgkmcnt(0)
	v_pk_fma_f32 v[4:5], v[18:19], v[8:9], v[4:5] op_sel_hi:[0,1,1]
	v_pk_fma_f32 v[6:7], v[18:19], v[10:11], v[6:7] op_sel_hi:[0,1,1]
	v_pk_mul_f32 v[6:7], v[26:27], v[6:7] op_sel_hi:[0,1]
	v_pk_mul_f32 v[4:5], v[26:27], v[4:5] op_sel_hi:[0,1]
	v_cvt_pk_bf16_f32 v4, v4, v5
	v_cvt_pk_bf16_f32 v5, v6, v7
	global_store_dwordx2 v[16:17], v[4:5], off offset:64
	v_xor_b32_e32 v4, s8, v96
	v_lshl_add_u32 v4, v4, 4, v19
	ds_read_b128 v[4:7], v4
	s_waitcnt lgkmcnt(0)
	v_pk_fma_f32 v[0:1], v[18:19], v[4:5], v[0:1] op_sel_hi:[0,1,1]
	v_pk_fma_f32 v[2:3], v[18:19], v[6:7], v[2:3] op_sel_hi:[0,1,1]
	v_pk_mul_f32 v[2:3], v[26:27], v[2:3] op_sel_hi:[0,1]
	v_pk_mul_f32 v[0:1], v[26:27], v[0:1] op_sel_hi:[0,1]
	v_cvt_pk_bf16_f32 v0, v0, v1
	v_cvt_pk_bf16_f32 v1, v2, v3
	global_store_dwordx2 v[16:17], v[0:1], off offset:96
	s_barrier

; #define LAS __attribute__((address_space(3)))
; template <int NH, class InitF>
; __device__ __forceinline__ void attn_core64(const LAS unsigned char* kbuf  , const LAS unsigned char* vbuf  , const InitF& initf  ,
;                                             const bf16x8 (&bq)[NH][2], float (&m)[NH], float (&l)[NH], f32x4 (&O)[NH][4], int lane) {
;     ...
;         f32x4 sa[4];
; #pragma unroll
;         for (int t = 0; t < 4; ++t) sa[t] = initf(hq, t);
; #pragma unroll
;         for (int t = 0; t < 4; ++t) { const bf16x8 k0 = *(const LAS bf16x8*)(kbuf + (16 * t + c) * 144 + 16 * g), k1 = *(const LAS bf16x8*)(kbuf + (16 * t + c) * 144 + 16 * g + 64);
;             sa[t] = __builtin_amdgcn_mfma_f32_16x16x32_bf16(k0, bq[hq][0], sa[t], 0, 0, 0); sa[t] = __builtin_amdgcn_mfma_f32_16x16x32_bf16(k1, bq[hq][1], sa[t], 0, 0, 0); }
; template <int NH, int NQ, bool TABLE> ...
;     ...
;         if (j >= jlo && j <= jhi && !(kb + 63 < 0 || kb >= SEQ)) {
;             if constexpr (TABLE) {
;                 const LAS unsigned char* bp[NQ];
; #pragma unroll
;                 for (int q = 0; q < NQ; ++q) bp[q] = tab[q] + 4 * kb;
;                 auto initf = [&](int hq, int t) { return *(const LAS f32x4*)(bp[hq] + 64 * t); };
;                 attn_core64<NH>(buf + SH_K, buf + SH_V, initf, bq, m, l, O, lane);
;             } else {
;                 const float fb = (float)(kb + iq[0]);
;                 if (__builtin_amdgcn_ballot_w64(!(fabsf(fb) <= flim && fabsf(fb + 51.f) <= flim)) == 0ull) {
;                     auto initf = [&](int hq, int t) { f32x4 v;
; #pragma unroll
;                         for (int r = 0; r < 4; ++r) v[r] = -slope2[hq] * fabsf(fb + (float)(16 * t + r));
;                         return v; };
;                     attn_core64<NH>(buf + SH_K, buf + SH_V, initf, bq, m, l, O, lane);
;                 } else {
;                     auto initf = [&](int hq, int t) { f32x4 v;
; #pragma unroll
;                         for (int r = 0; r < 4; ++r) { const float ad = fabsf(fb + (float)(16 * t + r)); v[r] = __builtin_fmaf(-slope2[hq], ad, (ad <= flim) ? 0.f : -3.0e38f); }
;                         return v; };
;                     attn_core64<NH>(buf + SH_K, buf + SH_V, initf, bq, m, l, O, lane);
.LBB0_246:
	s_add_i32 s8, s13, 0xfffff780
	s_cmp_lt_u32 s8, 0xfffff7c1
	s_cbranch_scc1 .LBB0_245
	v_add_u32_e32 v32, s13, v199
	v_cvt_f32_i32_e32 v32, v32
	s_bitcmp1_b32 s15, 0
	s_cselect_b32 s8, 0x4c00, 0
	s_add_i32 s16, s8, 0
	s_add_i32 s16, s16, 0x14000
	v_add_f32_e32 v62, 0x424c0000, v32
	v_cmp_nle_f32_e64 s[8:9], |v32|, s49
	v_cmp_nle_f32_e64 s[18:19], |v62|, s49
	v_add_u32_e32 v59, s16, v126
	v_add_f32_e32 v58, 1.0, v32
	v_add_f32_e32 v63, 0x42480000, v32
	s_or_b64 vcc, s[8:9], s[18:19]
	v_add_u32_e32 v202, v59, v161
	v_and_b32_e32 v146, 0x7fffffff, v32
	v_and_b32_e32 v145, 0x7fffffff, v62
	v_and_b32_e32 v147, 0x7fffffff, v58
	v_and_b32_e32 v144, 0x7fffffff, v63
	s_cbranch_vccz .LBB0_253
	s_mov_b32 s8, 2.0
	s_mov_b32 s9, 0x40400000
	v_pk_add_f32 v[60:61], v[32:33], s[8:9] op_sel_hi:[0,1]
	s_mov_b32 s8, 0x41900000
	s_mov_b32 s9, 0x41980000
	v_pk_add_f32 v[90:91], v[32:33], s[8:9] op_sel_hi:[0,1]
	s_mov_b32 s8, 0x42000000
	s_mov_b32 s9, 0x42040000
	v_pk_add_f32 v[92:93], v[32:33], s[8:9] op_sel_hi:[0,1]
	s_mov_b32 s8, 0x42080000
	s_mov_b32 s9, 0x420c0000
	v_pk_add_f32 v[98:99], v[32:33], s[8:9] op_sel_hi:[0,1]
	s_mov_b32 s8, 0x42400000
	s_mov_b32 s9, 0x42440000
	v_pk_add_f32 v[102:103], v[32:33], s[8:9] op_sel_hi:[0,1]
	v_cmp_le_f32_e64 s[8:9], |v32|, s49
	v_pk_add_f32 v[88:89], v[32:33], s[46:47] op_sel_hi:[0,1]
	ds_read_b128 v[64:67], v202
	ds_read_b128 v[68:71], v202 offset:64
	v_cndmask_b32_e64 v106, v222, 0, s[8:9]
	v_cmp_le_f32_e64 s[8:9], |v58|, s49
	v_and_b32_e32 v109, 0x7fffffff, v61
	v_and_b32_e32 v108, 0x7fffffff, v60
	v_cndmask_b32_e64 v107, v222, 0, s[8:9]
	v_cmp_le_f32_e64 s[8:9], |v61|, s49
	v_mov_b32_e32 v137, v136
	v_pk_fma_f32 v[58:59], v[138:139], v[146:147], v[106:107]
	v_cndmask_b32_e64 v111, v222, 0, s[8:9]
	v_cmp_le_f32_e64 s[8:9], |v60|, s49
	ds_read_b128 v[72:75], v202 offset:2304
	ds_read_b128 v[76:79], v202 offset:2368
	ds_read_b128 v[80:83], v202 offset:4608
	ds_read_b128 v[84:87], v202 offset:4672
	v_cndmask_b32_e64 v110, v222, 0, s[8:9]
	v_cmp_le_f32_e64 s[8:9], |v89|, s49
	v_pk_fma_f32 v[60:61], v[136:137], v[108:109], v[110:111]
	v_and_b32_e32 v113, 0x7fffffff, v89
	v_cndmask_b32_e64 v149, v222, 0, s[8:9]
	v_cmp_le_f32_e64 s[8:9], |v88|, s49
	v_and_b32_e32 v112, 0x7fffffff, v88
	v_and_b32_e32 v209, 0x7fffffff, v91
	v_cndmask_b32_e64 v148, v222, 0, s[8:9]
	v_cmp_le_f32_e64 s[8:9], |v91|, s49
	v_and_b32_e32 v208, 0x7fffffff, v90
	s_waitcnt lgkmcnt(5)
	v_mfma_f32_16x16x32_bf16 v[58:61], v[64:67], v[24:27], v[58:61]
	v_cndmask_b32_e64 v211, v222, 0, s[8:9]
	v_cmp_le_f32_e64 s[8:9], |v90|, s49
	v_pk_fma_f32 v[88:89], v[138:139], v[112:113], v[148:149]
	v_and_b32_e32 v213, 0x7fffffff, v93
	v_cndmask_b32_e64 v210, v222, 0, s[8:9]
	v_pk_fma_f32 v[90:91], v[136:137], v[208:209], v[210:211]
	v_cmp_le_f32_e64 s[8:9], |v93|, s49
	v_and_b32_e32 v212, 0x7fffffff, v92
	s_waitcnt lgkmcnt(3)
	v_mfma_f32_16x16x32_bf16 v[88:91], v[72:75], v[24:27], v[88:91]
	v_cndmask_b32_e64 v93, v222, 0, s[8:9]
	v_cmp_le_f32_e64 s[8:9], |v92|, s49
	v_and_b32_e32 v215, 0x7fffffff, v99
	v_mfma_f32_16x16x32_bf16 v[58:61], v[68:71], v[28:31], v[58:61]
	v_cndmask_b32_e64 v92, v222, 0, s[8:9]
	v_cmp_le_f32_e64 s[8:9], |v99|, s49
	v_and_b32_e32 v214, 0x7fffffff, v98
	s_waitcnt lgkmcnt(2)
	v_mfma_f32_16x16x32_bf16 v[94:97], v[76:79], v[28:31], v[88:91]
	v_cndmask_b32_e64 v217, v222, 0, s[8:9]
	v_cmp_le_f32_e64 s[8:9], |v98|, s49
	ds_read_b128 v[114:117], v202 offset:6912
	ds_read_b128 v[204:207], v202 offset:6976
	v_cndmask_b32_e64 v216, v222, 0, s[8:9]
	v_pk_fma_f32 v[90:91], v[136:137], v[214:215], v[216:217]
	v_pk_fma_f32 v[88:89], v[138:139], v[212:213], v[92:93]
	v_cmp_le_f32_e64 s[8:9], |v103|, s49
	v_max_f32_e32 v100, v61, v61
	s_waitcnt lgkmcnt(3)
	v_mfma_f32_16x16x32_bf16 v[88:91], v[80:83], v[24:27], v[88:91]
	v_cndmask_b32_e64 v227, v222, 0, s[8:9]
	v_cmp_le_f32_e64 s[8:9], |v102|, s49
	v_max_f32_e32 v98, v60, v60
	v_max_f32_e32 v98, v98, v100
	v_cndmask_b32_e64 v226, v222, 0, s[8:9]
	v_cmp_le_f32_e64 s[8:9], |v62|, s49
	v_and_b32_e32 v219, 0x7fffffff, v103
	v_and_b32_e32 v218, 0x7fffffff, v102
	v_cndmask_b32_e64 v229, v222, 0, s[8:9]
	v_cmp_le_f32_e64 s[8:9], |v63|, s49
	v_max3_f32 v118, v58, v59, v98
	s_waitcnt lgkmcnt(2)
; #define LAS __attribute__((address_space(3)))
; __device__ __forceinline__ unsigned cvt_pk_bf16(float lo, float hi) { const f32x2_t v = {lo, hi}; const bf16x2_t b = __builtin_convertvector(v, bf16x2_t); return __builtin_bit_cast(unsigned, b); }
; template <int O> __device__ __forceinline__ float xor_sw(float v) { return __int_as_float(__builtin_amdgcn_ds_swizzle(__float_as_int(v), 0x1f | (O << 10))); }
; template <int NH, class InitF>
; __device__ __forceinline__ void attn_core64(const LAS unsigned char* kbuf  , const LAS unsigned char* vbuf  , const InitF& initf  ,
;                                             const bf16x8 (&bq)[NH][2], float (&m)[NH], float (&l)[NH], f32x4 (&O)[NH][4], int lane) {
;     ...
;     for (int hq = 0; hq < NH; ++hq) {
;         f32x4 sa[4];
; #pragma unroll
;         for (int t = 0; t < 4; ++t) sa[t] = initf(hq, t);
; #pragma unroll
;         for (int t = 0; t < 4; ++t) { const bf16x8 k0 = *(const LAS bf16x8*)(kbuf + (16 * t + c) * 144 + 16 * g), k1 = *(const LAS bf16x8*)(kbuf + (16 * t + c) * 144 + 16 * g + 64);
;             sa[t] = __builtin_amdgcn_mfma_f32_16x16x32_bf16(k0, bq[hq][0], sa[t], 0, 0, 0); sa[t] = __builtin_amdgcn_mfma_f32_16x16x32_bf16(k1, bq[hq][1], sa[t], 0, 0, 0); }
;         float mx = -3.0e38f;
; #pragma unroll
;         for (int t = 0; t < 4; ++t) mx = fmaxf(mx, fmaxf(fmaxf(sa[t][0], sa[t][1]), fmaxf(sa[t][2], sa[t][3])));
;         mx = fmaxf(mx, xor_sw<16>(mx)); mx = max_x32(mx);
;         const float mn = fmaxf(m[hq], mx); corr[hq] = __builtin_amdgcn_exp2f(m[hq] - mn); m[hq] = mn;
;         float p[16], ps = 0.f;
; #pragma unroll
;         for (int i = 0; i < 16; ++i) { p[i] = __builtin_amdgcn_exp2f(sa[i >> 2][i & 3] - mn); ps += p[i]; }
;         l[hq] = l[hq] * corr[hq] + ps;
;         u32x4 pw0, pw1;
;         pw0.x = cvt_pk_bf16(p[0], p[1]); pw0.y = cvt_pk_bf16(p[2], p[3]); pw0.z = cvt_pk_bf16(p[4], p[5]); pw0.w = cvt_pk_bf16(p[6], p[7]);
;         pw1.x = cvt_pk_bf16(p[8], p[9]); pw1.y = cvt_pk_bf16(p[10], p[11]); pw1.z = cvt_pk_bf16(p[12], p[13]); pw1.w = cvt_pk_bf16(p[14], p[15]);
;         pb[hq][0] = __builtin_bit_cast(bf16x8, pw0); pb[hq][1] = __builtin_bit_cast(bf16x8, pw1);
;     }
; #pragma unroll
;     for (int hq = 0; hq < NH; ++hq) {
;         if (__builtin_amdgcn_ballot_w64(corr[hq] != 1.0f) != 0ull) {
; #pragma unroll
;             for (int mt = 0; mt < 4; ++mt) O[hq][mt] *= corr[hq]; } }
	v_mfma_f32_16x16x32_bf16 v[98:101], v[84:87], v[28:31], v[88:91]
	v_cndmask_b32_e64 v228, v222, 0, s[8:9]
	v_mov_b32_e32 v135, v134
	v_max_f32_e32 v62, v97, v97
	v_pk_fma_f32 v[88:89], v[138:139], v[218:219], v[226:227]
	v_pk_fma_f32 v[90:91], v[136:137], v[144:145], v[228:229]
	v_max_f32_e32 v63, v96, v96
	v_max_f32_e32 v119, v63, v62
	s_waitcnt lgkmcnt(1)
	v_mfma_f32_16x16x32_bf16 v[88:91], v[114:117], v[24:27], v[88:91]
	s_waitcnt lgkmcnt(0)
	v_mfma_f32_16x16x32_bf16 v[102:105], v[204:207], v[28:31], v[88:91]
	s_nop 5
	v_fma_f32 v90, v134, v108, v110
	v_fma_f32 v91, v135, v109, v111
	v_pk_fma_f32 v[88:89], v[140:141], v[146:147], v[106:107]
	s_nop 1
	v_mfma_f32_16x16x32_bf16 v[62:65], v[64:67], v[34:37], v[88:91]
	v_max3_f32 v66, v94, v95, v119
	v_max3_f32 v66, v118, s96, v66
	v_max_f32_e32 v67, v101, v101
	v_mfma_f32_16x16x32_bf16 v[118:121], v[68:71], v[38:41], v[62:65]
	v_max_f32_e32 v68, v100, v100
	v_max_f32_e32 v67, v68, v67
	v_max_f32_e32 v68, v105, v105
	s_nop 0
	v_pk_fma_f32 v[64:65], v[134:135], v[208:209], v[210:211]
	v_pk_fma_f32 v[62:63], v[140:141], v[112:113], v[148:149]
	v_max_f32_e32 v69, v104, v104
	v_max_f32_e32 v68, v69, v68
	v_mfma_f32_16x16x32_bf16 v[62:65], v[72:75], v[34:37], v[62:65]
	v_max3_f32 v67, v98, v99, v67
	v_max3_f32 v68, v102, v103, v68
	v_max3_f32 v66, v66, v67, v68
	v_mfma_f32_16x16x32_bf16 v[106:109], v[76:79], v[38:41], v[62:65]
	v_mov_b64_e32 v[72:73], v[52:53]
	v_mov_b64_e32 v[76:77], v[56:57]
	s_nop 0
	v_pk_fma_f32 v[64:65], v[134:135], v[214:215], v[216:217]
	v_pk_fma_f32 v[62:63], v[140:141], v[212:213], v[92:93]
	s_waitcnt lgkmcnt(0)
	v_mov_b32_e32 v67, v66
	s_nop 1
	v_permlane16_swap_b32_e32 v66, v67
	v_max_f32_e32 v67, v67, v67
	v_max_f32_e32 v66, v66, v67
	v_mfma_f32_16x16x32_bf16 v[62:65], v[80:83], v[34:37], v[62:65]
	v_mov_b32_e32 v67, v66
	s_nop 1
	v_permlane32_swap_b32_e32 v66, v67
	v_mfma_f32_16x16x32_bf16 v[110:113], v[84:87], v[38:41], v[62:65]
	v_mov_b64_e32 v[70:71], v[50:51]
	v_mov_b64_e32 v[74:75], v[54:55]
	s_nop 0
	v_pk_fma_f32 v[62:63], v[140:141], v[218:219], v[226:227]
	v_pk_fma_f32 v[64:65], v[134:135], v[144:145], v[228:229]
	v_max3_f32 v135, v201, v66, v67
	v_mov_b64_e32 v[68:69], v[48:49]
	v_mfma_f32_16x16x32_bf16 v[62:65], v[114:117], v[34:37], v[62:65]
	v_mov_b64_e32 v[66:67], v[46:47]
	v_mfma_f32_16x16x32_bf16 v[114:117], v[204:207], v[38:41], v[62:65]
	s_nop 5
	v_max_f32_e32 v62, v121, v121
	v_max_f32_e32 v63, v120, v120
	v_max_f32_e32 v62, v63, v62
	v_max_f32_e32 v63, v109, v109
	v_max_f32_e32 v64, v108, v108
	v_max_f32_e32 v63, v64, v63
	v_max3_f32 v62, v118, v119, v62
	v_max3_f32 v63, v106, v107, v63
	v_max3_f32 v62, v62, s96, v63
	v_max_f32_e32 v63, v113, v113
	v_max_f32_e32 v64, v112, v112
	v_max_f32_e32 v63, v64, v63
	v_max_f32_e32 v64, v117, v117
	v_max_f32_e32 v65, v116, v116
	v_max_f32_e32 v64, v65, v64
	v_max3_f32 v63, v110, v111, v63
	v_max3_f32 v64, v114, v115, v64
	v_max3_f32 v62, v62, v63, v64
	v_sub_f32_e32 v64, v201, v135
	v_exp_f32_e32 v149, v64
	s_waitcnt lgkmcnt(0)
	v_mov_b32_e32 v63, v62
	s_nop 1
	v_permlane16_swap_b32_e32 v62, v63
	v_max_f32_e32 v63, v63, v63
	v_max_f32_e32 v78, v62, v63
	v_mov_b32_e32 v79, v78
	v_mov_b64_e32 v[64:65], v[44:45]
	s_nop 0
	v_permlane32_swap_b32_e32 v78, v79
	v_cmp_neq_f32_e32 vcc, 1.0, v149
	v_mov_b64_e32 v[62:63], v[42:43]
	s_cbranch_vccz .LBB0_250
	v_mov_b32_e32 v62, v149
	v_pk_mul_f32 v[76:77], v[62:63], v[56:57] op_sel_hi:[0,1]
	v_pk_mul_f32 v[74:75], v[62:63], v[54:55] op_sel_hi:[0,1]
	v_pk_mul_f32 v[72:73], v[62:63], v[52:53] op_sel_hi:[0,1]
	v_pk_mul_f32 v[70:71], v[62:63], v[50:51] op_sel_hi:[0,1]
	v_pk_mul_f32 v[68:69], v[62:63], v[48:49] op_sel_hi:[0,1]
	v_pk_mul_f32 v[66:67], v[62:63], v[46:47] op_sel_hi:[0,1]
	v_pk_mul_f32 v[64:65], v[62:63], v[44:45] op_sel_hi:[0,1]
	v_pk_mul_f32 v[62:63], v[62:63], v[42:43] op_sel_hi:[0,1]

; template <int NH, class InitF>
; __device__ __forceinline__ void attn_core64(const LAS unsigned char* kbuf  , const LAS unsigned char* vbuf  , const InitF& initf  ,
;                                             const bf16x8 (&bq)[NH][2], float (&m)[NH], float (&l)[NH], f32x4 (&O)[NH][4], int lane) {
;     ...
;     for (int hq = 0; hq < NH; ++hq) {
;         f32x4 sa[4];
; #pragma unroll
;         for (int t = 0; t < 4; ++t) sa[t] = initf(hq, t);
; #pragma unroll
;         for (int t = 0; t < 4; ++t) { const bf16x8 k0 = *(const LAS bf16x8*)(kbuf + (16 * t + c) * 144 + 16 * g), k1 = *(const LAS bf16x8*)(kbuf + (16 * t + c) * 144 + 16 * g + 64);
;             sa[t] = __builtin_amdgcn_mfma_f32_16x16x32_bf16(k0, bq[hq][0], sa[t], 0, 0, 0); sa[t] = __builtin_amdgcn_mfma_f32_16x16x32_bf16(k1, bq[hq][1], sa[t], 0, 0, 0); }
;         float mx = -3.0e38f;
; #pragma unroll
;         for (int t = 0; t < 4; ++t) mx = fmaxf(mx, fmaxf(fmaxf(sa[t][0], sa[t][1]), fmaxf(sa[t][2], sa[t][3])));
;         mx = fmaxf(mx, xor_sw<16>(mx)); mx = max_x32(mx);
;         const float mn = fmaxf(m[hq], mx); corr[hq] = __builtin_amdgcn_exp2f(m[hq] - mn); m[hq] = mn;
;         float p[16], ps = 0.f;
; #pragma unroll
;         for (int i = 0; i < 16; ++i) { p[i] = __builtin_amdgcn_exp2f(sa[i >> 2][i & 3] - mn); ps += p[i]; }
;         l[hq] = l[hq] * corr[hq] + ps;
;         u32x4 pw0, pw1;
;         pw0.x = cvt_pk_bf16(p[0], p[1]); pw0.y = cvt_pk_bf16(p[2], p[3]); pw0.z = cvt_pk_bf16(p[4], p[5]); pw0.w = cvt_pk_bf16(p[6], p[7]);
;         pw1.x = cvt_pk_bf16(p[8], p[9]); pw1.y = cvt_pk_bf16(p[10], p[11]); pw1.z = cvt_pk_bf16(p[12], p[13]); pw1.w = cvt_pk_bf16(p[14], p[15]);
;         pb[hq][0] = __builtin_bit_cast(bf16x8, pw0); pb[hq][1] = __builtin_bit_cast(bf16x8, pw1);
;     }
; #pragma unroll
;     for (int hq = 0; hq < NH; ++hq) {
;         if (__builtin_amdgcn_ballot_w64(corr[hq] != 1.0f) != 0ull) {
; #pragma unroll
; template <int NH, int NQ, bool TABLE> ...
;     ...
;                 if (__builtin_amdgcn_ballot_w64(!(fabsf(fb) <= flim && fabsf(fb + 51.f) <= flim)) == 0ull) {
;                     auto initf = [&](int hq, int t) { f32x4 v;
; #pragma unroll
;                         for (int r = 0; r < 4; ++r) v[r] = -slope2[hq] * fabsf(fb + (float)(16 * t + r));
;                         return v; };
;                     attn_core64<NH>(buf + SH_K, buf + SH_V, initf, bq, m, l, O, lane);
.LBB0_253:
	s_cbranch_execz .LBB0_244
	ds_read_b128 v[74:77], v202
	ds_read_b128 v[78:81], v202 offset:64
	s_mov_b32 s8, 2.0
	s_mov_b32 s9, 0x40400000
	v_pk_add_f32 v[58:59], v[32:33], s[8:9] op_sel_hi:[0,1]
	s_mov_b32 s8, 0x41900000
	v_and_b32_e32 v87, 0x7fffffff, v59
	v_and_b32_e32 v86, 0x7fffffff, v58
	v_mov_b32_e32 v137, v136
	s_mov_b32 s9, 0x41980000
	v_pk_mul_f32 v[60:61], v[86:87], v[136:137]
	v_pk_mul_f32 v[58:59], v[146:147], v[138:139]
	v_pk_add_f32 v[62:63], v[32:33], s[46:47] op_sel_hi:[0,1]
	v_pk_add_f32 v[64:65], v[32:33], s[8:9] op_sel_hi:[0,1]
	s_waitcnt lgkmcnt(1)
	v_mfma_f32_16x16x32_bf16 v[58:61], v[74:77], v[24:27], v[58:61]
	s_mov_b32 s8, 0x42000000
	ds_read_b128 v[82:85], v202 offset:2304
	ds_read_b128 v[90:93], v202 offset:2368
	ds_read_b128 v[94:97], v202 offset:4608
	ds_read_b128 v[98:101], v202 offset:4672
	v_and_b32_e32 v111, 0x7fffffff, v63
	v_and_b32_e32 v110, 0x7fffffff, v62
	v_and_b32_e32 v113, 0x7fffffff, v65
	v_and_b32_e32 v112, 0x7fffffff, v64
	s_mov_b32 s9, 0x42040000
	v_pk_mul_f32 v[64:65], v[112:113], v[136:137]
	v_pk_mul_f32 v[62:63], v[110:111], v[138:139]
	v_pk_add_f32 v[66:67], v[32:33], s[8:9] op_sel_hi:[0,1]
	s_mov_b32 s8, 0x42080000
	s_waitcnt lgkmcnt(3)
	v_mfma_f32_16x16x32_bf16 v[62:65], v[82:85], v[24:27], v[62:65]
	s_mov_b32 s9, 0x420c0000
	v_pk_add_f32 v[68:69], v[32:33], s[8:9] op_sel_hi:[0,1]
	s_mov_b32 s8, 0x42400000
	v_mfma_f32_16x16x32_bf16 v[58:61], v[78:81], v[28:31], v[58:61]
	s_mov_b32 s9, 0x42440000
	ds_read_b128 v[102:105], v202 offset:6912
	ds_read_b128 v[106:109], v202 offset:6976
	v_pk_add_f32 v[70:71], v[32:33], s[8:9] op_sel_hi:[0,1]
	s_waitcnt lgkmcnt(4)
	v_mfma_f32_16x16x32_bf16 v[62:65], v[90:93], v[28:31], v[62:65]
	s_nop 1
	v_max_f32_e32 v32, v61, v61
	v_and_b32_e32 v115, 0x7fffffff, v67
	v_and_b32_e32 v114, 0x7fffffff, v66
	v_and_b32_e32 v117, 0x7fffffff, v69
	v_and_b32_e32 v116, 0x7fffffff, v68
	v_max_f32_e32 v72, v60, v60
	v_and_b32_e32 v119, 0x7fffffff, v71
	v_and_b32_e32 v118, 0x7fffffff, v70
	v_pk_mul_f32 v[68:69], v[116:117], v[136:137]
	v_pk_mul_f32 v[66:67], v[114:115], v[138:139]
	v_max_f32_e32 v32, v72, v32
	v_pk_mul_f32 v[70:71], v[118:119], v[138:139]
	v_pk_mul_f32 v[72:73], v[144:145], v[136:137]
	s_waitcnt lgkmcnt(3)
	v_mfma_f32_16x16x32_bf16 v[66:69], v[94:97], v[24:27], v[66:69]
	v_max_f32_e32 v88, v65, v65
	v_max_f32_e32 v89, v64, v64
	v_mov_b32_e32 v135, v134
	s_waitcnt lgkmcnt(1)
	v_mfma_f32_16x16x32_bf16 v[70:73], v[102:105], v[24:27], v[70:73]
	v_max_f32_e32 v120, v89, v88
	v_pk_mul_f32 v[88:89], v[86:87], v[134:135]
	v_pk_mul_f32 v[86:87], v[146:147], v[140:141]
	v_mfma_f32_16x16x32_bf16 v[66:69], v[98:101], v[28:31], v[66:69]
	v_max3_f32 v32, v58, v59, v32
	v_mfma_f32_16x16x32_bf16 v[74:77], v[74:77], v[34:37], v[86:89]
	s_waitcnt lgkmcnt(0)
	v_mfma_f32_16x16x32_bf16 v[70:73], v[106:109], v[28:31], v[70:73]
	s_nop 0
	v_max3_f32 v86, v62, v63, v120
	v_max3_f32 v32, v32, s96, v86
	s_nop 0
	v_max_f32_e32 v120, v69, v69
	v_mfma_f32_16x16x32_bf16 v[86:89], v[78:81], v[38:41], v[74:77]
	v_max_f32_e32 v78, v68, v68
	v_max_f32_e32 v78, v78, v120
	v_pk_mul_f32 v[80:81], v[116:117], v[134:135]
	v_pk_mul_f32 v[76:77], v[112:113], v[134:135]
	v_pk_mul_f32 v[74:75], v[110:111], v[140:141]
	s_nop 1
	v_mfma_f32_16x16x32_bf16 v[74:77], v[82:85], v[34:37], v[74:77]
	v_max_f32_e32 v83, v73, v73
	v_max_f32_e32 v84, v72, v72
	v_max_f32_e32 v83, v84, v83
	v_max3_f32 v82, v66, v67, v78
	v_pk_mul_f32 v[78:79], v[114:115], v[140:141]
	v_max3_f32 v83, v70, v71, v83
	v_max3_f32 v32, v32, v82, v83
	v_mfma_f32_16x16x32_bf16 v[78:81], v[94:97], v[34:37], v[78:81]
	v_mul_f32_e64 v82, v118, v140
	v_mul_f32_e64 v83, v119, v141
	v_pk_mul_f32 v[84:85], v[144:145], v[134:135]
	v_mfma_f32_16x16x32_bf16 v[74:77], v[90:93], v[38:41], v[74:77]
	v_max_f32_e32 v91, v89, v89
	v_max_f32_e32 v92, v88, v88
	v_max_f32_e32 v91, v92, v91
	v_mfma_f32_16x16x32_bf16 v[82:85], v[102:105], v[34:37], v[82:85]
	s_nop 2
	v_max_f32_e32 v92, v77, v77
	v_max_f32_e32 v93, v76, v76
	v_mfma_f32_16x16x32_bf16 v[78:81], v[98:101], v[38:41], v[78:81]
	v_max_f32_e32 v92, v93, v92
	v_max3_f32 v91, v86, v87, v91
	v_max3_f32 v92, v74, v75, v92
	v_mfma_f32_16x16x32_bf16 v[82:85], v[106:109], v[38:41], v[82:85]
	v_max3_f32 v91, v91, s96, v92
	s_nop 2
	v_max_f32_e32 v92, v81, v81
	v_max_f32_e32 v93, v80, v80
	v_max_f32_e32 v92, v93, v92
	s_waitcnt lgkmcnt(0)
	v_mov_b32_e32 v90, v32
	s_nop 1
	v_permlane16_swap_b32_e32 v32, v90
	v_max_f32_e32 v90, v90, v90
	v_max_f32_e32 v93, v85, v85
	v_max_f32_e32 v94, v84, v84
	v_max_f32_e32 v93, v94, v93
	v_max3_f32 v92, v78, v79, v92
	v_max3_f32 v93, v82, v83, v93
	v_max_f32_e32 v32, v32, v90
	v_max3_f32 v92, v91, v92, v93
	v_mov_b32_e32 v90, v32
	s_nop 0
	v_permlane32_swap_b32_e32 v32, v90
	v_max3_f32 v135, v201, v32, v90
	v_sub_f32_e32 v32, v201, v135
	v_exp_f32_e32 v91, v32
	s_waitcnt lgkmcnt(0)
	v_mov_b32_e32 v93, v92
	s_nop 1
	v_permlane16_swap_b32_e32 v92, v93
	v_max_f32_e32 v32, v93, v93
	v_max_f32_e32 v32, v92, v32
	v_mov_b32_e32 v90, v32
	s_nop 1
	v_permlane32_swap_b32_e32 v32, v90
	v_cmp_neq_f32_e32 vcc, 1.0, v91
	s_cbranch_vccz .LBB0_256
	v_mov_b32_e32 v92, v91
	v_pk_mul_f32 v[56:57], v[92:93], v[56:57] op_sel_hi:[0,1]
	v_pk_mul_f32 v[54:55], v[92:93], v[54:55] op_sel_hi:[0,1]
	v_pk_mul_f32 v[52:53], v[92:93], v[52:53] op_sel_hi:[0,1]
	v_pk_mul_f32 v[50:51], v[92:93], v[50:51] op_sel_hi:[0,1]
	v_pk_mul_f32 v[48:49], v[92:93], v[48:49] op_sel_hi:[0,1]
	v_pk_mul_f32 v[46:47], v[92:93], v[46:47] op_sel_hi:[0,1]
	v_pk_mul_f32 v[44:45], v[92:93], v[44:45] op_sel_hi:[0,1]
	v_pk_mul_f32 v[42:43], v[92:93], v[42:43] op_sel_hi:[0,1]

; __device__ __forceinline__ unsigned cvt_pk_bf16(float lo, float hi) { const f32x2_t v = {lo, hi}; const bf16x2_t b = __builtin_convertvector(v, bf16x2_t); return __builtin_bit_cast(unsigned, b); }
; template <int O> __device__ __forceinline__ float xor_sw(float v) { return __int_as_float(__builtin_amdgcn_ds_swizzle(__float_as_int(v), 0x1f | (O << 10))); }
; __device__ __forceinline__ float sum_x32(float v) { const auto r = __builtin_amdgcn_permlane32_swap(__float_as_uint(v), __float_as_uint(v), false, false); return __uint_as_float(r[0]) + __uint_as_float(r[1]); }
; template <int NH>
; __device__ __forceinline__ void attn_store(bf16_t* orow  , const int (&ocol)[NH], const float (&l)[NH], const float (&extra)[NH], const f32x4 (&O)[NH][4], int lane) {
;     const int g = lane >> 4;
; #pragma unroll
;     for (int hq = 0; hq < NH; ++hq) { float lt = l[hq]; lt += xor_sw<16>(lt); lt = sum_x32(lt); lt += extra[hq];
;         const float inv = 1.0f / lt;
; #pragma unroll
;         for (int mt = 0; mt < 4; ++mt) { u32x2 w;
;             w.x = cvt_pk_bf16(O[hq][mt][0] * inv, O[hq][mt][1] * inv); w.y = cvt_pk_bf16(O[hq][mt][2] * inv, O[hq][mt][3] * inv);
;             *(u32x2*)(orow + ocol[hq] + 16 * mt + 4 * g) = w; } }
; __global__ void __launch_bounds__(NWAVES * 64, 2) mk_fwd(Args args) {
;     ...
;                         int ocol[2]; float extra[2];
; #pragma unroll
;                         for (int j = 0; j < 2; ++j) { const int hq = 4 * kvh + 2 * hp + j; ocol[j] = 512 + hq * 64; extra[j] = __builtin_amdgcn_exp2f(sinkp[hq] * LOG2E - m[j]); }
;                         attn_store<2>(CAT + (size_t)(b * SEQ + qp) * D, ocol, l, extra, O, lane);
.LBB0_258:
	s_lshl_b32 s8, s14, 2
	s_waitcnt vmcnt(1)
	v_mov_b32_e32 v12, s8
	global_load_dwordx2 v[12:13], v12, s[6:7]
	s_mov_b32 s8, 0x3fb8aa3b
	s_lshl_b32 s68, s11, 1
	s_waitcnt vmcnt(0)
	v_fma_f32 v12, v12, s8, -v201
	v_exp_f32_e32 v16, v12
	v_fma_f32 v12, v13, s8, -v200
	v_exp_f32_e32 v26, v12
	v_lshl_add_u32 v12, s12, 11, v198
	v_ashrrev_i32_e32 v13, 31, v12
	v_lshlrev_b64 v[12:13], 11, v[12:13]
	v_lshl_add_u64 v[14:15], s[80:81], 0, v[12:13]
	s_waitcnt lgkmcnt(0)
	v_mov_b32_e32 v12, v143
	s_nop 1
	v_permlane16_swap_b32_e32 v143, v12
	v_add_f32_e32 v12, v143, v12
	v_mov_b32_e32 v13, v12
	s_nop 1
	v_permlane32_swap_b32_e32 v12, v13
	v_add_f32_e32 v12, v12, v13
	v_add_f32_e32 v12, v16, v12
	v_div_scale_f32 v13, s[8:9], v12, v12, 1.0
	v_rcp_f32_e32 v16, v13
	s_nop 0
	v_fma_f32 v17, -v13, v16, 1.0
	v_fmac_f32_e32 v16, v17, v16
	v_div_scale_f32 v17, vcc, 1.0, v12, 1.0
	v_mul_f32_e32 v18, v17, v16
	v_fma_f32 v19, -v13, v18, v17
	v_fmac_f32_e32 v18, v19, v16
	v_fma_f32 v13, -v13, v18, v17
	v_div_fmas_f32 v13, v13, v16, v18
	v_div_fixup_f32 v12, v13, v12, 1.0
	v_pk_mul_f32 v[16:17], v[54:55], v[12:13] op_sel_hi:[1,0]
	v_pk_mul_f32 v[18:19], v[56:57], v[12:13] op_sel_hi:[1,0]
	v_cvt_pk_bf16_f32 v16, v16, v17
	v_cvt_pk_bf16_f32 v17, v18, v19
	v_lshl_add_u64 v[18:19], v[14:15], 0, s[68:69]
	v_lshl_add_u64 v[18:19], v[18:19], 0, v[128:129]
	global_store_dwordx2 v[18:19], v[16:17], off offset:1024
	v_pk_mul_f32 v[16:17], v[12:13], v[50:51] op_sel_hi:[0,1]
	v_pk_mul_f32 v[24:25], v[12:13], v[52:53] op_sel_hi:[0,1]
	v_cvt_pk_bf16_f32 v16, v16, v17
	v_cvt_pk_bf16_f32 v17, v24, v25
	global_store_dwordx2 v[18:19], v[16:17], off offset:1056
	v_pk_mul_f32 v[16:17], v[12:13], v[46:47] op_sel_hi:[0,1]
	v_pk_mul_f32 v[24:25], v[12:13], v[48:49] op_sel_hi:[0,1]
	v_cvt_pk_bf16_f32 v16, v16, v17
	v_cvt_pk_bf16_f32 v17, v24, v25
	global_store_dwordx2 v[18:19], v[16:17], off offset:1088
	v_pk_mul_f32 v[16:17], v[12:13], v[42:43] op_sel_hi:[0,1]
	v_pk_mul_f32 v[12:13], v[12:13], v[44:45] op_sel_hi:[0,1]
	v_cvt_pk_bf16_f32 v16, v16, v17
	v_cvt_pk_bf16_f32 v17, v12, v13
	global_store_dwordx2 v[18:19], v[16:17], off offset:1120
	s_lshl_b32 s68, s10, 1
	v_lshl_add_u64 v[14:15], v[14:15], 0, s[68:69]
	v_lshl_add_u64 v[14:15], v[14:15], 0, v[128:129]
	s_waitcnt lgkmcnt(0)
	v_mov_b32_e32 v12, v142
	s_nop 1
	v_permlane16_swap_b32_e32 v142, v12
	v_add_f32_e32 v12, v142, v12
	v_mov_b32_e32 v13, v12
	s_nop 1
	v_permlane32_swap_b32_e32 v12, v13
	v_add_f32_e32 v12, v12, v13
	v_add_f32_e32 v12, v26, v12
	v_div_scale_f32 v13, s[8:9], v12, v12, 1.0
	v_rcp_f32_e32 v16, v13
	s_mov_b64 s[8:9], 0
	v_fma_f32 v17, -v13, v16, 1.0
	v_fmac_f32_e32 v16, v17, v16
	v_div_scale_f32 v17, vcc, 1.0, v12, 1.0
	v_mul_f32_e32 v18, v17, v16
	v_fma_f32 v19, -v13, v18, v17
	v_fmac_f32_e32 v18, v19, v16
	v_fma_f32 v13, -v13, v18, v17
	v_div_fmas_f32 v13, v13, v16, v18
	v_div_fixup_f32 v12, v13, v12, 1.0
	v_pk_mul_f32 v[16:17], v[20:21], v[12:13] op_sel_hi:[1,0]
	v_pk_mul_f32 v[18:19], v[22:23], v[12:13] op_sel_hi:[1,0]
	v_pk_mul_f32 v[8:9], v[12:13], v[8:9] op_sel_hi:[0,1]
	v_pk_mul_f32 v[10:11], v[12:13], v[10:11] op_sel_hi:[0,1]
	v_pk_mul_f32 v[4:5], v[12:13], v[4:5] op_sel_hi:[0,1]
	v_pk_mul_f32 v[6:7], v[12:13], v[6:7] op_sel_hi:[0,1]
	v_pk_mul_f32 v[0:1], v[12:13], v[0:1] op_sel_hi:[0,1]
	v_pk_mul_f32 v[2:3], v[12:13], v[2:3] op_sel_hi:[0,1]
	v_cvt_pk_bf16_f32 v16, v16, v17
	v_cvt_pk_bf16_f32 v17, v18, v19
	v_cvt_pk_bf16_f32 v8, v8, v9
	v_cvt_pk_bf16_f32 v9, v10, v11
	v_cvt_pk_bf16_f32 v4, v4, v5
	v_cvt_pk_bf16_f32 v5, v6, v7
	v_cvt_pk_bf16_f32 v0, v0, v1
	v_cvt_pk_bf16_f32 v1, v2, v3
	global_store_dwordx2 v[14:15], v[16:17], off offset:1024
	global_store_dwordx2 v[14:15], v[8:9], off offset:1056
	global_store_dwordx2 v[14:15], v[4:5], off offset:1088
	global_store_dwordx2 v[14:15], v[0:1], off offset:1120

; template <int NH, class InitF>
; __device__ __forceinline__ void attn_core(const bf16x8 (&kf)[2][2], const LAS unsigned char* vbuf, const InitF& initf  ,
;                                           const bf16x8 (&bq)[NH][2], float (&m)[NH], float (&l)[NH], f32x4 (&O)[NH][4], int lane) {
;     ...
;     attn_vfrag(vbuf, vf, lane);
; #pragma unroll
;     for (int hq = 0; hq < NH; ++hq) {
;         f32x4 s0 = initf(hq, 0), s1 = initf(hq, 1);
;         s0 = __builtin_amdgcn_mfma_f32_16x16x32_bf16(kf[0][0], bq[hq][0], s0, 0, 0, 0); s0 = __builtin_amdgcn_mfma_f32_16x16x32_bf16(kf[0][1], bq[hq][1], s0, 0, 0, 0);
;         s1 = __builtin_amdgcn_mfma_f32_16x16x32_bf16(kf[1][0], bq[hq][0], s1, 0, 0, 0); s1 = __builtin_amdgcn_mfma_f32_16x16x32_bf16(kf[1][1], bq[hq][1], s1, 0, 0, 0);
;         float mx = fmaxf(fmaxf(fmaxf(s0[0], s0[1]), fmaxf(s0[2], s0[3])), fmaxf(fmaxf(s1[0], s1[1]), fmaxf(s1[2], s1[3])));
;         mx = fmaxf(mx, xor_sw<16>(mx)); mx = max_x32(mx);
;         const float mn = fmaxf(m[hq], mx), corr = __builtin_amdgcn_exp2f(m[hq] - mn); m[hq] = mn;
;         float p[8], ps = 0.f;
; #pragma unroll
;         for (int i = 0; i < 8; ++i) { p[i] = __builtin_amdgcn_exp2f((i < 4 ? s0[i & 3] : s1[i & 3]) - mn); ps += p[i]; }
;         l[hq] = l[hq] * corr + ps;
;         u32x4 pw; pw.x = cvt_pk_bf16(p[0], p[1]); pw.y = cvt_pk_bf16(p[2], p[3]); pw.z = cvt_pk_bf16(p[4], p[5]); pw.w = cvt_pk_bf16(p[6], p[7]);
;         const bf16x8 pb = __builtin_bit_cast(bf16x8, pw);
;         if (__builtin_amdgcn_ballot_w64(corr != 1.0f) != 0ull) {
; #pragma unroll
;             for (int mt = 0; mt < 4; ++mt) O[hq][mt] *= corr; }
; template <int NH, int P, class Desc, class BiasF> ...
;     ...
;     for (int t0 = 0; t0 < ntile; t0 += U) {
; #pragma unroll
;         for (int u = 0; u < U; ++u) {
;             const int t = t0 + u;
;             attn_vwrite(vr[(u + 1) % P], vl + ((u + 1) & 1) * 5120, lane);
;             const TileD td = dsc(t);
;             if (td.valid) { const LAS unsigned char* bp[NH];
; #pragma unroll
;                 for (int hq = 0; hq < NH; ++hq) bp[hq] = biasf(td, hq);
;                 auto initf = [&](int hq, int hh) { return *(const LAS f32x4*)(bp[hq] + 64 * hh); };
;                 attn_core<NH>(kf[u % P], vl + (u & 1) * 5120, initf, bq, m, l, O, lane); }
;             attn_load(kp_base, vp_base, dsc(t + P), kf[u % P], vr[u % P], lane);
.LBB0_265:
	s_cmp_gt_i32 s33, s30
	s_waitcnt vmcnt(3)
	ds_write_b128 v187, v[60:63] offset:5120
	s_waitcnt vmcnt(2)
	ds_write_b128 v188, v[64:67] offset:5120
	s_waitcnt vmcnt(1)
	ds_write_b128 v189, v[68:71] offset:5120
	s_waitcnt vmcnt(0)
	ds_write_b128 v190, v[72:75] offset:5120
	s_cbranch_scc0 .LBB0_269
	s_lshr_b32 s16, s33, 2
	v_add_u32_e32 v32, s16, v100
	ds_read_b128 v[60:63], v32 offset:512
	s_waitcnt lgkmcnt(0)
	v_mfma_f32_16x16x32_bf16 v[40:43], v[40:43], v[0:3], v[60:63]
	s_nop 2
	ds_read_b128 v[60:63], v32 offset:576
	v_mfma_f32_16x16x32_bf16 v[64:67], v[24:27], v[4:7], v[40:43]
	s_waitcnt lgkmcnt(0)
	v_mfma_f32_16x16x32_bf16 v[34:37], v[36:39], v[0:3], v[60:63]
	v_mfma_f32_16x16x32_bf16 v[60:63], v[28:31], v[4:7], v[34:37]
	s_nop 4
	v_max_f32_e32 v24, v65, v65
	v_max_f32_e32 v25, v64, v64
	v_max_f32_e32 v26, v67, v67
	v_max_f32_e32 v27, v66, v66
	v_max_f32_e32 v24, v25, v24
	v_max_f32_e32 v28, v63, v63
	v_max_f32_e32 v29, v62, v62
	v_max_f32_e32 v25, v27, v26
	v_max_f32_e32 v26, v29, v28
	v_max3_f32 v26, v60, v61, v26
	v_max3_f32 v26, v24, v25, v26
	ds_read_b64_tr_b16 v[38:39], v191
	ds_read_b64_tr_b16 v[34:35], v191 offset:32
	ds_read_b64_tr_b16 v[28:29], v191 offset:64
	ds_read_b64_tr_b16 v[24:25], v191 offset:96
	s_waitcnt lgkmcnt(4)
	v_mov_b32_e32 v27, v26
	s_nop 1
	v_permlane16_swap_b32_e32 v26, v27
	v_max_f32_e32 v27, v27, v27
	v_max_f32_e32 v26, v26, v27
	v_mov_b32_e32 v27, v26
	s_nop 1
	v_permlane32_swap_b32_e32 v26, v27
	v_max3_f32 v76, v116, v26, v27
	v_sub_f32_e32 v26, v116, v76
	v_exp_f32_e32 v32, v26
	ds_read_b64_tr_b16 v[40:41], v191 offset:2560
	ds_read_b64_tr_b16 v[36:37], v191 offset:2592
	ds_read_b64_tr_b16 v[30:31], v191 offset:2624
	ds_read_b64_tr_b16 v[26:27], v191 offset:2656
	v_cmp_neq_f32_e32 vcc, 1.0, v32
	s_cbranch_vccz .LBB0_268
	v_pk_mul_f32 v[22:23], v[22:23], v[32:33] op_sel_hi:[1,0]
	v_pk_mul_f32 v[20:21], v[20:21], v[32:33] op_sel_hi:[1,0]
	v_pk_mul_f32 v[18:19], v[18:19], v[32:33] op_sel_hi:[1,0]
	v_pk_mul_f32 v[16:17], v[16:17], v[32:33] op_sel_hi:[1,0]
	v_pk_mul_f32 v[14:15], v[14:15], v[32:33] op_sel_hi:[1,0]
	v_pk_mul_f32 v[12:13], v[12:13], v[32:33] op_sel_hi:[1,0]
	v_pk_mul_f32 v[10:11], v[10:11], v[32:33] op_sel_hi:[1,0]
	v_pk_mul_f32 v[8:9], v[8:9], v[32:33] op_sel_hi:[1,0]

; template <int NH, class InitF>
; __device__ __forceinline__ void attn_core(const bf16x8 (&kf)[2][2], const LAS unsigned char* vbuf, const InitF& initf  ,
;                                           const bf16x8 (&bq)[NH][2], float (&m)[NH], float (&l)[NH], f32x4 (&O)[NH][4], int lane) {
;     ...
;     attn_vfrag(vbuf, vf, lane);
; #pragma unroll
;     for (int hq = 0; hq < NH; ++hq) {
;         f32x4 s0 = initf(hq, 0), s1 = initf(hq, 1);
;         s0 = __builtin_amdgcn_mfma_f32_16x16x32_bf16(kf[0][0], bq[hq][0], s0, 0, 0, 0); s0 = __builtin_amdgcn_mfma_f32_16x16x32_bf16(kf[0][1], bq[hq][1], s0, 0, 0, 0);
;         s1 = __builtin_amdgcn_mfma_f32_16x16x32_bf16(kf[1][0], bq[hq][0], s1, 0, 0, 0); s1 = __builtin_amdgcn_mfma_f32_16x16x32_bf16(kf[1][1], bq[hq][1], s1, 0, 0, 0);
;         float mx = fmaxf(fmaxf(fmaxf(s0[0], s0[1]), fmaxf(s0[2], s0[3])), fmaxf(fmaxf(s1[0], s1[1]), fmaxf(s1[2], s1[3])));
;         mx = fmaxf(mx, xor_sw<16>(mx)); mx = max_x32(mx);
;         const float mn = fmaxf(m[hq], mx), corr = __builtin_amdgcn_exp2f(m[hq] - mn); m[hq] = mn;
;         float p[8], ps = 0.f;
; #pragma unroll
;         for (int i = 0; i < 8; ++i) { p[i] = __builtin_amdgcn_exp2f((i < 4 ? s0[i & 3] : s1[i & 3]) - mn); ps += p[i]; }
;         l[hq] = l[hq] * corr + ps;
;         u32x4 pw; pw.x = cvt_pk_bf16(p[0], p[1]); pw.y = cvt_pk_bf16(p[2], p[3]); pw.z = cvt_pk_bf16(p[4], p[5]); pw.w = cvt_pk_bf16(p[6], p[7]);
;         const bf16x8 pb = __builtin_bit_cast(bf16x8, pw);
;         if (__builtin_amdgcn_ballot_w64(corr != 1.0f) != 0ull) {
; #pragma unroll
;             for (int mt = 0; mt < 4; ++mt) O[hq][mt] *= corr; }
; template <int NH, int P, class Desc, class BiasF> ...
;     ...
;     for (int t0 = 0; t0 < ntile; t0 += U) {
; #pragma unroll
;         for (int u = 0; u < U; ++u) {
;             const int t = t0 + u;
;             attn_vwrite(vr[(u + 1) % P], vl + ((u + 1) & 1) * 5120, lane);
;             const TileD td = dsc(t);
;             if (td.valid) { const LAS unsigned char* bp[NH];
; #pragma unroll
;                 for (int hq = 0; hq < NH; ++hq) bp[hq] = biasf(td, hq);
;                 auto initf = [&](int hq, int hh) { return *(const LAS f32x4*)(bp[hq] + 64 * hh); };
;                 attn_core<NH>(kf[u % P], vl + (u & 1) * 5120, initf, bq, m, l, O, lane); }
;             attn_load(kp_base, vp_base, dsc(t + P), kf[u % P], vr[u % P], lane);
.LBB0_275:
	s_or_b32 s18, s33, 0x200
	s_cmp_ge_u32 s18, s31
	s_waitcnt vmcnt(3)
	ds_write_b128 v187, v[68:71]
	s_waitcnt vmcnt(2)
	ds_write_b128 v188, v[60:63]
	s_waitcnt vmcnt(1)
	ds_write_b128 v189, v[64:67]
	s_waitcnt vmcnt(0)
	ds_write_b128 v190, v[72:75]
	s_cbranch_scc1 .LBB0_279
	s_lshr_b32 s18, s18, 2
	v_add_u32_e32 v32, s18, v100
	ds_read_b128 v[60:63], v32 offset:512
	s_waitcnt lgkmcnt(0)
	v_mfma_f32_16x16x32_bf16 v[56:59], v[56:59], v[0:3], v[60:63]
	s_nop 2
	ds_read_b128 v[60:63], v32 offset:576
	v_mfma_f32_16x16x32_bf16 v[64:67], v[44:47], v[4:7], v[56:59]
	s_waitcnt lgkmcnt(0)
	v_mfma_f32_16x16x32_bf16 v[48:51], v[48:51], v[0:3], v[60:63]
	v_mfma_f32_16x16x32_bf16 v[60:63], v[52:55], v[4:7], v[48:51]
	s_nop 4
	v_max_f32_e32 v32, v65, v65
	v_max_f32_e32 v34, v64, v64
	v_max_f32_e32 v35, v67, v67
	v_max_f32_e32 v44, v66, v66
	v_max_f32_e32 v32, v34, v32
	v_max_f32_e32 v45, v63, v63
	v_max_f32_e32 v46, v62, v62
	v_max_f32_e32 v34, v44, v35
	v_max_f32_e32 v35, v46, v45
	v_max3_f32 v35, v60, v61, v35
	v_max3_f32 v32, v32, v34, v35
	ds_read_b64_tr_b16 v[56:57], v191 offset:5120
	ds_read_b64_tr_b16 v[52:53], v191 offset:5152
	ds_read_b64_tr_b16 v[48:49], v191 offset:5184
	ds_read_b64_tr_b16 v[44:45], v191 offset:5216
	ds_read_b64_tr_b16 v[58:59], v191 offset:7680
	ds_read_b64_tr_b16 v[54:55], v191 offset:7712
	ds_read_b64_tr_b16 v[50:51], v191 offset:7744
	ds_read_b64_tr_b16 v[46:47], v191 offset:7776
	s_waitcnt lgkmcnt(8)
	v_mov_b32_e32 v34, v32
	s_nop 1
	v_permlane16_swap_b32_e32 v32, v34
	v_max_f32_e32 v34, v34, v34
	v_max_f32_e32 v32, v32, v34
	v_mov_b32_e32 v34, v32
	s_nop 1
	v_permlane32_swap_b32_e32 v32, v34
	v_max3_f32 v116, v76, v32, v34
	v_sub_f32_e32 v32, v76, v116
	v_exp_f32_e32 v32, v32
	s_nop 0
	v_cmp_neq_f32_e32 vcc, 1.0, v32
	s_cbranch_vccz .LBB0_278
	v_pk_mul_f32 v[22:23], v[22:23], v[32:33] op_sel_hi:[1,0]
	v_pk_mul_f32 v[20:21], v[20:21], v[32:33] op_sel_hi:[1,0]
	v_pk_mul_f32 v[18:19], v[18:19], v[32:33] op_sel_hi:[1,0]
	v_pk_mul_f32 v[16:17], v[16:17], v[32:33] op_sel_hi:[1,0]
	v_pk_mul_f32 v[14:15], v[14:15], v[32:33] op_sel_hi:[1,0]
	v_pk_mul_f32 v[12:13], v[12:13], v[32:33] op_sel_hi:[1,0]
	v_pk_mul_f32 v[10:11], v[10:11], v[32:33] op_sel_hi:[1,0]
	v_pk_mul_f32 v[8:9], v[8:9], v[32:33] op_sel_hi:[1,0]

; template <int NH, class InitF>
; __device__ __forceinline__ void attn_core(const bf16x8 (&kf)[2][2], const LAS unsigned char* vbuf, const InitF& initf  ,
;                                           const bf16x8 (&bq)[NH][2], float (&m)[NH], float (&l)[NH], f32x4 (&O)[NH][4], int lane) {
;     ...
;     attn_vfrag(vbuf, vf, lane);
; #pragma unroll
;     for (int hq = 0; hq < NH; ++hq) {
;         f32x4 s0 = initf(hq, 0), s1 = initf(hq, 1);
;         s0 = __builtin_amdgcn_mfma_f32_16x16x32_bf16(kf[0][0], bq[hq][0], s0, 0, 0, 0); s0 = __builtin_amdgcn_mfma_f32_16x16x32_bf16(kf[0][1], bq[hq][1], s0, 0, 0, 0);
;         s1 = __builtin_amdgcn_mfma_f32_16x16x32_bf16(kf[1][0], bq[hq][0], s1, 0, 0, 0); s1 = __builtin_amdgcn_mfma_f32_16x16x32_bf16(kf[1][1], bq[hq][1], s1, 0, 0, 0);
;         float mx = fmaxf(fmaxf(fmaxf(s0[0], s0[1]), fmaxf(s0[2], s0[3])), fmaxf(fmaxf(s1[0], s1[1]), fmaxf(s1[2], s1[3])));
;         mx = fmaxf(mx, xor_sw<16>(mx)); mx = max_x32(mx);
;         const float mn = fmaxf(m[hq], mx), corr = __builtin_amdgcn_exp2f(m[hq] - mn); m[hq] = mn;
;         float p[8], ps = 0.f;
; #pragma unroll
;         for (int i = 0; i < 8; ++i) { p[i] = __builtin_amdgcn_exp2f((i < 4 ? s0[i & 3] : s1[i & 3]) - mn); ps += p[i]; }
;         l[hq] = l[hq] * corr + ps;
;         u32x4 pw; pw.x = cvt_pk_bf16(p[0], p[1]); pw.y = cvt_pk_bf16(p[2], p[3]); pw.z = cvt_pk_bf16(p[4], p[5]); pw.w = cvt_pk_bf16(p[6], p[7]);
;         const bf16x8 pb = __builtin_bit_cast(bf16x8, pw);
;         if (__builtin_amdgcn_ballot_w64(corr != 1.0f) != 0ull) {
; #pragma unroll
;             for (int mt = 0; mt < 4; ++mt) O[hq][mt] *= corr; }
; template <int NH, int P, class Desc, class BiasF> ...
;     ...
;     for (int t0 = 0; t0 < ntile; t0 += U) {
; #pragma unroll
;         for (int u = 0; u < U; ++u) {
;             const int t = t0 + u;
;             attn_vwrite(vr[(u + 1) % P], vl + ((u + 1) & 1) * 5120, lane);
;             const TileD td = dsc(t);
;             if (td.valid) { const LAS unsigned char* bp[NH];
; #pragma unroll
;                 for (int hq = 0; hq < NH; ++hq) bp[hq] = biasf(td, hq);
;                 auto initf = [&](int hq, int hh) { return *(const LAS f32x4*)(bp[hq] + 64 * hh); };
;                 attn_core<NH>(kf[u % P], vl + (u & 1) * 5120, initf, bq, m, l, O, lane); }
;             attn_load(kp_base, vp_base, dsc(t + P), kf[u % P], vr[u % P], lane);
.LBB0_289:
	s_cmp_gt_i32 s16, s30
	s_waitcnt vmcnt(3)
	ds_write_b128 v187, v[84:87] offset:5120
	s_waitcnt vmcnt(2)
	ds_write_b128 v188, v[88:91] offset:5120
	s_waitcnt vmcnt(1)
	ds_write_b128 v189, v[92:95] offset:5120
	s_waitcnt vmcnt(0)
	ds_write_b128 v190, v[96:99] offset:5120
	s_cbranch_scc0 .LBB0_293
	s_lshr_b32 s12, s16, 2
	v_add_u32_e32 v32, s12, v100
	ds_read_b128 v[84:87], v32 offset:512
	s_waitcnt lgkmcnt(0)
	v_mfma_f32_16x16x32_bf16 v[64:67], v[64:67], v[24:27], v[84:87]
	s_nop 2
	ds_read_b128 v[84:87], v32 offset:576
	v_mfma_f32_16x16x32_bf16 v[88:91], v[52:55], v[28:31], v[64:67]
	s_waitcnt lgkmcnt(0)
	v_mfma_f32_16x16x32_bf16 v[60:63], v[60:63], v[24:27], v[84:87]
	v_mfma_f32_16x16x32_bf16 v[84:87], v[56:59], v[28:31], v[60:63]
	s_nop 4
	v_max_f32_e32 v32, v89, v89
	v_max_f32_e32 v34, v88, v88
	v_max_f32_e32 v35, v91, v91
	v_max_f32_e32 v52, v90, v90
	v_max_f32_e32 v32, v34, v32
	v_max_f32_e32 v53, v87, v87
	v_max_f32_e32 v54, v86, v86
	v_max_f32_e32 v34, v52, v35
	v_max_f32_e32 v35, v54, v53
	v_max3_f32 v35, v84, v85, v35
	v_max3_f32 v32, v32, v34, v35
	ds_read_b64_tr_b16 v[64:65], v191
	ds_read_b64_tr_b16 v[60:61], v191 offset:32
	ds_read_b64_tr_b16 v[56:57], v191 offset:64
	ds_read_b64_tr_b16 v[52:53], v191 offset:96
	ds_read_b64_tr_b16 v[66:67], v191 offset:2560
	ds_read_b64_tr_b16 v[62:63], v191 offset:2592
	ds_read_b64_tr_b16 v[58:59], v191 offset:2624
	ds_read_b64_tr_b16 v[54:55], v191 offset:2656
	s_waitcnt lgkmcnt(8)
	v_mov_b32_e32 v34, v32
	s_nop 1
	v_permlane16_swap_b32_e32 v32, v34
	v_max_f32_e32 v34, v34, v34
	v_max_f32_e32 v32, v32, v34
	v_mov_b32_e32 v34, v32
	s_nop 1
	v_permlane32_swap_b32_e32 v32, v34
	v_max3_f32 v34, v118, v32, v34
	v_sub_f32_e32 v32, v118, v34
	v_exp_f32_e32 v32, v32
	s_nop 0
	v_cmp_neq_f32_e32 vcc, 1.0, v32
	s_cbranch_vccz .LBB0_292
	v_pk_mul_f32 v[50:51], v[50:51], v[32:33] op_sel_hi:[1,0]
	v_pk_mul_f32 v[48:49], v[48:49], v[32:33] op_sel_hi:[1,0]
	v_pk_mul_f32 v[46:47], v[46:47], v[32:33] op_sel_hi:[1,0]
	v_pk_mul_f32 v[44:45], v[44:45], v[32:33] op_sel_hi:[1,0]
	v_pk_mul_f32 v[42:43], v[42:43], v[32:33] op_sel_hi:[1,0]
	v_pk_mul_f32 v[40:41], v[40:41], v[32:33] op_sel_hi:[1,0]
	v_pk_mul_f32 v[38:39], v[38:39], v[32:33] op_sel_hi:[1,0]
	v_pk_mul_f32 v[36:37], v[36:37], v[32:33] op_sel_hi:[1,0]

; template <int NH, class InitF>
; __device__ __forceinline__ void attn_core(const bf16x8 (&kf)[2][2], const LAS unsigned char* vbuf, const InitF& initf  ,
;                                           const bf16x8 (&bq)[NH][2], float (&m)[NH], float (&l)[NH], f32x4 (&O)[NH][4], int lane) {
;     ...
;     attn_vfrag(vbuf, vf, lane);
; #pragma unroll
;     for (int hq = 0; hq < NH; ++hq) {
;         f32x4 s0 = initf(hq, 0), s1 = initf(hq, 1);
;         s0 = __builtin_amdgcn_mfma_f32_16x16x32_bf16(kf[0][0], bq[hq][0], s0, 0, 0, 0); s0 = __builtin_amdgcn_mfma_f32_16x16x32_bf16(kf[0][1], bq[hq][1], s0, 0, 0, 0);
;         s1 = __builtin_amdgcn_mfma_f32_16x16x32_bf16(kf[1][0], bq[hq][0], s1, 0, 0, 0); s1 = __builtin_amdgcn_mfma_f32_16x16x32_bf16(kf[1][1], bq[hq][1], s1, 0, 0, 0);
;         float mx = fmaxf(fmaxf(fmaxf(s0[0], s0[1]), fmaxf(s0[2], s0[3])), fmaxf(fmaxf(s1[0], s1[1]), fmaxf(s1[2], s1[3])));
;         mx = fmaxf(mx, xor_sw<16>(mx)); mx = max_x32(mx);
;         const float mn = fmaxf(m[hq], mx), corr = __builtin_amdgcn_exp2f(m[hq] - mn); m[hq] = mn;
;         float p[8], ps = 0.f;
; #pragma unroll
;         for (int i = 0; i < 8; ++i) { p[i] = __builtin_amdgcn_exp2f((i < 4 ? s0[i & 3] : s1[i & 3]) - mn); ps += p[i]; }
;         l[hq] = l[hq] * corr + ps;
;         u32x4 pw; pw.x = cvt_pk_bf16(p[0], p[1]); pw.y = cvt_pk_bf16(p[2], p[3]); pw.z = cvt_pk_bf16(p[4], p[5]); pw.w = cvt_pk_bf16(p[6], p[7]);
;         const bf16x8 pb = __builtin_bit_cast(bf16x8, pw);
;         if (__builtin_amdgcn_ballot_w64(corr != 1.0f) != 0ull) {
; #pragma unroll
;             for (int mt = 0; mt < 4; ++mt) O[hq][mt] *= corr; }
; template <int NH, int P, class Desc, class BiasF> ...
;     ...
;     for (int t0 = 0; t0 < ntile; t0 += U) {
; #pragma unroll
;         for (int u = 0; u < U; ++u) {
;             const int t = t0 + u;
;             attn_vwrite(vr[(u + 1) % P], vl + ((u + 1) & 1) * 5120, lane);
;             const TileD td = dsc(t);
;             if (td.valid) { const LAS unsigned char* bp[NH];
; #pragma unroll
;                 for (int hq = 0; hq < NH; ++hq) bp[hq] = biasf(td, hq);
;                 auto initf = [&](int hq, int hh) { return *(const LAS f32x4*)(bp[hq] + 64 * hh); };
;                 attn_core<NH>(kf[u % P], vl + (u & 1) * 5120, initf, bq, m, l, O, lane); }
;             attn_load(kp_base, vp_base, dsc(t + P), kf[u % P], vr[u % P], lane);
.LBB0_299:
	s_or_b32 s14, s16, 0x200
	s_cmp_ge_u32 s14, s31
	s_waitcnt vmcnt(3)
	ds_write_b128 v187, v[92:95]
	s_waitcnt vmcnt(2)
	ds_write_b128 v188, v[84:87]
	s_waitcnt vmcnt(1)
	ds_write_b128 v189, v[88:91]
	s_waitcnt vmcnt(0)
	ds_write_b128 v190, v[96:99]
	s_cbranch_scc1 .LBB0_303
	s_lshr_b32 s14, s14, 2
	v_add_u32_e32 v32, s14, v100
	ds_read_b128 v[84:87], v32 offset:512
	s_waitcnt lgkmcnt(0)
	v_mfma_f32_16x16x32_bf16 v[80:83], v[80:83], v[24:27], v[84:87]
	s_nop 2
	ds_read_b128 v[84:87], v32 offset:576
	v_mfma_f32_16x16x32_bf16 v[88:91], v[68:71], v[28:31], v[80:83]
	s_waitcnt lgkmcnt(0)
	v_mfma_f32_16x16x32_bf16 v[72:75], v[72:75], v[24:27], v[84:87]
	v_mfma_f32_16x16x32_bf16 v[84:87], v[76:79], v[28:31], v[72:75]
	s_nop 4
	v_max_f32_e32 v32, v89, v89
	v_max_f32_e32 v35, v88, v88
	v_max_f32_e32 v68, v91, v91
	v_max_f32_e32 v69, v90, v90
	v_max_f32_e32 v32, v35, v32
	v_max_f32_e32 v70, v87, v87
	v_max_f32_e32 v71, v86, v86
	v_max_f32_e32 v35, v69, v68
	v_max_f32_e32 v68, v71, v70
	v_max3_f32 v68, v84, v85, v68
	v_max3_f32 v32, v32, v35, v68
	ds_read_b64_tr_b16 v[80:81], v191 offset:5120
	ds_read_b64_tr_b16 v[76:77], v191 offset:5152
	ds_read_b64_tr_b16 v[72:73], v191 offset:5184
	ds_read_b64_tr_b16 v[68:69], v191 offset:5216
	ds_read_b64_tr_b16 v[82:83], v191 offset:7680
	ds_read_b64_tr_b16 v[78:79], v191 offset:7712
	ds_read_b64_tr_b16 v[74:75], v191 offset:7744
	ds_read_b64_tr_b16 v[70:71], v191 offset:7776
	s_waitcnt lgkmcnt(8)
	v_mov_b32_e32 v35, v32
	s_nop 1
	v_permlane16_swap_b32_e32 v32, v35
	v_max_f32_e32 v35, v35, v35
	v_max_f32_e32 v32, v32, v35
	v_mov_b32_e32 v35, v32
	s_nop 1
	v_permlane32_swap_b32_e32 v32, v35
	v_max3_f32 v118, v34, v32, v35
	v_sub_f32_e32 v32, v34, v118
	v_exp_f32_e32 v32, v32
	s_nop 0
	v_cmp_neq_f32_e32 vcc, 1.0, v32
	s_cbranch_vccz .LBB0_302
	v_pk_mul_f32 v[50:51], v[50:51], v[32:33] op_sel_hi:[1,0]
	v_pk_mul_f32 v[48:49], v[48:49], v[32:33] op_sel_hi:[1,0]
	v_pk_mul_f32 v[46:47], v[46:47], v[32:33] op_sel_hi:[1,0]
	v_pk_mul_f32 v[44:45], v[44:45], v[32:33] op_sel_hi:[1,0]
	v_pk_mul_f32 v[42:43], v[42:43], v[32:33] op_sel_hi:[1,0]
	v_pk_mul_f32 v[40:41], v[40:41], v[32:33] op_sel_hi:[1,0]
	v_pk_mul_f32 v[38:39], v[38:39], v[32:33] op_sel_hi:[1,0]
	v_pk_mul_f32 v[36:37], v[36:37], v[32:33] op_sel_hi:[1,0]

; #define LAS __attribute__((address_space(3)))
; template <int NH, class InitF>
; __device__ __forceinline__ void attn_core(const bf16x8 (&kf)[2][2], const LAS unsigned char* vbuf, const InitF& initf  ,
;                                           const bf16x8 (&bq)[NH][2], float (&m)[NH], float (&l)[NH], f32x4 (&O)[NH][4], int lane) {
;     ...
;     attn_vfrag(vbuf, vf, lane);
; #pragma unroll
;     for (int hq = 0; hq < NH; ++hq) {
;         f32x4 s0 = initf(hq, 0), s1 = initf(hq, 1);
;         s0 = __builtin_amdgcn_mfma_f32_16x16x32_bf16(kf[0][0], bq[hq][0], s0, 0, 0, 0); s0 = __builtin_amdgcn_mfma_f32_16x16x32_bf16(kf[0][1], bq[hq][1], s0, 0, 0, 0);
;         s1 = __builtin_amdgcn_mfma_f32_16x16x32_bf16(kf[1][0], bq[hq][0], s1, 0, 0, 0); s1 = __builtin_amdgcn_mfma_f32_16x16x32_bf16(kf[1][1], bq[hq][1], s1, 0, 0, 0);
;         float mx = fmaxf(fmaxf(fmaxf(s0[0], s0[1]), fmaxf(s0[2], s0[3])), fmaxf(fmaxf(s1[0], s1[1]), fmaxf(s1[2], s1[3])));
;         mx = fmaxf(mx, xor_sw<16>(mx)); mx = max_x32(mx);
;         const float mn = fmaxf(m[hq], mx), corr = __builtin_amdgcn_exp2f(m[hq] - mn); m[hq] = mn;
;         float p[8], ps = 0.f;
; #pragma unroll
;         for (int i = 0; i < 8; ++i) { p[i] = __builtin_amdgcn_exp2f((i < 4 ? s0[i & 3] : s1[i & 3]) - mn); ps += p[i]; }
;         l[hq] = l[hq] * corr + ps;
;         u32x4 pw; pw.x = cvt_pk_bf16(p[0], p[1]); pw.y = cvt_pk_bf16(p[2], p[3]); pw.z = cvt_pk_bf16(p[4], p[5]); pw.w = cvt_pk_bf16(p[6], p[7]);
;         const bf16x8 pb = __builtin_bit_cast(bf16x8, pw);
;         if (__builtin_amdgcn_ballot_w64(corr != 1.0f) != 0ull) {
; #pragma unroll
;             for (int mt = 0; mt < 4; ++mt) O[hq][mt] *= corr; }
; #pragma unroll
;         for (int mt = 0; mt < 4; ++mt) O[hq][mt] = __builtin_amdgcn_mfma_f32_16x16x32_bf16(vf[mt], pb, O[hq][mt], 0, 0, 0);
;     }
; template <int NH, int P, class Desc, class BiasF> ...
;     ...
;     for (int t0 = 0; t0 < ntile; t0 += U) {
; #pragma unroll
;         for (int u = 0; u < U; ++u) {
;             const int t = t0 + u;
;             attn_vwrite(vr[(u + 1) % P], vl + ((u + 1) & 1) * 5120, lane);
;             const TileD td = dsc(t);
;             if (td.valid) { const LAS unsigned char* bp[NH];
; #pragma unroll
;                 for (int hq = 0; hq < NH; ++hq) bp[hq] = biasf(td, hq);
;                 auto initf = [&](int hq, int hh) { return *(const LAS f32x4*)(bp[hq] + 64 * hh); };
.LBB0_317:
	s_add_i32 s30, s18, s16
	s_add_i32 s10, s30, 0xffffff00
	s_cmpk_gt_u32 s10, 0x7ff
	v_add_u32_e32 v109, s16, v108
	s_waitcnt vmcnt(3)
	ds_write_b128 v187, v[92:95] offset:5120
	s_waitcnt vmcnt(2)
	ds_write_b128 v188, v[84:87] offset:5120
	s_waitcnt vmcnt(1)
	ds_write_b128 v189, v[88:91] offset:5120
	s_waitcnt vmcnt(0)
	ds_write_b128 v190, v[96:99] offset:5120
	s_cbranch_scc1 .LBB0_323
	v_add_u32_e32 v32, 0x229c0, v109
	ds_read_b128 v[84:87], v32
	v_add_u32_e32 v32, 0x22a00, v109
	ds_read_b128 v[88:91], v32
	s_waitcnt lgkmcnt(1)
	v_mfma_f32_16x16x32_bf16 v[84:87], v[52:55], v[0:3], v[84:87]
	s_waitcnt lgkmcnt(0)
	v_mfma_f32_16x16x32_bf16 v[88:91], v[60:63], v[0:3], v[88:91]
	v_mfma_f32_16x16x32_bf16 v[100:103], v[56:59], v[4:7], v[84:87]
	v_mfma_f32_16x16x32_bf16 v[104:107], v[64:67], v[4:7], v[88:91]
	s_nop 6
	v_max_f32_e32 v32, v101, v101
	v_max_f32_e32 v34, v100, v100
	v_max_f32_e32 v84, v103, v103
	v_max_f32_e32 v85, v102, v102
	v_max_f32_e32 v86, v107, v107
	v_max_f32_e32 v87, v106, v106
	v_max_f32_e32 v32, v34, v32
	v_max_f32_e32 v34, v85, v84
	v_max_f32_e32 v84, v87, v86
	v_max3_f32 v84, v104, v105, v84
	v_max3_f32 v32, v32, v34, v84
	ds_read_b64_tr_b16 v[96:97], v191
	ds_read_b64_tr_b16 v[92:93], v191 offset:32
	ds_read_b64_tr_b16 v[88:89], v191 offset:64
	ds_read_b64_tr_b16 v[84:85], v191 offset:96
	ds_read_b64_tr_b16 v[98:99], v191 offset:2560
	ds_read_b64_tr_b16 v[94:95], v191 offset:2592
	ds_read_b64_tr_b16 v[90:91], v191 offset:2624
	ds_read_b64_tr_b16 v[86:87], v191 offset:2656
	s_waitcnt lgkmcnt(8)
	v_mov_b32_e32 v34, v32
	s_nop 1
	v_permlane16_swap_b32_e32 v32, v34
	v_max_f32_e32 v34, v34, v34
	v_max_f32_e32 v32, v32, v34
	v_mov_b32_e32 v34, v32
	s_nop 1
	v_permlane32_swap_b32_e32 v32, v34
	v_max3_f32 v110, v116, v32, v34
	v_sub_f32_e32 v32, v116, v110
	v_exp_f32_e32 v32, v32
	s_nop 0
	v_cmp_neq_f32_e32 vcc, 1.0, v32
	s_cbranch_vccz .LBB0_320
	v_pk_mul_f32 v[22:23], v[22:23], v[32:33] op_sel_hi:[1,0]
	v_pk_mul_f32 v[20:21], v[20:21], v[32:33] op_sel_hi:[1,0]
	v_pk_mul_f32 v[18:19], v[32:33], v[18:19] op_sel_hi:[0,1]
	v_pk_mul_f32 v[16:17], v[32:33], v[16:17] op_sel_hi:[0,1]
	v_pk_mul_f32 v[14:15], v[32:33], v[14:15] op_sel_hi:[0,1]
	v_pk_mul_f32 v[12:13], v[32:33], v[12:13] op_sel_hi:[0,1]
	v_pk_mul_f32 v[10:11], v[32:33], v[10:11] op_sel_hi:[0,1]
	v_pk_mul_f32 v[8:9], v[32:33], v[8:9] op_sel_hi:[0,1]
.LBB0_320:
	v_sub_f32_e32 v100, v100, v110
	v_sub_f32_e32 v101, v101, v110
	v_sub_f32_e32 v102, v102, v110
	v_sub_f32_e32 v103, v103, v110
	v_sub_f32_e32 v104, v104, v110
	v_sub_f32_e32 v105, v105, v110
	v_sub_f32_e32 v106, v106, v110
	v_sub_f32_e32 v107, v107, v110
	v_exp_f32_e32 v100, v100
	v_exp_f32_e32 v101, v101
	v_exp_f32_e32 v102, v102
	v_exp_f32_e32 v103, v103
	v_exp_f32_e32 v104, v104
	v_exp_f32_e32 v105, v105
	v_exp_f32_e32 v106, v106
	v_exp_f32_e32 v107, v107
	v_add_u32_e32 v34, s16, v35
	v_add_u32_e32 v111, 0x229b8, v34
	v_cvt_pk_bf16_f32 v112, v100, v101
	v_cvt_pk_bf16_f32 v113, v102, v103
	v_cvt_pk_bf16_f32 v114, v104, v105
	v_cvt_pk_bf16_f32 v115, v106, v107
	v_add_u32_e32 v34, 0x229f8, v34
	ds_read_b128 v[134:137], v34
	s_waitcnt lgkmcnt(4)
	v_mfma_f32_16x16x32_bf16 v[20:23], v[96:99], v[112:115], v[20:23]
	s_waitcnt lgkmcnt(3)
	v_mfma_f32_16x16x32_bf16 v[16:19], v[92:95], v[112:115], v[16:19]
	s_waitcnt lgkmcnt(2)
	v_mfma_f32_16x16x32_bf16 v[12:15], v[88:91], v[112:115], v[12:15]
	s_waitcnt lgkmcnt(1)
	v_mfma_f32_16x16x32_bf16 v[8:11], v[84:87], v[112:115], v[8:11]
	ds_read_b128 v[112:115], v111
	s_waitcnt lgkmcnt(0)
	v_mfma_f32_16x16x32_bf16 v[52:55], v[52:55], v[24:27], v[112:115]
	v_mfma_f32_16x16x32_bf16 v[56:59], v[56:59], v[28:31], v[52:55]
	v_mfma_f32_16x16x32_bf16 v[52:55], v[60:63], v[24:27], v[134:137]
	v_mfma_f32_16x16x32_bf16 v[52:55], v[64:67], v[28:31], v[52:55]
	s_nop 5
	v_max_f32_e32 v34, v57, v57
	v_max_f32_e32 v60, v56, v56
	v_max_f32_e32 v34, v60, v34
	v_max_f32_e32 v60, v59, v59
	v_max_f32_e32 v61, v58, v58
	v_max_f32_e32 v60, v61, v60
	v_max_f32_e32 v61, v55, v55
	v_max_f32_e32 v62, v54, v54
	v_max_f32_e32 v61, v62, v61
	v_max3_f32 v61, v52, v53, v61
	v_max3_f32 v34, v34, v60, v61
	s_waitcnt lgkmcnt(0)
	v_mov_b32_e32 v60, v34
	s_nop 1
	v_permlane16_swap_b32_e32 v34, v60
	v_max_f32_e32 v60, v60, v60
	v_max_f32_e32 v34, v34, v60
	v_mov_b32_e32 v60, v34
	s_nop 1
	v_permlane32_swap_b32_e32 v34, v60
	v_max3_f32 v111, v118, v34, v60
	v_sub_f32_e32 v34, v118, v111
	v_exp_f32_e32 v34, v34
	s_nop 0
	v_cmp_neq_f32_e32 vcc, 1.0, v34
	s_cbranch_vccz .LBB0_322
	v_pk_mul_f32 v[50:51], v[34:35], v[50:51] op_sel_hi:[0,1]
	v_pk_mul_f32 v[48:49], v[34:35], v[48:49] op_sel_hi:[0,1]
	v_pk_mul_f32 v[46:47], v[34:35], v[46:47] op_sel_hi:[0,1]
	v_pk_mul_f32 v[44:45], v[34:35], v[44:45] op_sel_hi:[0,1]
	v_pk_mul_f32 v[42:43], v[34:35], v[42:43] op_sel_hi:[0,1]
	v_pk_mul_f32 v[40:41], v[34:35], v[40:41] op_sel_hi:[0,1]
	v_pk_mul_f32 v[38:39], v[34:35], v[38:39] op_sel_hi:[0,1]
	v_pk_mul_f32 v[36:37], v[34:35], v[36:37] op_sel_hi:[0,1]

; #define LAS __attribute__((address_space(3)))
; template <int NH, class InitF>
; __device__ __forceinline__ void attn_core(const bf16x8 (&kf)[2][2], const LAS unsigned char* vbuf, const InitF& initf  ,
;                                           const bf16x8 (&bq)[NH][2], float (&m)[NH], float (&l)[NH], f32x4 (&O)[NH][4], int lane) {
;     bf16x8 vf[4];
;     attn_vfrag(vbuf, vf, lane);
; #pragma unroll
;     for (int hq = 0; hq < NH; ++hq) {
;         f32x4 s0 = initf(hq, 0), s1 = initf(hq, 1);
;         s0 = __builtin_amdgcn_mfma_f32_16x16x32_bf16(kf[0][0], bq[hq][0], s0, 0, 0, 0); s0 = __builtin_amdgcn_mfma_f32_16x16x32_bf16(kf[0][1], bq[hq][1], s0, 0, 0, 0);
;         s1 = __builtin_amdgcn_mfma_f32_16x16x32_bf16(kf[1][0], bq[hq][0], s1, 0, 0, 0); s1 = __builtin_amdgcn_mfma_f32_16x16x32_bf16(kf[1][1], bq[hq][1], s1, 0, 0, 0);
;         float mx = fmaxf(fmaxf(fmaxf(s0[0], s0[1]), fmaxf(s0[2], s0[3])), fmaxf(fmaxf(s1[0], s1[1]), fmaxf(s1[2], s1[3])));
;         mx = fmaxf(mx, xor_sw<16>(mx)); mx = max_x32(mx);
;         const float mn = fmaxf(m[hq], mx), corr = __builtin_amdgcn_exp2f(m[hq] - mn); m[hq] = mn;
;         float p[8], ps = 0.f;
; #pragma unroll
;         for (int i = 0; i < 8; ++i) { p[i] = __builtin_amdgcn_exp2f((i < 4 ? s0[i & 3] : s1[i & 3]) - mn); ps += p[i]; }
;         l[hq] = l[hq] * corr + ps;
;         u32x4 pw; pw.x = cvt_pk_bf16(p[0], p[1]); pw.y = cvt_pk_bf16(p[2], p[3]); pw.z = cvt_pk_bf16(p[4], p[5]); pw.w = cvt_pk_bf16(p[6], p[7]);
;         const bf16x8 pb = __builtin_bit_cast(bf16x8, pw);
;         if (__builtin_amdgcn_ballot_w64(corr != 1.0f) != 0ull) {
; #pragma unroll
;             for (int mt = 0; mt < 4; ++mt) O[hq][mt] *= corr; }
; #pragma unroll
;         for (int mt = 0; mt < 4; ++mt) O[hq][mt] = __builtin_amdgcn_mfma_f32_16x16x32_bf16(vf[mt], pb, O[hq][mt], 0, 0, 0);
;     }
; template <int NH, int P, class Desc, class BiasF> ...
;     ...
;             attn_vwrite(vr[(u + 1) % P], vl + ((u + 1) & 1) * 5120, lane);
;             const TileD td = dsc(t);
;             if (td.valid) { const LAS unsigned char* bp[NH];
; #pragma unroll
;                 for (int hq = 0; hq < NH; ++hq) bp[hq] = biasf(td, hq);
;                 auto initf = [&](int hq, int hh) { return *(const LAS f32x4*)(bp[hq] + 64 * hh); };
;                 attn_core<NH>(kf[u % P], vl + (u & 1) * 5120, initf, bq, m, l, O, lane); }
.LBB0_329:
	s_add_i32 s14, s30, 0xffffff80
	s_cmpk_gt_u32 s14, 0x7ff
	s_waitcnt vmcnt(3)
	ds_write_b128 v187, v[92:95]
	s_waitcnt vmcnt(2)
	ds_write_b128 v188, v[84:87]
	s_waitcnt vmcnt(1)
	ds_write_b128 v189, v[88:91]
	s_waitcnt vmcnt(0)
	ds_write_b128 v190, v[96:99]
	s_cbranch_scc1 .LBB0_335
	v_add_u32_e32 v32, 0x22a40, v109
	ds_read_b128 v[84:87], v32
	v_add_u32_e32 v32, 0x22a80, v109
	ds_read_b128 v[88:91], v32
	s_waitcnt lgkmcnt(1)
	v_mfma_f32_16x16x32_bf16 v[84:87], v[72:75], v[0:3], v[84:87]
	s_waitcnt lgkmcnt(0)
	v_mfma_f32_16x16x32_bf16 v[88:91], v[76:79], v[0:3], v[88:91]
	v_mfma_f32_16x16x32_bf16 v[100:103], v[68:71], v[4:7], v[84:87]
	v_mfma_f32_16x16x32_bf16 v[104:107], v[80:83], v[4:7], v[88:91]
	s_nop 6
	v_max_f32_e32 v32, v101, v101
	v_max_f32_e32 v34, v100, v100
	v_max_f32_e32 v84, v103, v103
	v_max_f32_e32 v85, v102, v102
	v_max_f32_e32 v86, v107, v107
	v_max_f32_e32 v87, v106, v106
	v_max_f32_e32 v32, v34, v32
	v_max_f32_e32 v34, v85, v84
	v_max_f32_e32 v84, v87, v86
	v_max3_f32 v84, v104, v105, v84
	v_max3_f32 v32, v32, v34, v84
	ds_read_b64_tr_b16 v[96:97], v191 offset:5120
	ds_read_b64_tr_b16 v[92:93], v191 offset:5152
	ds_read_b64_tr_b16 v[88:89], v191 offset:5184
	ds_read_b64_tr_b16 v[84:85], v191 offset:5216
	ds_read_b64_tr_b16 v[98:99], v191 offset:7680
	ds_read_b64_tr_b16 v[94:95], v191 offset:7712
	ds_read_b64_tr_b16 v[90:91], v191 offset:7744
	ds_read_b64_tr_b16 v[86:87], v191 offset:7776
	s_waitcnt lgkmcnt(8)
	v_mov_b32_e32 v34, v32
	s_nop 1
	v_permlane16_swap_b32_e32 v32, v34
	v_max_f32_e32 v34, v34, v34
	v_max_f32_e32 v32, v32, v34
	v_mov_b32_e32 v34, v32
	s_nop 1
	v_permlane32_swap_b32_e32 v32, v34
	v_max3_f32 v116, v110, v32, v34
	v_sub_f32_e32 v32, v110, v116
	v_exp_f32_e32 v32, v32
	s_nop 0
	v_cmp_neq_f32_e32 vcc, 1.0, v32
	s_cbranch_vccz .LBB0_332
	v_pk_mul_f32 v[22:23], v[22:23], v[32:33] op_sel_hi:[1,0]
	v_pk_mul_f32 v[20:21], v[20:21], v[32:33] op_sel_hi:[1,0]
	v_pk_mul_f32 v[18:19], v[32:33], v[18:19] op_sel_hi:[0,1]
	v_pk_mul_f32 v[16:17], v[32:33], v[16:17] op_sel_hi:[0,1]
	v_pk_mul_f32 v[14:15], v[32:33], v[14:15] op_sel_hi:[0,1]
	v_pk_mul_f32 v[12:13], v[32:33], v[12:13] op_sel_hi:[0,1]
	v_pk_mul_f32 v[10:11], v[32:33], v[10:11] op_sel_hi:[0,1]
	v_pk_mul_f32 v[8:9], v[32:33], v[8:9] op_sel_hi:[0,1]
.LBB0_332:
	v_sub_f32_e32 v100, v100, v116
	v_sub_f32_e32 v101, v101, v116
	v_sub_f32_e32 v102, v102, v116
	v_sub_f32_e32 v103, v103, v116
	v_sub_f32_e32 v104, v104, v116
	v_sub_f32_e32 v105, v105, v116
	v_sub_f32_e32 v106, v106, v116
	v_sub_f32_e32 v107, v107, v116
	v_exp_f32_e32 v100, v100
	v_exp_f32_e32 v101, v101
	v_exp_f32_e32 v102, v102
	v_exp_f32_e32 v103, v103
	v_exp_f32_e32 v104, v104
	v_exp_f32_e32 v105, v105
	v_exp_f32_e32 v106, v106
	v_exp_f32_e32 v107, v107
	v_add_u32_e32 v34, s16, v35
	v_add_u32_e32 v109, 0x22a38, v34
	v_cvt_pk_bf16_f32 v112, v100, v101
	v_cvt_pk_bf16_f32 v113, v102, v103
	v_cvt_pk_bf16_f32 v114, v104, v105
	v_cvt_pk_bf16_f32 v115, v106, v107
	v_add_u32_e32 v34, 0x22a78, v34
	ds_read_b128 v[134:137], v34
	s_waitcnt lgkmcnt(4)
	v_mfma_f32_16x16x32_bf16 v[20:23], v[96:99], v[112:115], v[20:23]
	s_waitcnt lgkmcnt(3)
	v_mfma_f32_16x16x32_bf16 v[16:19], v[92:95], v[112:115], v[16:19]
	s_waitcnt lgkmcnt(2)
	v_mfma_f32_16x16x32_bf16 v[12:15], v[88:91], v[112:115], v[12:15]
	s_waitcnt lgkmcnt(1)
	v_mfma_f32_16x16x32_bf16 v[8:11], v[84:87], v[112:115], v[8:11]
	ds_read_b128 v[112:115], v109
	s_waitcnt lgkmcnt(0)
	v_mfma_f32_16x16x32_bf16 v[72:75], v[72:75], v[24:27], v[112:115]
	v_mfma_f32_16x16x32_bf16 v[72:75], v[68:71], v[28:31], v[72:75]
	v_mfma_f32_16x16x32_bf16 v[68:71], v[76:79], v[24:27], v[134:137]
	v_mfma_f32_16x16x32_bf16 v[68:71], v[80:83], v[28:31], v[68:71]
	s_nop 5
	v_max_f32_e32 v34, v73, v73
	v_max_f32_e32 v76, v72, v72
	v_max_f32_e32 v34, v76, v34
	v_max_f32_e32 v76, v75, v75
	v_max_f32_e32 v77, v74, v74
	v_max_f32_e32 v76, v77, v76
	v_max_f32_e32 v77, v71, v71
	v_max_f32_e32 v78, v70, v70
	v_max_f32_e32 v77, v78, v77
	v_max3_f32 v77, v68, v69, v77
	v_max3_f32 v34, v34, v76, v77
	s_waitcnt lgkmcnt(0)
	v_mov_b32_e32 v76, v34
	s_nop 1
	v_permlane16_swap_b32_e32 v34, v76
	v_max_f32_e32 v76, v76, v76
	v_max_f32_e32 v34, v34, v76
	v_mov_b32_e32 v76, v34
	s_nop 1
	v_permlane32_swap_b32_e32 v34, v76
	v_max3_f32 v118, v111, v34, v76
	v_sub_f32_e32 v34, v111, v118
	v_exp_f32_e32 v34, v34
	s_nop 0
	v_cmp_neq_f32_e32 vcc, 1.0, v34
	s_cbranch_vccz .LBB0_334
	v_pk_mul_f32 v[50:51], v[34:35], v[50:51] op_sel_hi:[0,1]
	v_pk_mul_f32 v[48:49], v[34:35], v[48:49] op_sel_hi:[0,1]
	v_pk_mul_f32 v[46:47], v[34:35], v[46:47] op_sel_hi:[0,1]
	v_pk_mul_f32 v[44:45], v[34:35], v[44:45] op_sel_hi:[0,1]
	v_pk_mul_f32 v[42:43], v[34:35], v[42:43] op_sel_hi:[0,1]
	v_pk_mul_f32 v[40:41], v[34:35], v[40:41] op_sel_hi:[0,1]
	v_pk_mul_f32 v[38:39], v[34:35], v[38:39] op_sel_hi:[0,1]
	v_pk_mul_f32 v[36:37], v[34:35], v[36:37] op_sel_hi:[0,1]

; #define LAS __attribute__((address_space(3)))
; __device__ __forceinline__ bf16x8 attn_sh_load(const char* kp_base, const char* vp_base, int kb, int tid, int r) {
;     kb = kb < 0 ? 0 : (kb > SEQ - 64 ? SEQ - 64 : kb);
;     const int row = 32 * r + ((tid & 255) >> 3), cc = tid & 7; const int kp = kb + row;
;     return ld16((tid >> 8) ? vp_base : kp_base, (unsigned)kp * (unsigned)(ODD_IN * 2) + 16u * cc);
; }
; template <int NH, int NQ, bool TABLE> ...
;     const int g = lane >> 4;
;     int iq[NQ];
; #pragma unroll
;     for (int q = 0; q < NQ; ++q) iq[q] = 4 * g - (int)fqp[q];
;     bf16x8 ra[2];
; #pragma unroll
; __global__ void __launch_bounds__(NWAVES * 64, 2) mk_fwd(Args args) {
;     ...
;                         bf16x8 qraw[2][2];
; #pragma unroll
;                         for (int sl = 0; sl < 2; ++sl) { const bf16_t* qr = hb + (size_t)(256 * ib + 32 * wave + 16 * sl + c) * ODD_IN + h * 64 + 8 * g; qraw[sl][0] = *(const bf16x8*)qr; qraw[sl][1] = *(const bf16x8*)(qr + 32); }
;                         __syncthreads();
;                         {   LAS float* PARK = (LAS float*)lds;
; #pragma unroll
;                             for (int q = 0; q < 2; ++q) { float lt = l[q]; lt += xor_sw<16>(lt); lt = sum_x32(lt);
;                                 const int pp = wave + 8 * q + 16 * c;
; #pragma unroll
;                                 for (int mt = 0; mt < 4; ++mt) *(LAS f32x4*)(PARK + pp * 68 + 4 * ((4 * mt + g) ^ c)) = O[q][mt];
;                                 if (g == 0) { PARK[pp * 68 + 64] = m[q]; PARK[pp * 68 + 65] = lt; } }
;                             const LAS unsigned char* t1[2];
; #pragma unroll
;                             for (int sl = 0; sl < 2; ++sl) { const int qp = 256 * ib + 32 * wave + 16 * sl + c;
;                                 bq[sl][0] = q_prescale(qraw[sl][0]); bq[sl][1] = q_prescale(qraw[sl][1]);
;                                 m[sl] = -1e30f; l[sl] = 0.f; fq2[sl] = (float)qp;
; #pragma unroll
;                                 for (int mt = 0; mt < 4; ++mt) O[sl][mt] = (f32x4){0.f, 0.f, 0.f, 0.f};
;                                 t1[sl] = (const LAS unsigned char*)TAB1 + 2592 * (c & 3) + 4 * (320 + (c & 3) + 4 * g - qp); }
;                             attn_stream<2, 2, true>(kpb, vpb, 256 * ib - 64, 6, 64.f, fq2, t1, slope22, bq, m, l, O, sh, tid, lane, wave >> 1, (wave >> 1) + 2);
.LBB0_340:
	v_readlane_b32 s10, v253, 18
	s_add_i32 s10, s29, s10
	v_lshl_add_u64 v[0:1], v[130:131], 1, s[8:9]
	v_add_u32_e32 v4, s10, v193
	v_mad_i64_i32 v[2:3], s[10:11], v4, s50, v[0:1]
	global_load_dwordx4 v[24:27], v[2:3], off
	global_load_dwordx4 v[28:31], v[2:3], off offset:64
	v_add_u32_e32 v2, 16, v4
	v_mad_i64_i32 v[0:1], s[10:11], v2, s50, v[0:1]
	global_load_dwordx4 v[4:7], v[0:1], off
	s_nop 0
	global_load_dwordx4 v[0:3], v[0:1], off offset:64
	s_movk_i32 s10, 0x110
	v_xor_b32_e32 v34, v192, v193
	v_lshlrev_b32_e32 v34, 4, v34
	s_waitcnt vmcnt(4)
	v_add_u32_e32 v98, 4, v192
	s_waitcnt lgkmcnt(0)
	v_mov_b32_e32 v32, v119
	s_nop 1
	v_permlane16_swap_b32_e32 v119, v32
	v_add_f32_e32 v35, v119, v32
	v_mul_lo_u32 v32, v117, s10
	v_add_u32_e32 v32, 0, v32
	v_add_u32_e32 v34, v32, v34
	s_barrier
	ds_write_b128 v34, v[20:23]
	v_xor_b32_e32 v20, v98, v193
	v_lshlrev_b32_e32 v20, 4, v20
	v_add_u32_e32 v20, v32, v20
	v_add_u32_e32 v97, 8, v192
	ds_write_b128 v20, v[16:19]
	v_xor_b32_e32 v16, v97, v193
	v_lshlrev_b32_e32 v16, 4, v16
	v_add_u32_e32 v16, v32, v16
	v_add_u32_e32 v96, 12, v192
	ds_write_b128 v16, v[12:15]
	v_xor_b32_e32 v12, v96, v193
	v_mov_b32_e32 v52, v35
	v_lshlrev_b32_e32 v12, 4, v12
	v_cmp_eq_u32_e32 vcc, 0, v192
	v_permlane32_swap_b32_e32 v35, v52
	v_add_u32_e32 v12, v32, v12
	ds_write_b128 v12, v[8:11]
	s_and_saveexec_b64 s[10:11], vcc
	v_add_f32_e32 v117, v35, v52
	ds_write_b64 v32, v[116:117] offset:256
	s_or_b64 exec, exec, s[10:11]
	ds_write_b128 v34, v[48:51] offset:2176
	ds_write_b128 v20, v[44:47] offset:2176
	ds_write_b128 v16, v[40:43] offset:2176
	ds_write_b128 v12, v[36:39] offset:2176
	s_waitcnt lgkmcnt(4)
	v_mov_b32_e32 v8, v133
	s_nop 1
	v_permlane16_swap_b32_e32 v133, v8
	v_add_f32_e32 v8, v133, v8
	v_mov_b32_e32 v9, v8
	s_nop 1
	v_permlane32_swap_b32_e32 v8, v9
	s_and_saveexec_b64 s[10:11], vcc
	v_add_f32_e32 v119, v8, v9
	ds_write_b64 v32, v[118:119] offset:2432
	s_or_b64 exec, exec, s[10:11]
	s_add_u32 s10, s8, 0x400
	s_addc_u32 s11, s9, 0
	s_add_u32 s8, s8, 0x800
	s_addc_u32 s9, s9, 0
	s_sub_i32 s12, s29, 64
	v_mov_b32_e32 v8, 0x7c0
	v_med3_i32 v8, s12, 0, v8
	v_or_b32_e32 v10, v8, v156
	v_mov_b32_e32 v8, s9
	v_mov_b32_e32 v9, s11
	v_cndmask_b32_e64 v93, v8, v9, s[4:5]
	v_mov_b32_e32 v8, s8
	v_mov_b32_e32 v9, s10
	v_cndmask_b32_e64 v92, v8, v9, s[4:5]
	v_mul_u32_u24_e32 v8, 0x1200, v10
	s_mov_b32 s10, 0x3e38aa3b
	s_waitcnt vmcnt(3)
	v_lshlrev_b32_e32 v20, 16, v26
	v_and_b32_e32 v21, 0xffff0000, v26
	v_or_b32_e32 v32, v8, v157
	v_pk_mul_f32 v[34:35], v[20:21], s[10:11] op_sel_hi:[1,0]
	v_lshlrev_b32_e32 v20, 16, v27
	v_and_b32_e32 v21, 0xffff0000, v27
	v_or_b32_e32 v22, s29, v156
	v_lshl_add_u64 v[8:9], v[92:93], 0, v[32:33]
	v_mad_u32_u24 v32, v10, s50, v158
	v_pk_mul_f32 v[36:37], v[20:21], s[10:11] op_sel_hi:[1,0]
	v_mul_u32_u24_e32 v20, 0x1200, v22
	v_lshl_add_u64 v[12:13], v[92:93], 0, v[32:33]
	v_or_b32_e32 v32, v20, v157
	global_load_dwordx4 v[8:11], v[8:9], off
	s_nop 0
	global_load_dwordx4 v[12:15], v[12:13], off
	v_lshl_add_u64 v[20:21], v[92:93], 0, v[32:33]
	v_mad_u32_u24 v32, v22, s50, v158
	v_lshlrev_b32_e32 v16, 16, v24
	v_and_b32_e32 v17, 0xffff0000, v24
	v_lshlrev_b32_e32 v18, 16, v25
	v_and_b32_e32 v19, 0xffff0000, v25
	v_lshl_add_u64 v[24:25], v[92:93], 0, v[32:33]
	global_load_dwordx4 v[20:23], v[20:21], off
	s_nop 0
	global_load_dwordx4 v[24:27], v[24:25], off
	v_pk_mul_f32 v[16:17], v[16:17], s[10:11] op_sel_hi:[1,0]
	v_pk_mul_f32 v[18:19], v[18:19], s[10:11] op_sel_hi:[1,0]
	v_cvt_pk_bf16_f32 v16, v16, v17
	v_cvt_pk_bf16_f32 v17, v18, v19
	v_cvt_pk_bf16_f32 v18, v34, v35
	s_waitcnt vmcnt(6)
	v_lshlrev_b32_e32 v34, 16, v28
	v_and_b32_e32 v35, 0xffff0000, v28
	v_lshlrev_b32_e32 v28, 16, v29
	v_and_b32_e32 v29, 0xffff0000, v29
	v_cvt_pk_bf16_f32 v19, v36, v37
	v_pk_mul_f32 v[36:37], v[28:29], s[10:11] op_sel_hi:[1,0]
	v_lshlrev_b32_e32 v28, 16, v30
	v_and_b32_e32 v29, 0xffff0000, v30
	v_pk_mul_f32 v[34:35], v[34:35], s[10:11] op_sel_hi:[1,0]
	v_pk_mul_f32 v[38:39], v[28:29], s[10:11] op_sel_hi:[1,0]
	v_lshlrev_b32_e32 v28, 16, v31
	v_and_b32_e32 v29, 0xffff0000, v31
	v_pk_mul_f32 v[40:41], v[28:29], s[10:11] op_sel_hi:[1,0]
	v_cvt_pk_bf16_f32 v28, v34, v35
	s_waitcnt vmcnt(5)
	v_lshlrev_b32_e32 v34, 16, v4
	v_and_b32_e32 v35, 0xffff0000, v4
	v_lshlrev_b32_e32 v4, 16, v5
	v_and_b32_e32 v5, 0xffff0000, v5
	v_pk_mul_f32 v[34:35], v[34:35], s[10:11] op_sel_hi:[1,0]
	v_pk_mul_f32 v[4:5], v[4:5], s[10:11] op_sel_hi:[1,0]
	v_cvt_pk_bf16_f32 v29, v36, v37
	v_lshlrev_b32_e32 v36, 16, v6
	v_and_b32_e32 v37, 0xffff0000, v6
	v_lshlrev_b32_e32 v6, 16, v7
	v_and_b32_e32 v7, 0xffff0000, v7
	v_cvt_pk_bf16_f32 v34, v34, v35
	v_cvt_pk_bf16_f32 v35, v4, v5
	s_waitcnt vmcnt(4)
	v_lshlrev_b32_e32 v4, 16, v0
	v_and_b32_e32 v5, 0xffff0000, v0
	v_lshlrev_b32_e32 v0, 16, v1
	v_and_b32_e32 v1, 0xffff0000, v1
	v_pk_mul_f32 v[36:37], v[36:37], s[10:11] op_sel_hi:[1,0]
	v_pk_mul_f32 v[6:7], v[6:7], s[10:11] op_sel_hi:[1,0]
	v_pk_mul_f32 v[0:1], v[0:1], s[10:11] op_sel_hi:[1,0]
	v_mul_u32_u24_e32 v42, 0xa20, v120
	v_cvt_pk_bf16_f32 v30, v38, v39
	v_cvt_pk_bf16_f32 v36, v36, v37
	v_cvt_pk_bf16_f32 v37, v6, v7
	v_lshlrev_b32_e32 v6, 16, v2
	v_and_b32_e32 v7, 0xffff0000, v2
	v_lshlrev_b32_e32 v2, 16, v3
	v_and_b32_e32 v3, 0xffff0000, v3
	v_cvt_pk_bf16_f32 v39, v0, v1
	v_lshlrev_b32_e32 v0, 2, v120
	v_pk_mul_f32 v[2:3], v[2:3], s[10:11] op_sel_hi:[1,0]
	v_add3_u32 v0, v42, v121, v0
	v_lshlrev_b32_e32 v1, 2, v193
	v_cvt_pk_bf16_f32 v31, v40, v41
	v_pk_mul_f32 v[4:5], v[4:5], s[10:11] op_sel_hi:[1,0]
	v_pk_mul_f32 v[6:7], v[6:7], s[10:11] op_sel_hi:[1,0]
	v_cvt_pk_bf16_f32 v41, v2, v3
	v_sub_u32_e32 v0, v0, v1
	v_readlane_b32 s10, v255, 34
	v_mov_b32_e32 v2, v33
	v_mov_b32_e32 v3, v33
	v_cvt_pk_bf16_f32 v38, v4, v5
	v_cvt_pk_bf16_f32 v40, v6, v7
	s_waitcnt vmcnt(3)
	ds_write_b128 v196, v[8:11]
	s_waitcnt vmcnt(2)
	ds_write_b128 v197, v[12:15]
	v_add_u32_e32 v100, s10, v0
	v_mov_b32_e32 v32, v33
	v_mov_b32_e32 v0, v33
	v_mov_b32_e32 v1, v33
	v_mov_b64_e32 v[6:7], v[2:3]
	v_mov_b64_e32 v[10:11], v[2:3]
	v_mov_b64_e32 v[14:15], v[2:3]
	v_mov_b64_e32 v[44:45], v[2:3]
	v_mov_b64_e32 v[48:49], v[2:3]
	v_mov_b64_e32 v[52:53], v[2:3]
	v_mov_b64_e32 v[56:57], v[2:3]
	s_add_i32 s8, s17, 64
	s_mov_b32 s9, 0
	v_mov_b32_e32 v94, 0xf149f2ca
	v_mov_b32_e32 v95, 0xf149f2ca
	v_mov_b64_e32 v[4:5], v[0:1]
	v_mov_b64_e32 v[8:9], v[0:1]
	v_mov_b64_e32 v[12:13], v[0:1]
	v_mov_b64_e32 v[42:43], v[0:1]
	v_mov_b64_e32 v[46:47], v[0:1]
	v_mov_b64_e32 v[50:51], v[0:1]
	v_mov_b64_e32 v[54:55], v[0:1]
	s_mov_b32 s10, 0
	v_mov_b64_e32 v[90:91], v[32:33]
	s_waitcnt lgkmcnt(0)
	s_barrier
; template <int NH, class InitF>
; __device__ __forceinline__ void attn_core64(const LAS unsigned char* kbuf  , const LAS unsigned char* vbuf  , const InitF& initf  ,
;                                             const bf16x8 (&bq)[NH][2], float (&m)[NH], float (&l)[NH], f32x4 (&O)[NH][4], int lane) {
;     const int c = lane & 15, g = lane >> 4;
;     bf16x8 pb[NH][2]; float corr[NH];
; #pragma unroll
;     for (int hq = 0; hq < NH; ++hq) {
;         f32x4 sa[4];
; #pragma unroll
;         for (int t = 0; t < 4; ++t) sa[t] = initf(hq, t);
; #pragma unroll
;         for (int t = 0; t < 4; ++t) { const bf16x8 k0 = *(const LAS bf16x8*)(kbuf + (16 * t + c) * 144 + 16 * g), k1 = *(const LAS bf16x8*)(kbuf + (16 * t + c) * 144 + 16 * g + 64);
;             sa[t] = __builtin_amdgcn_mfma_f32_16x16x32_bf16(k0, bq[hq][0], sa[t], 0, 0, 0); sa[t] = __builtin_amdgcn_mfma_f32_16x16x32_bf16(k1, bq[hq][1], sa[t], 0, 0, 0); }
;         float mx = -3.0e38f;
; #pragma unroll
;         for (int t = 0; t < 4; ++t) mx = fmaxf(mx, fmaxf(fmaxf(sa[t][0], sa[t][1]), fmaxf(sa[t][2], sa[t][3])));
;         mx = fmaxf(mx, xor_sw<16>(mx)); mx = max_x32(mx);
;         const float mn = fmaxf(m[hq], mx); corr[hq] = __builtin_amdgcn_exp2f(m[hq] - mn); m[hq] = mn;
;         float p[16], ps = 0.f;
; #pragma unroll
;         for (int i = 0; i < 16; ++i) { p[i] = __builtin_amdgcn_exp2f(sa[i >> 2][i & 3] - mn); ps += p[i]; }
;         l[hq] = l[hq] * corr[hq] + ps;
;         u32x4 pw0, pw1;
;         pw0.x = cvt_pk_bf16(p[0], p[1]); pw0.y = cvt_pk_bf16(p[2], p[3]); pw0.z = cvt_pk_bf16(p[4], p[5]); pw0.w = cvt_pk_bf16(p[6], p[7]);
;         pw1.x = cvt_pk_bf16(p[8], p[9]); pw1.y = cvt_pk_bf16(p[10], p[11]); pw1.z = cvt_pk_bf16(p[12], p[13]); pw1.w = cvt_pk_bf16(p[14], p[15]);
;         pb[hq][0] = __builtin_bit_cast(bf16x8, pw0); pb[hq][1] = __builtin_bit_cast(bf16x8, pw1);
;     }
; #pragma unroll
;     for (int hq = 0; hq < NH; ++hq) {
;         if (__builtin_amdgcn_ballot_w64(corr[hq] != 1.0f) != 0ull) {
; #pragma unroll
;             for (int mt = 0; mt < 4; ++mt) O[hq][mt] *= corr[hq]; } }
; template <int NH, int NQ, bool TABLE> ...
;     ...
;     for (int j = 0; j < ntile; ++j) {
;         const int kb = kb0 + 64 * j; LAS unsigned char* buf = sh + (j & 1) * SH_BUF;
;         if (j >= jlo && j <= jhi && !(kb + 63 < 0 || kb >= SEQ)) {
;             if constexpr (TABLE) {
.LBB0_345:
	s_cmp_lt_u32 s10, s56
	s_cselect_b64 s[12:13], -1, 0
	s_cmp_gt_u32 s10, s38
	s_cselect_b64 s[14:15], -1, 0
	s_add_i32 s11, s8, 0xfffff780
	s_cmp_lt_u32 s11, 0xfffff7c1
	s_cselect_b64 s[16:17], -1, 0
	s_or_b64 s[12:13], s[12:13], s[16:17]
	s_or_b64 s[12:13], s[12:13], s[14:15]
	s_and_b64 vcc, exec, s[12:13]
	s_cbranch_vccnz .LBB0_351
	s_bitcmp1_b32 s10, 0
	s_cselect_b32 s11, 0x4c00, 0
	s_add_i32 s11, s11, 0
	s_add_i32 s11, s11, 0x14000
	v_add3_u32 v32, s11, v126, v161
	ds_read_b128 v[58:61], v32
	v_add_u32_e32 v82, s9, v100
	v_add_u32_e32 v62, 0x20440, v82
	ds_read_b128 v[62:65], v62
	v_add_u32_e32 v70, 0x20400, v82
	v_add_u32_e32 v71, 0x20500, v82
	ds_read_b128 v[66:69], v32 offset:64
	ds_read_b128 v[74:77], v70
	ds_read_b128 v[70:73], v71
	ds_read_b128 v[102:105], v32 offset:2304
	ds_read_b128 v[110:113], v32 offset:2368
	s_waitcnt lgkmcnt(5)
	v_mfma_f32_16x16x32_bf16 v[78:81], v[58:61], v[16:19], v[62:65]
	v_add_u32_e32 v83, 0x20480, v82
	ds_read_b128 v[106:109], v83
	ds_read_b128 v[118:121], v32 offset:4608
	ds_read_b128 v[130:133], v32 offset:4672
	ds_read_b128 v[134:137], v32 offset:6912
	ds_read_b128 v[138:141], v32 offset:6976
	s_waitcnt lgkmcnt(9)
	v_mfma_f32_16x16x32_bf16 v[86:89], v[66:69], v[28:31], v[78:81]
	s_nop 2
	v_add_u32_e32 v78, 0x204c0, v82
	ds_read_b128 v[114:117], v78
	s_waitcnt lgkmcnt(5)
	v_mfma_f32_16x16x32_bf16 v[78:81], v[102:105], v[16:19], v[106:109]
	s_nop 0
	v_max_f32_e32 v32, v89, v89
	v_max_f32_e32 v99, v88, v88
	v_max_f32_e32 v32, v99, v32
	v_mfma_f32_16x16x32_bf16 v[82:85], v[110:113], v[28:31], v[78:81]
	v_max3_f32 v32, v86, v87, v32
	s_waitcnt lgkmcnt(0)
	v_mfma_f32_16x16x32_bf16 v[78:81], v[118:121], v[16:19], v[114:117]
	v_mfma_f32_16x16x32_bf16 v[70:73], v[134:137], v[16:19], v[70:73]
	s_nop 3
	v_max_f32_e32 v99, v85, v85
	v_max_f32_e32 v101, v84, v84
	v_mfma_f32_16x16x32_bf16 v[58:61], v[58:61], v[34:37], v[74:77]
	v_mfma_f32_16x16x32_bf16 v[78:81], v[130:133], v[28:31], v[78:81]
	v_mfma_f32_16x16x32_bf16 v[70:73], v[138:141], v[28:31], v[70:73]
	v_mfma_f32_16x16x32_bf16 v[74:77], v[66:69], v[38:41], v[58:61]
	s_nop 4
	v_max_f32_e32 v58, v101, v99
	v_max3_f32 v58, v82, v83, v58
	v_max3_f32 v32, v32, s96, v58
	v_mfma_f32_16x16x32_bf16 v[58:61], v[102:105], v[34:37], v[62:65]
	v_max_f32_e32 v67, v73, v73
	v_max_f32_e32 v68, v72, v72
	v_max_f32_e32 v67, v68, v67
	v_max_f32_e32 v62, v81, v81
	v_max_f32_e32 v63, v80, v80
	v_max_f32_e32 v62, v63, v62
	v_max3_f32 v66, v78, v79, v62
	v_max3_f32 v67, v70, v71, v67
	v_max3_f32 v32, v32, v66, v67
	v_mfma_f32_16x16x32_bf16 v[62:65], v[118:121], v[34:37], v[106:109]
	v_max_f32_e32 v101, v77, v77
	v_max_f32_e32 v102, v76, v76
	v_max_f32_e32 v101, v102, v101
	v_mfma_f32_16x16x32_bf16 v[58:61], v[110:113], v[38:41], v[58:61]
	s_waitcnt lgkmcnt(0)
	v_mov_b32_e32 v66, v32
	s_nop 1
	v_permlane16_swap_b32_e32 v32, v66
	v_max_f32_e32 v99, v66, v66
	v_max3_f32 v101, v74, v75, v101
	v_max_f32_e32 v32, v32, v99
	v_mfma_f32_16x16x32_bf16 v[66:69], v[134:137], v[34:37], v[114:117]
	v_mov_b32_e32 v99, v32
	s_nop 1
	v_max_f32_e32 v102, v61, v61
	v_max_f32_e32 v103, v60, v60
	v_mfma_f32_16x16x32_bf16 v[62:65], v[130:133], v[38:41], v[62:65]
	v_max_f32_e32 v102, v103, v102
	v_max3_f32 v102, v58, v59, v102
	v_max3_f32 v101, v101, s96, v102
	v_mfma_f32_16x16x32_bf16 v[66:69], v[138:141], v[38:41], v[66:69]
	v_permlane32_swap_b32_e32 v32, v99
	s_nop 2
	v_max_f32_e32 v102, v65, v65
	v_max_f32_e32 v103, v64, v64
	v_max_f32_e32 v102, v103, v102
	s_nop 0
	v_max_f32_e32 v103, v69, v69
	v_max_f32_e32 v104, v68, v68
	v_max_f32_e32 v103, v104, v103
	v_max3_f32 v102, v62, v63, v102
	v_max3_f32 v103, v66, v67, v103
	v_max3_f32 v102, v101, v102, v103
	v_max3_f32 v101, v95, v32, v99
	v_sub_f32_e32 v32, v95, v101
	v_exp_f32_e32 v95, v32
	s_waitcnt lgkmcnt(0)
	v_mov_b32_e32 v103, v102
	s_nop 1
	v_permlane16_swap_b32_e32 v102, v103
	v_max_f32_e32 v32, v103, v103
	v_max_f32_e32 v32, v102, v32
	v_mov_b32_e32 v99, v32
	s_nop 1
	v_permlane32_swap_b32_e32 v32, v99
	v_cmp_neq_f32_e32 vcc, 1.0, v95
	s_cbranch_vccz .LBB0_348
	v_mov_b32_e32 v102, v95
	v_pk_mul_f32 v[56:57], v[102:103], v[56:57] op_sel_hi:[0,1]
	v_pk_mul_f32 v[54:55], v[102:103], v[54:55] op_sel_hi:[0,1]
	v_pk_mul_f32 v[52:53], v[102:103], v[52:53] op_sel_hi:[0,1]
	v_pk_mul_f32 v[50:51], v[102:103], v[50:51] op_sel_hi:[0,1]
	v_pk_mul_f32 v[48:49], v[102:103], v[48:49] op_sel_hi:[0,1]
	v_pk_mul_f32 v[46:47], v[102:103], v[46:47] op_sel_hi:[0,1]
	v_pk_mul_f32 v[44:45], v[102:103], v[44:45] op_sel_hi:[0,1]
	v_pk_mul_f32 v[42:43], v[102:103], v[42:43] op_sel_hi:[0,1]

; #define LAS __attribute__((address_space(3)))
; __device__ __forceinline__ void unpack8(const u32x4 w, float (&f)[8]) { f[0] = bf_lo(w.x); f[1] = bf_hi(w.x); f[2] = bf_lo(w.y); f[3] = bf_hi(w.y); f[4] = bf_lo(w.z); f[5] = bf_hi(w.z); f[6] = bf_lo(w.w); f[7] = bf_hi(w.w); }
; __device__ __forceinline__ u32x4 pack8(const float (&f)[8]) { u32x4 o; o.x = cvt_pk_bf16(f[0], f[1]); o.y = cvt_pk_bf16(f[2], f[3]); o.z = cvt_pk_bf16(f[4], f[5]); o.w = cvt_pk_bf16(f[6], f[7]); return o; }
; #define PHASE_IDS() int lane = lane_id(); asm volatile("" : "+v"(lane)); const int wave = wave_s, tid = wave_s * 64 + lane, gw = vcu * NWAVES + wave; (void)tid; (void)gw
; __global__ void __launch_bounds__(NWAVES * 64, 2) mk_fwd(Args args) {
;     ...
;             PHASE_IDS();
;             constexpr int XS = 1028;
;             LAS float* XL = (LAS float*)lds;
;             LAS float* PART = (LAS float*)(lds + 65792);
;             LAS float* LOG = (LAS float*)(lds + 82176);
;             LAS int* LCNT = (LAS int*)(lds + 84224);
;             LAS int* GBASE = (LAS int*)(lds + 84352);
;             LAS i32x4* REC = (LAS i32x4*)(lds + 84480);
;             LAS float* TSC = (LAS float*)(lds + 122880);
;             LAS float* TOP = (LAS float*)(lds + 124928);
;             const float* lng = args.in[15] + (size_t)(layer * 2 + 0) * D; const float* lnb = args.in[16] + (size_t)(layer * 2 + 0) * D;
;             const float* rw = args.in[9] + (size_t)layer * D * NEXP; const float* rb = args.in[10] + layer * NEXP;
;             if (tid < 32) LCNT[tid] = 0;
;             __syncthreads();
;             const int tk = lane & 15, kq = lane >> 4;
;             auto split8 = [](const float (&f)[8], bf16x8& hi, bf16x8& lo) { const u32x4 h = pack8(f); float fh[8], fl[8]; unpack8(h, fh);
; #pragma unroll
;                 for (int i = 0; i < 8; ++i) fl[i] = f[i] - fh[i];
;                 hi = __builtin_bit_cast(bf16x8, h); lo = __builtin_bit_cast(bf16x8, pack8(fl)); };
;             bf16x8 rwh[4][2], rwl[4][2];
; #pragma unroll
;             for (int ks = 0; ks < 4; ++ks)
; #pragma unroll
;                 for (int tile = 0; tile < 2; ++tile) { float f[8];
; #pragma unroll
;                     for (int j = 0; j < 8; ++j) f[j] = rw[(size_t)(128 * wave + 32 * ks + 8 * kq + j) * NEXP + 16 * tile + tk];
;                     split8(f, rwh[ks][tile], rwl[ks][tile]); }
.LBB0_481:
	s_mov_b32 s2, -1
	s_waitcnt lgkmcnt(0)
	s_barrier
	s_nop 0
	v_mbcnt_lo_u32_b32 v0, s2, 0
	v_mbcnt_hi_u32_b32 v106, s2, v0
	v_readlane_b32 s2, v253, 9
	s_nop 1
	v_add_u32_e32 v94, s2, v106
	v_cmp_gt_i32_e64 s[2:3], 32, v94
	v_lshl_add_u32 v107, v94, 2, 0
	s_and_saveexec_b64 s[4:5], s[2:3]
	v_add_u32_e32 v0, 0x14900, v107
	ds_write_b32 v0, v33
	s_or_b64 exec, exec, s[4:5]
	v_readlane_b32 s8, v252, 43
	s_lshl_b32 s4, s66, 11
	v_readlane_b32 s16, v252, 51
	v_readlane_b32 s17, v252, 52
	v_readlane_b32 s18, v252, 53
	v_readlane_b32 s19, v252, 54
	v_readlane_b32 s20, v252, 55
	v_readlane_b32 s21, v252, 56
	s_mov_b32 s5, s69
	s_mov_b32 s6, s4
	v_readlane_b32 s22, v252, 57
	v_readlane_b32 s23, v252, 58
	s_mov_b64 s[16:17], s[20:21]
	v_writelane_b32 v254, s6, 40
	s_lshl_b64 s[4:5], s[4:5], 2
	s_mov_b64 s[18:19], s[22:23]
	v_writelane_b32 v254, s7, 41
	v_readlane_b32 s9, v252, 44
	v_readlane_b32 s10, v252, 45
	v_readlane_b32 s11, v252, 46
	s_add_u32 s6, s18, s4
	s_addc_u32 s7, s19, s5
	v_readlane_b32 s8, v252, 0
	v_writelane_b32 v254, s6, 48
	v_readlane_b32 s9, v252, 1
	s_add_u32 s4, s8, s4
	v_writelane_b32 v254, s7, 49
	s_addc_u32 s5, s9, s5
	v_writelane_b32 v254, s4, 44
	s_mov_b32 s67, s69
	s_lshl_b64 s[40:41], s[66:67], 17
	v_writelane_b32 v254, s5, 45
	v_readlane_b32 s4, v253, 25
	v_readlane_b32 s5, v253, 26
	s_andn2_b64 vcc, exec, s[4:5]
	s_mov_b32 s6, 0
	v_readlane_b32 s12, v252, 47
	v_readlane_b32 s13, v252, 48
	v_readlane_b32 s14, v252, 49
	v_readlane_b32 s15, v252, 50
	v_readlane_b32 s10, v252, 2
	v_readlane_b32 s11, v252, 3
	s_waitcnt lgkmcnt(0)
	s_barrier
	s_cbranch_vccnz .LBB0_496
	s_lshl_b32 s68, s66, 5
	v_readlane_b32 s8, v252, 43
	s_lshl_b64 s[4:5], s[68:69], 2
	v_readlane_b32 s12, v252, 47
	v_readlane_b32 s13, v252, 48
	s_add_u32 s6, s12, s4
	v_lshlrev_b32_e32 v2, 3, v106
	s_addc_u32 s7, s13, s5
	v_ashrrev_i32_e32 v3, 31, v2
	v_readlane_b32 s4, v254, 48
	v_lshlrev_b64 v[0:1], 2, v[2:3]
	v_readlane_b32 s5, v254, 49
	v_readlane_b32 s9, v252, 44
	v_ashrrev_i32_e32 v5, 4, v106
	v_lshl_add_u64 v[96:97], s[4:5], 0, v[0:1]
	v_readlane_b32 s4, v254, 44
	v_readlane_b32 s5, v254, 45
	v_lshlrev_b32_e32 v6, 2, v94
	v_readlane_b32 s13, v255, 41
	v_lshl_add_u64 v[98:99], s[4:5], 0, v[0:1]
	v_and_b32_e32 v0, 31, v106
	v_lshlrev_b32_e32 v32, 2, v0
	v_readlane_b32 s8, v253, 28
	v_readlane_b32 s10, v252, 45
	v_and_b32_e32 v4, 15, v106
	v_ashrrev_i32_e32 v95, 5, v94
	v_and_b32_e32 v7, 0xffffff80, v6
	v_readlane_b32 s9, v255, 40
	v_add_u32_e32 v109, s13, v6
	s_add_i32 s4, 0, 0x14900
	v_mov_b32_e32 v6, s8
	s_movk_i32 s8, 0x1010
	v_lshl_add_u64 v[102:103], s[6:7], 0, v[32:33]
	s_add_i32 s6, 0, 0x1e800
	v_lshl_add_u32 v64, v5, 3, s42
	v_readlane_b32 s11, v252, 46
	v_add3_u32 v108, s9, v7, v32
	v_add_u32_e32 v110, s4, v32
	v_mad_u32_u24 v78, v4, s8, v6
	v_lshl_add_u32 v112, v95, 4, s6
	s_add_u32 s6, s10, s40
	s_addc_u32 s7, s11, s41
	v_lshlrev_b32_e32 v32, 2, v4
	v_lshlrev_b32_e32 v1, 5, v5
	v_lshlrev_b32_e32 v80, 2, v5
	v_lshl_add_u64 v[62:63], s[6:7], 0, v[32:33]
	v_add_u32_e32 v111, s13, v7
	v_readlane_b32 s6, v255, 15
	v_lshl_add_u64 v[100:101], s[36:37], 0, v[2:3]
	v_lshlrev_b64 v[2:3], 1, v[2:3]
	v_readlane_b32 s7, v255, 16
	v_readlane_b32 s14, v252, 49
	v_readlane_b32 s15, v252, 50
	v_add_u32_e32 v79, s9, v32
	s_mov_b32 s12, 0
	v_cmp_eq_u32_e64 s[4:5], 0, v106
	v_lshl_add_u32 v113, v106, 5, 0
	v_lshl_add_u64 v[104:105], s[94:95], 0, v[2:3]
	v_add_u32_e32 v114, v78, v1
	v_readlane_b32 s13, v255, 30
	v_readlane_b32 s14, v255, 19
	v_readlane_b32 s15, v252, 6
	v_readlane_b32 s16, v252, 51
	v_readlane_b32 s17, v252, 52
	v_readlane_b32 s18, v252, 53
	v_readlane_b32 s19, v252, 54
	v_readlane_b32 s20, v252, 55
	v_readlane_b32 s21, v252, 56
	v_readlane_b32 s22, v252, 57
	v_readlane_b32 s23, v252, 58
	v_lshl_add_u64 v[74:75], s[6:7], 0, v[2:3]
	v_readlane_b32 s6, v255, 28
	v_add_lshl_u32 v80, v80, s6, 7
	s_add_i32 s6, 0, 0x14a00
	v_lshl_add_u32 v32, v95, 6, s6
	v_add_u32_e32 v115, v79, v80
	v_ashrrev_i32_e32 v65, 31, v64
	v_lshlrev_b64 v[178:179], 7, v[64:65]
	s_mov_b64 s[98:99], 0x1000
	v_lshl_add_u64 v[178:179], v[62:63], 0, v[178:179]
	v_lshl_add_u64 v[180:181], v[178:179], 0, s[98:99]
	v_lshl_add_u64 v[182:183], v[180:181], 0, s[98:99]
	v_lshl_add_u64 v[184:185], v[182:183], 0, s[98:99]
	global_load_dword v4, v[184:185], off offset:64
	global_load_dword v8, v[184:185], off offset:192
	global_load_dword v5, v[184:185], off offset:320
	global_load_dword v9, v[184:185], off offset:448
	global_load_dword v6, v[184:185], off offset:576
	global_load_dword v10, v[184:185], off offset:704
	global_load_dword v7, v[184:185], off offset:832
	global_load_dword v11, v[184:185], off offset:960
	global_load_dword v12, v[184:185], off
	global_load_dword v16, v[184:185], off offset:128
	global_load_dword v13, v[184:185], off offset:256
	global_load_dword v17, v[184:185], off offset:384
	global_load_dword v14, v[184:185], off offset:512
	global_load_dword v18, v[184:185], off offset:640
	global_load_dword v15, v[184:185], off offset:768
	global_load_dword v19, v[184:185], off offset:896
	global_load_dword v20, v[182:183], off offset:64
	global_load_dword v24, v[182:183], off offset:192
	global_load_dword v21, v[182:183], off offset:320
	global_load_dword v25, v[182:183], off offset:448
	global_load_dword v22, v[182:183], off offset:576
	global_load_dword v26, v[182:183], off offset:704
	global_load_dword v23, v[182:183], off offset:832
	global_load_dword v27, v[182:183], off offset:960
	global_load_dword v28, v[182:183], off
	global_load_dword v34, v[182:183], off offset:128
	global_load_dword v29, v[182:183], off offset:256
	global_load_dword v35, v[182:183], off offset:384
; __device__ __forceinline__ void ln_row16(float (&v)[16], const float* lng, const float* lnb, int lane, float (&o)[16]) {
;     ...
;     for (int hf = 0; hf < 2; ++hf) { const int col = 512 * hf + 8 * lane;
;         const f32x4 g0 = *(const f32x4*)(lng + col), g1 = *(const f32x4*)(lng + col + 4), b0 = *(const f32x4*)(lnb + col), b1 = *(const f32x4*)(lnb + col + 4);
; __global__ void __launch_bounds__(NWAVES * 64, 2) mk_fwd(Args args) {
;     ...
;             bf16x8 rwh[4][2], rwl[4][2];
; #pragma unroll
;             for (int ks = 0; ks < 4; ++ks)
; #pragma unroll
;                 for (int tile = 0; tile < 2; ++tile) { float f[8];
; #pragma unroll
;                     for (int j = 0; j < 8; ++j) f[j] = rw[(size_t)(128 * wave + 32 * ks + 8 * kq + j) * NEXP + 16 * tile + tk];
;                     split8(f, rwh[ks][tile], rwl[ks][tile]); }
;             int nbatch = 0;
;             for (int rep = 0; rep < NREP(3); ++rep) {
;             const bool dummy = rep + 1 < NREP(3);
;             bf16_t* XBo = dummy ? CAT : XB; unsigned char* XQo = dummy ? (unsigned char*)HB : ws + WS_XQ;
;             if (rep > 0) { __syncthreads(); if (tid < 32) LCNT[tid] = 0; __syncthreads(); }
;             nbatch = 0;
;             u32x4 yp[2][2];
;             {   const int b0 = bx < T / 16 ? bx : 0;
; #pragma unroll
;                 for (int ii = 0; ii < 2; ++ii) { const size_t t = (size_t)b0 * 16 + wave * 2 + ii; yp[ii][0] = *(const u32x4*)(YB + t * D + 8 * lane); yp[ii][1] = *(const u32x4*)(YB + t * D + 512 + 8 * lane); } }
	global_load_dword v30, v[182:183], off offset:512
	global_load_dword v36, v[182:183], off offset:640
	global_load_dword v31, v[182:183], off offset:768
	global_load_dword v37, v[182:183], off offset:896
	global_load_dword v38, v[180:181], off offset:64
	global_load_dword v42, v[180:181], off offset:192
	global_load_dword v39, v[180:181], off offset:320
	global_load_dword v43, v[180:181], off offset:448
	global_load_dword v40, v[180:181], off offset:576
	global_load_dword v44, v[180:181], off offset:704
	global_load_dword v41, v[180:181], off offset:832
	global_load_dword v45, v[180:181], off offset:960
	global_load_dword v46, v[180:181], off
	global_load_dword v50, v[180:181], off offset:128
	global_load_dword v47, v[180:181], off offset:256
	global_load_dword v51, v[180:181], off offset:384
	global_load_dword v48, v[180:181], off offset:512
	global_load_dword v52, v[180:181], off offset:640
	global_load_dword v49, v[180:181], off offset:768
	global_load_dword v53, v[180:181], off offset:896
	global_load_dword v54, v[178:179], off offset:64
	global_load_dword v58, v[178:179], off offset:192
	global_load_dword v55, v[178:179], off offset:320
	global_load_dword v59, v[178:179], off offset:448
	global_load_dword v56, v[178:179], off offset:576
	global_load_dword v60, v[178:179], off offset:704
	global_load_dword v57, v[178:179], off offset:832
	global_load_dword v61, v[178:179], off offset:960
	global_load_dword v62, v[178:179], off
	global_load_dword v66, v[178:179], off offset:128
	global_load_dword v63, v[178:179], off offset:256
	global_load_dword v67, v[178:179], off offset:384
	global_load_dword v64, v[178:179], off offset:512
	global_load_dword v68, v[178:179], off offset:640
	global_load_dword v65, v[178:179], off offset:768
	global_load_dword v69, v[178:179], off offset:896
	global_load_dwordx4 v[82:85], v[74:75], off offset:3072
	global_load_dwordx4 v[78:81], v[74:75], off offset:2048
	global_load_dwordx4 v[70:73], v[74:75], off offset:1024
	s_nop 0
	global_load_dwordx4 v[74:77], v[74:75], off
	global_load_dword v249, v[102:103], off
	global_load_dwordx4 v[204:207], v[96:97], off
	global_load_dwordx4 v[226:229], v[98:99], off
	global_load_dwordx4 v[208:211], v[96:97], off offset:16
	global_load_dwordx4 v[230:233], v[98:99], off offset:16
	global_load_dwordx4 v[212:215], v[96:97], off offset:2048
	global_load_dwordx4 v[234:237], v[98:99], off offset:2048
	global_load_dwordx4 v[216:219], v[96:97], off offset:2064
	global_load_dwordx4 v[238:241], v[98:99], off offset:2064
	s_waitcnt vmcnt(63)
	v_cvt_pk_bf16_f32 v186, v4, v8
	v_cvt_pk_bf16_f32 v187, v5, v9
	v_cvt_pk_bf16_f32 v188, v6, v10
	v_cvt_pk_bf16_f32 v189, v7, v11
	v_lshlrev_b32_e32 v190, 16, v186
	v_and_b32_e32 v194, 0xffff0000, v186
	v_lshlrev_b32_e32 v191, 16, v187
	v_and_b32_e32 v195, 0xffff0000, v187
	v_lshlrev_b32_e32 v192, 16, v188
	v_and_b32_e32 v196, 0xffff0000, v188
	v_lshlrev_b32_e32 v193, 16, v189
	v_and_b32_e32 v197, 0xffff0000, v189
	v_sub_f32_e32 v4, v4, v190
	v_sub_f32_e32 v8, v8, v194
	v_sub_f32_e32 v5, v5, v191
	v_sub_f32_e32 v9, v9, v195
	v_sub_f32_e32 v6, v6, v192
	v_sub_f32_e32 v10, v10, v196
	v_sub_f32_e32 v7, v7, v193
	v_sub_f32_e32 v11, v11, v197
	v_cvt_pk_bf16_f32 v8, v4, v8
	v_cvt_pk_bf16_f32 v9, v5, v9
	v_cvt_pk_bf16_f32 v10, v6, v10
	v_cvt_pk_bf16_f32 v11, v7, v11
	v_mov_b32_e32 v4, v186
	v_mov_b32_e32 v5, v187
	v_mov_b32_e32 v6, v188
	v_mov_b32_e32 v7, v189
	s_waitcnt vmcnt(61)
	v_cvt_pk_bf16_f32 v186, v12, v16
	v_cvt_pk_bf16_f32 v187, v13, v17
	v_cvt_pk_bf16_f32 v188, v14, v18
	v_cvt_pk_bf16_f32 v189, v15, v19
	v_lshlrev_b32_e32 v190, 16, v186
	v_and_b32_e32 v194, 0xffff0000, v186
	v_lshlrev_b32_e32 v191, 16, v187
	v_and_b32_e32 v195, 0xffff0000, v187
	v_lshlrev_b32_e32 v192, 16, v188
	v_and_b32_e32 v196, 0xffff0000, v188
	v_lshlrev_b32_e32 v193, 16, v189
	v_and_b32_e32 v197, 0xffff0000, v189
	v_sub_f32_e32 v12, v12, v190
	v_sub_f32_e32 v16, v16, v194
	v_sub_f32_e32 v13, v13, v191
	v_sub_f32_e32 v17, v17, v195
	v_sub_f32_e32 v14, v14, v192
	v_sub_f32_e32 v18, v18, v196
	v_sub_f32_e32 v15, v15, v193
	v_sub_f32_e32 v19, v19, v197
	v_cvt_pk_bf16_f32 v16, v12, v16
	v_cvt_pk_bf16_f32 v17, v13, v17
	v_cvt_pk_bf16_f32 v18, v14, v18
	v_cvt_pk_bf16_f32 v19, v15, v19
	v_mov_b32_e32 v12, v186
	v_mov_b32_e32 v13, v187
	v_mov_b32_e32 v14, v188
	v_mov_b32_e32 v15, v189
	s_waitcnt vmcnt(53)
	v_cvt_pk_bf16_f32 v186, v20, v24
	v_cvt_pk_bf16_f32 v187, v21, v25
	v_cvt_pk_bf16_f32 v188, v22, v26
	v_cvt_pk_bf16_f32 v189, v23, v27
	v_lshlrev_b32_e32 v190, 16, v186
	v_and_b32_e32 v194, 0xffff0000, v186
	v_lshlrev_b32_e32 v191, 16, v187
	v_and_b32_e32 v195, 0xffff0000, v187
	v_lshlrev_b32_e32 v192, 16, v188
	v_and_b32_e32 v196, 0xffff0000, v188
	v_lshlrev_b32_e32 v193, 16, v189
	v_and_b32_e32 v197, 0xffff0000, v189
	v_sub_f32_e32 v20, v20, v190
	v_sub_f32_e32 v24, v24, v194
	v_sub_f32_e32 v21, v21, v191
	v_sub_f32_e32 v25, v25, v195
	v_sub_f32_e32 v22, v22, v192
	v_sub_f32_e32 v26, v26, v196
	v_sub_f32_e32 v23, v23, v193
	v_sub_f32_e32 v27, v27, v197
	v_cvt_pk_bf16_f32 v24, v20, v24
	v_cvt_pk_bf16_f32 v25, v21, v25
	v_cvt_pk_bf16_f32 v26, v22, v26
	v_cvt_pk_bf16_f32 v27, v23, v27
	v_mov_b32_e32 v20, v186
	v_mov_b32_e32 v21, v187
	v_mov_b32_e32 v22, v188
	v_mov_b32_e32 v23, v189
	s_waitcnt vmcnt(45)
; __device__ __forceinline__ void unpack8(const u32x4 w, float (&f)[8]) { f[0] = bf_lo(w.x); f[1] = bf_hi(w.x); f[2] = bf_lo(w.y); f[3] = bf_hi(w.y); f[4] = bf_lo(w.z); f[5] = bf_hi(w.z); f[6] = bf_lo(w.w); f[7] = bf_hi(w.w); }
; __device__ __forceinline__ u32x4 pack8(const float (&f)[8]) { u32x4 o; o.x = cvt_pk_bf16(f[0], f[1]); o.y = cvt_pk_bf16(f[2], f[3]); o.z = cvt_pk_bf16(f[4], f[5]); o.w = cvt_pk_bf16(f[6], f[7]); return o; }
; __global__ void __launch_bounds__(NWAVES * 64, 2) mk_fwd(Args args) {
;     ...
;             auto split8 = [](const float (&f)[8], bf16x8& hi, bf16x8& lo) { const u32x4 h = pack8(f); float fh[8], fl[8]; unpack8(h, fh);
; #pragma unroll
;                 for (int i = 0; i < 8; ++i) fl[i] = f[i] - fh[i];
;                 hi = __builtin_bit_cast(bf16x8, h); lo = __builtin_bit_cast(bf16x8, pack8(fl)); };
;             bf16x8 rwh[4][2], rwl[4][2];
; #pragma unroll
;             for (int ks = 0; ks < 4; ++ks)
; #pragma unroll
;                 for (int tile = 0; tile < 2; ++tile) { float f[8];
; #pragma unroll
;                     for (int j = 0; j < 8; ++j) f[j] = rw[(size_t)(128 * wave + 32 * ks + 8 * kq + j) * NEXP + 16 * tile + tk];
;                     split8(f, rwh[ks][tile], rwl[ks][tile]); }
;     ...
;             for (int bi = bx; bi < T / 16; bi += G, ++nbatch) {
;                 u32x4 yc[2][2];
; #pragma unroll
;                 for (int ii = 0; ii < 2; ++ii) { yc[ii][0] = yp[ii][0]; yc[ii][1] = yp[ii][1]; }
;                 {   const int bn = (bi + G < T / 16) ? bi + G : bi;
; #pragma unroll
;                     for (int ii = 0; ii < 2; ++ii) { const size_t t = (size_t)bn * 16 + wave * 2 + ii; yp[ii][0] = *(const u32x4*)(YB + t * D + 8 * lane); yp[ii][1] = *(const u32x4*)(YB + t * D + 512 + 8 * lane); } }
	v_cvt_pk_bf16_f32 v186, v28, v34
	v_cvt_pk_bf16_f32 v187, v29, v35
	v_cvt_pk_bf16_f32 v188, v30, v36
	v_cvt_pk_bf16_f32 v189, v31, v37
	v_lshlrev_b32_e32 v190, 16, v186
	v_and_b32_e32 v194, 0xffff0000, v186
	v_lshlrev_b32_e32 v191, 16, v187
	v_and_b32_e32 v195, 0xffff0000, v187
	v_lshlrev_b32_e32 v192, 16, v188
	v_and_b32_e32 v196, 0xffff0000, v188
	v_lshlrev_b32_e32 v193, 16, v189
	v_and_b32_e32 v197, 0xffff0000, v189
	v_sub_f32_e32 v28, v28, v190
	v_sub_f32_e32 v34, v34, v194
	v_sub_f32_e32 v29, v29, v191
	v_sub_f32_e32 v35, v35, v195
	v_sub_f32_e32 v30, v30, v192
	v_sub_f32_e32 v36, v36, v196
	v_sub_f32_e32 v31, v31, v193
	v_sub_f32_e32 v37, v37, v197
	v_cvt_pk_bf16_f32 v34, v28, v34
	v_cvt_pk_bf16_f32 v35, v29, v35
	v_cvt_pk_bf16_f32 v36, v30, v36
	v_cvt_pk_bf16_f32 v37, v31, v37
	v_mov_b32_e32 v28, v186
	v_mov_b32_e32 v29, v187
	v_mov_b32_e32 v30, v188
	v_mov_b32_e32 v31, v189
	s_waitcnt vmcnt(37)
	v_cvt_pk_bf16_f32 v186, v38, v42
	v_cvt_pk_bf16_f32 v187, v39, v43
	v_cvt_pk_bf16_f32 v188, v40, v44
	v_cvt_pk_bf16_f32 v189, v41, v45
	v_lshlrev_b32_e32 v190, 16, v186
	v_and_b32_e32 v194, 0xffff0000, v186
	v_lshlrev_b32_e32 v191, 16, v187
	v_and_b32_e32 v195, 0xffff0000, v187
	v_lshlrev_b32_e32 v192, 16, v188
	v_and_b32_e32 v196, 0xffff0000, v188
	v_lshlrev_b32_e32 v193, 16, v189
	v_and_b32_e32 v197, 0xffff0000, v189
	v_sub_f32_e32 v38, v38, v190
	v_sub_f32_e32 v42, v42, v194
	v_sub_f32_e32 v39, v39, v191
	v_sub_f32_e32 v43, v43, v195
	v_sub_f32_e32 v40, v40, v192
	v_sub_f32_e32 v44, v44, v196
	v_sub_f32_e32 v41, v41, v193
	v_sub_f32_e32 v45, v45, v197
	v_cvt_pk_bf16_f32 v42, v38, v42
	v_cvt_pk_bf16_f32 v43, v39, v43
	v_cvt_pk_bf16_f32 v44, v40, v44
	v_cvt_pk_bf16_f32 v45, v41, v45
	v_mov_b32_e32 v38, v186
	v_mov_b32_e32 v39, v187
	v_mov_b32_e32 v40, v188
	v_mov_b32_e32 v41, v189
	s_waitcnt vmcnt(29)
	v_cvt_pk_bf16_f32 v186, v46, v50
	v_cvt_pk_bf16_f32 v187, v47, v51
	v_cvt_pk_bf16_f32 v188, v48, v52
	v_cvt_pk_bf16_f32 v189, v49, v53
	v_lshlrev_b32_e32 v190, 16, v186
	v_and_b32_e32 v194, 0xffff0000, v186
	v_lshlrev_b32_e32 v191, 16, v187
	v_and_b32_e32 v195, 0xffff0000, v187
	v_lshlrev_b32_e32 v192, 16, v188
	v_and_b32_e32 v196, 0xffff0000, v188
	v_lshlrev_b32_e32 v193, 16, v189
	v_and_b32_e32 v197, 0xffff0000, v189
	v_sub_f32_e32 v46, v46, v190
	v_sub_f32_e32 v50, v50, v194
	v_sub_f32_e32 v47, v47, v191
	v_sub_f32_e32 v51, v51, v195
	v_sub_f32_e32 v48, v48, v192
	v_sub_f32_e32 v52, v52, v196
	v_sub_f32_e32 v49, v49, v193
	v_sub_f32_e32 v53, v53, v197
	v_cvt_pk_bf16_f32 v50, v46, v50
	v_cvt_pk_bf16_f32 v51, v47, v51
	v_cvt_pk_bf16_f32 v52, v48, v52
	v_cvt_pk_bf16_f32 v53, v49, v53
	v_mov_b32_e32 v46, v186
	v_mov_b32_e32 v47, v187
	v_mov_b32_e32 v48, v188
	v_mov_b32_e32 v49, v189
	s_waitcnt vmcnt(21)
	v_cvt_pk_bf16_f32 v186, v54, v58
	v_cvt_pk_bf16_f32 v187, v55, v59
	v_cvt_pk_bf16_f32 v188, v56, v60
	v_cvt_pk_bf16_f32 v189, v57, v61
	v_lshlrev_b32_e32 v190, 16, v186
	v_and_b32_e32 v194, 0xffff0000, v186
	v_lshlrev_b32_e32 v191, 16, v187
	v_and_b32_e32 v195, 0xffff0000, v187
	v_lshlrev_b32_e32 v192, 16, v188
	v_and_b32_e32 v196, 0xffff0000, v188
	v_lshlrev_b32_e32 v193, 16, v189
	v_and_b32_e32 v197, 0xffff0000, v189
	v_sub_f32_e32 v54, v54, v190
	v_sub_f32_e32 v58, v58, v194
	v_sub_f32_e32 v55, v55, v191
	v_sub_f32_e32 v59, v59, v195
	v_sub_f32_e32 v56, v56, v192
	v_sub_f32_e32 v60, v60, v196
	v_sub_f32_e32 v57, v57, v193
	v_sub_f32_e32 v61, v61, v197
	v_cvt_pk_bf16_f32 v58, v54, v58
	v_cvt_pk_bf16_f32 v59, v55, v59
	v_cvt_pk_bf16_f32 v60, v56, v60
	v_cvt_pk_bf16_f32 v61, v57, v61
	v_mov_b32_e32 v54, v186
	v_mov_b32_e32 v55, v187
	v_mov_b32_e32 v56, v188
	v_mov_b32_e32 v57, v189
	s_waitcnt vmcnt(13)
	v_cvt_pk_bf16_f32 v186, v62, v66
	v_cvt_pk_bf16_f32 v187, v63, v67
	v_cvt_pk_bf16_f32 v188, v64, v68
	v_cvt_pk_bf16_f32 v189, v65, v69
	v_lshlrev_b32_e32 v190, 16, v186
	v_and_b32_e32 v194, 0xffff0000, v186
	v_lshlrev_b32_e32 v191, 16, v187
	v_and_b32_e32 v195, 0xffff0000, v187
	v_lshlrev_b32_e32 v192, 16, v188
	v_and_b32_e32 v196, 0xffff0000, v188
	v_lshlrev_b32_e32 v193, 16, v189
	v_and_b32_e32 v197, 0xffff0000, v189
	v_sub_f32_e32 v62, v62, v190
	v_sub_f32_e32 v66, v66, v194
	v_sub_f32_e32 v63, v63, v191
	v_sub_f32_e32 v67, v67, v195
	v_sub_f32_e32 v64, v64, v192
	v_sub_f32_e32 v68, v68, v196
	v_sub_f32_e32 v65, v65, v193
	v_sub_f32_e32 v69, v69, v197
	v_cvt_pk_bf16_f32 v66, v62, v66
	v_cvt_pk_bf16_f32 v67, v63, v67
	v_cvt_pk_bf16_f32 v68, v64, v68
	v_cvt_pk_bf16_f32 v69, v65, v69
	v_mov_b32_e32 v62, v186
	v_mov_b32_e32 v63, v187
	v_mov_b32_e32 v64, v188
	v_mov_b32_e32 v65, v189
.LBB0_485:
	s_mov_b32 s6, s15
	s_add_i32 s15, s15, s72
	s_cmpk_gt_i32 s15, 0x7ff
	s_cselect_b64 s[8:9], -1, 0
	s_cmpk_lt_i32 s15, 0x800
	s_cselect_b32 s6, s15, s6
	s_ashr_i32 s7, s6, 31
	s_lshl_b64 s[6:7], s[6:7], 4
	v_readlane_b32 s10, v255, 19
	s_add_u32 s6, s6, s10
	s_addc_u32 s7, s7, 0
	s_lshl_b64 s[6:7], s[6:7], 11
	s_mov_b64 s[98:99], s[6:7]
	s_waitcnt vmcnt(0)
	v_mov_b64_e32 v[88:89], v[84:85]
	v_mov_b64_e32 v[92:93], v[80:81]
	v_mov_b64_e32 v[86:87], v[82:83]
	v_mov_b64_e32 v[90:91], v[78:79]
	v_mov_b64_e32 v[118:119], v[76:77]
	v_mov_b64_e32 v[122:123], v[72:73]
	v_mov_b64_e32 v[116:117], v[74:75]
	v_mov_b64_e32 v[120:121], v[70:71]
	s_and_b64 vcc, exec, s[8:9]
	s_cbranch_vccnz .Lph3_no_prefetch
	v_lshl_add_u64 v[246:247], v[104:105], 0, s[98:99]
	global_load_dwordx4 v[74:77], v[246:247], off
	global_load_dwordx4 v[70:73], v[246:247], off offset:1024
	global_load_dwordx4 v[78:81], v[246:247], off offset:2048
	global_load_dwordx4 v[82:85], v[246:247], off offset:3072
; __device__ __forceinline__ void unpack8(const u32x4 w, float (&f)[8]) { f[0] = bf_lo(w.x); f[1] = bf_hi(w.x); f[2] = bf_lo(w.y); f[3] = bf_hi(w.y); f[4] = bf_lo(w.z); f[5] = bf_hi(w.z); f[6] = bf_lo(w.w); f[7] = bf_hi(w.w); }
; __device__ __forceinline__ float wave_sum(float v) { v += dpp_f<0xB1>(v); v += dpp_f<0x4E>(v); v += dpp_f<0x141>(v); v += dpp_f<0x140>(v); v += xor_sw<16>(v); return sum_x32(v); }
; __device__ __forceinline__ void ln_row16(float (&v)[16], const float* lng, const float* lnb, int lane, float (&o)[16]) {
;     const float s = ((v[0] + v[1]) + (v[2] + v[3])) + ((v[4] + v[5]) + (v[6] + v[7])) + (((v[8] + v[9]) + (v[10] + v[11])) + ((v[12] + v[13]) + (v[14] + v[15])));
;     const float mean = wave_sum(s) * (1.0f / D);
; #pragma unroll
;     for (int i = 0; i < 16; ++i) v[i] -= mean;
;     const float s2 = ((v[0] * v[0] + v[1] * v[1]) + (v[2] * v[2] + v[3] * v[3])) + ((v[4] * v[4] + v[5] * v[5]) + (v[6] * v[6] + v[7] * v[7]))
;                    + (((v[8] * v[8] + v[9] * v[9]) + (v[10] * v[10] + v[11] * v[11])) + ((v[12] * v[12] + v[13] * v[13]) + (v[14] * v[14] + v[15] * v[15])));
;     const float rstd = 1.0f / sqrtf(wave_sum(s2) * (1.0f / D) + LN_EPS);
; #pragma unroll
;     for (int hf = 0; hf < 2; ++hf) { const int col = 512 * hf + 8 * lane;
;         const f32x4 g0 = *(const f32x4*)(lng + col), g1 = *(const f32x4*)(lng + col + 4), b0 = *(const f32x4*)(lnb + col), b1 = *(const f32x4*)(lnb + col + 4);
; #pragma unroll
;         for (int i = 0; i < 4; ++i) { o[8 * hf + i] = v[8 * hf + i] * rstd * g0[i] + b0[i]; o[8 * hf + 4 + i] = v[8 * hf + 4 + i] * rstd * g1[i] + b1[i]; } }
; __global__ void __launch_bounds__(NWAVES * 64, 2) mk_fwd(Args args) {
;     ...
;                 for (int ii = 0; ii < 2; ++ii) {
;                     const int tl = wave * 2 + ii, t = bi * 16 + tl;
;                     float v[16], o[16];
; #pragma unroll
;                     for (int hf = 0; hf < 2; ++hf) { float f[8]; unpack8(yc[ii][hf], f);
; #pragma unroll
;                         for (int i = 0; i < 8; ++i) v[8 * hf + i] = f[i]; }
;                     ln_row16(v, lng, lnb, lane, o);
.Lph3_no_prefetch:
	s_nop 0
	s_nop 0
	s_nop 0
	s_nop 0
	v_lshlrev_b32_e32 v2, 16, v116
	v_and_b32_e32 v3, 0xffff0000, v116
	v_lshlrev_b32_e32 v152, 16, v117
	v_and_b32_e32 v153, 0xffff0000, v117
	v_lshlrev_b32_e32 v154, 16, v118
	v_and_b32_e32 v155, 0xffff0000, v118
	v_lshlrev_b32_e32 v156, 16, v119
	v_and_b32_e32 v157, 0xffff0000, v119
	s_nop 0
	s_nop 0
	s_nop 0
	s_nop 0
	v_lshlrev_b32_e32 v160, 16, v122
	v_and_b32_e32 v161, 0xffff0000, v122
	v_lshlrev_b32_e32 v122, 16, v123
	v_and_b32_e32 v123, 0xffff0000, v123
	v_lshlrev_b32_e32 v158, 16, v120
	v_and_b32_e32 v159, 0xffff0000, v120
	v_lshlrev_b32_e32 v120, 16, v121
	v_and_b32_e32 v121, 0xffff0000, v121
	v_add_f32_e32 v1, v123, v122
	v_add_f32_e32 v162, v161, v160
	v_add_f32_e32 v1, v162, v1
	v_add_f32_e32 v162, v121, v120
	v_add_f32_e32 v163, v159, v158
	v_add_f32_e32 v162, v163, v162
	v_add_f32_e32 v1, v162, v1
	v_add_f32_e32 v162, v157, v156
	v_add_f32_e32 v163, v155, v154
	v_add_f32_e32 v162, v163, v162
	v_add_f32_e32 v163, v153, v152
	v_add_f32_e32 v164, v3, v2
	v_add_f32_e32 v163, v164, v163
	v_add_f32_e32 v162, v163, v162
	v_add_f32_e32 v1, v162, v1
	s_mov_b32 s6, 0xf800000
	s_nop 0
	v_add_f32_dpp v1, v1, v1 quad_perm:[1,0,3,2] row_mask:0xf bank_mask:0xf bound_ctrl:1
	s_nop 1
	v_add_f32_dpp v1, v1, v1 quad_perm:[2,3,0,1] row_mask:0xf bank_mask:0xf bound_ctrl:1
	s_nop 1
	v_add_f32_dpp v1, v1, v1 row_half_mirror row_mask:0xf bank_mask:0xf bound_ctrl:1
	s_nop 1
	v_add_f32_dpp v1, v1, v1 row_mirror row_mask:0xf bank_mask:0xf bound_ctrl:1
	s_waitcnt lgkmcnt(0)
	v_mov_b32_e32 v162, v1
	s_nop 1
	v_permlane16_swap_b32_e32 v1, v162
	v_add_f32_e32 v1, v1, v162
	v_mov_b32_e32 v162, v1
	s_nop 1
	v_permlane32_swap_b32_e32 v1, v162
	v_add_f32_e32 v1, v1, v162
	v_mul_f32_e32 v162, 0x3a800000, v1
	v_pk_add_f32 v[2:3], v[2:3], v[162:163] op_sel_hi:[1,0] neg_lo:[0,1] neg_hi:[0,1]
	v_pk_add_f32 v[152:153], v[152:153], v[162:163] op_sel_hi:[1,0] neg_lo:[0,1] neg_hi:[0,1]
	v_pk_add_f32 v[154:155], v[154:155], v[162:163] op_sel_hi:[1,0] neg_lo:[0,1] neg_hi:[0,1]
	v_pk_add_f32 v[156:157], v[156:157], v[162:163] op_sel_hi:[1,0] neg_lo:[0,1] neg_hi:[0,1]
	v_pk_add_f32 v[158:159], v[158:159], v[162:163] op_sel_hi:[1,0] neg_lo:[0,1] neg_hi:[0,1]
	v_pk_add_f32 v[164:165], v[120:121], v[162:163] op_sel_hi:[1,0] neg_lo:[0,1] neg_hi:[0,1]
	v_pk_add_f32 v[160:161], v[160:161], v[162:163] op_sel_hi:[1,0] neg_lo:[0,1] neg_hi:[0,1]
	v_pk_add_f32 v[162:163], v[122:123], v[162:163] op_sel_hi:[1,0] neg_lo:[0,1] neg_hi:[0,1]
	v_pk_mul_f32 v[120:121], v[2:3], v[2:3]
	v_pk_mul_f32 v[122:123], v[152:153], v[152:153]
	v_pk_mul_f32 v[166:167], v[154:155], v[154:155]
	v_pk_mul_f32 v[168:169], v[156:157], v[156:157]
	v_pk_mul_f32 v[170:171], v[158:159], v[158:159]
	v_pk_mul_f32 v[172:173], v[164:165], v[164:165]
	v_pk_mul_f32 v[174:175], v[160:161], v[160:161]
	v_pk_mul_f32 v[176:177], v[162:163], v[162:163]
	v_add_f32_e32 v174, v174, v175
	v_add_f32_e32 v1, v176, v177
	v_add_f32_e32 v172, v172, v173
	v_add_f32_e32 v170, v170, v171
	v_add_f32_e32 v168, v168, v169
	v_add_f32_e32 v166, v166, v167
	v_add_f32_e32 v122, v122, v123
	v_add_f32_e32 v120, v120, v121
	v_add_f32_e32 v1, v174, v1
	v_add_f32_e32 v170, v170, v172
	v_add_f32_e32 v166, v166, v168
	v_add_f32_e32 v120, v120, v122
	v_add_f32_e32 v1, v170, v1
	v_add_f32_e32 v120, v120, v166
	v_add_f32_e32 v1, v120, v1
	s_nop 1
	v_add_f32_dpp v1, v1, v1 quad_perm:[1,0,3,2] row_mask:0xf bank_mask:0xf bound_ctrl:1
	s_nop 1
	v_add_f32_dpp v1, v1, v1 quad_perm:[2,3,0,1] row_mask:0xf bank_mask:0xf bound_ctrl:1
	s_nop 1
	v_add_f32_dpp v1, v1, v1 row_half_mirror row_mask:0xf bank_mask:0xf bound_ctrl:1
	s_nop 1
	v_add_f32_dpp v1, v1, v1 row_mirror row_mask:0xf bank_mask:0xf bound_ctrl:1
	s_waitcnt lgkmcnt(0)
	v_mov_b32_e32 v120, v1
	s_nop 1
	v_permlane16_swap_b32_e32 v1, v120
	v_add_f32_e32 v1, v1, v120
	v_mov_b32_e32 v120, v1
	s_nop 1
	v_permlane32_swap_b32_e32 v1, v120
	v_add_f32_e32 v1, v1, v120
	v_fmamk_f32 v1, v1, 0x3a800000, v250
	v_cmp_gt_f32_e32 vcc, s6, v1
	v_mul_f32_e32 v120, 0x4f800000, v1
	s_nop 0
	v_cndmask_b32_e32 v1, v1, v120, vcc
	v_sqrt_f32_e32 v120, v1
	s_nop 0
	v_add_u32_e32 v121, -1, v120
	v_fma_f32 v122, -v121, v120, v1
	v_cmp_ge_f32_e64 s[6:7], 0, v122
	v_add_u32_e32 v122, 1, v120
	s_nop 0
	v_cndmask_b32_e64 v121, v120, v121, s[6:7]
	v_fma_f32 v120, -v122, v120, v1
	v_cmp_lt_f32_e64 s[6:7], 0, v120
	s_nop 1
	v_cndmask_b32_e64 v120, v121, v122, s[6:7]
	v_mul_f32_e32 v121, 0x37800000, v120
	v_cndmask_b32_e32 v120, v120, v121, vcc
	v_cmp_class_f32_e32 vcc, v1, v251
	s_nop 1
	v_cndmask_b32_e32 v1, v120, v1, vcc
	v_div_scale_f32 v120, s[6:7], v1, v1, 1.0
	v_rcp_f32_e32 v121, v120
	s_mul_i32 s6, s73, 0x2020
	v_fma_f32 v122, -v120, v121, 1.0
	v_fmac_f32_e32 v121, v122, v121
	v_div_scale_f32 v122, vcc, 1.0, v1, 1.0
	v_mul_f32_e32 v123, v122, v121
	v_fma_f32 v166, -v120, v123, v122
	v_fmac_f32_e32 v123, v166, v121
	v_fma_f32 v120, -v120, v123, v122
	v_div_fmas_f32 v120, v120, v121, v123
	v_div_fixup_f32 v166, v120, v1, 1.0
	v_pk_mul_f32 v[2:3], v[2:3], v[166:167] op_sel_hi:[1,0]
	v_add_u32_e32 v1, s6, v113
	s_nop 0
	v_pk_fma_f32 v[120:121], v[204:205], v[2:3], v[226:227]
	v_pk_mul_f32 v[2:3], v[154:155], v[166:167] op_sel_hi:[1,0]
	v_readlane_b32 s6, v255, 36
	v_pk_fma_f32 v[124:125], v[208:209], v[2:3], v[230:231]
	v_pk_mul_f32 v[2:3], v[152:153], v[166:167] op_sel_hi:[1,0]
	s_add_i32 s10, s6, s14
	v_pk_fma_f32 v[122:123], v[206:207], v[2:3], v[228:229]
	v_pk_mul_f32 v[2:3], v[156:157], v[166:167] op_sel_hi:[1,0]
	s_ashr_i32 s11, s10, 31
	v_pk_fma_f32 v[126:127], v[210:211], v[2:3], v[232:233]
	v_pk_mul_f32 v[2:3], v[158:159], v[166:167] op_sel_hi:[1,0]
; #define LAS __attribute__((address_space(3)))
; __device__ __forceinline__ float wave_max(float v) { v = fmaxf(v, dpp_f<0xB1>(v)); v = fmaxf(v, dpp_f<0x4E>(v)); v = fmaxf(v, dpp_f<0x141>(v)); v = fmaxf(v, dpp_f<0x140>(v)); v = fmaxf(v, xor_sw<16>(v)); return max_x32(v); }
; __device__ __forceinline__ float q8_row16(const float (&o)[16], unsigned char* qrow, int lane) {
;     float am = 0.f;
; #pragma unroll
;     for (int i = 0; i < 16; ++i) am = fmaxf(am, fabsf(o[i]));
;     am = wave_max(am);
;     const float qs = am > 0.f ? am * (1.0f / 127.0f) : 1.0f, qinv = 1.0f / qs;
; #pragma unroll
;     for (int hf = 0; hf < 2; ++hf) { u32x2 q; q.x = q8x4(o[8 * hf], o[8 * hf + 1], o[8 * hf + 2], o[8 * hf + 3], qinv); q.y = q8x4(o[8 * hf + 4], o[8 * hf + 5], o[8 * hf + 6], o[8 * hf + 7], qinv);
;         *(u32x2*)(qrow + 512 * hf + 8 * lane) = q; }
;     return qs;
; }
; __global__ void __launch_bounds__(NWAVES * 64, 2) mk_fwd(Args args) {
;     ...
; #pragma unroll
;                     for (int hf = 0; hf < 2; ++hf) { const int col = 512 * hf + 8 * lane;
;                         *(LAS f32x4*)(XL + tl * XS + col) = (f32x4){o[8 * hf], o[8 * hf + 1], o[8 * hf + 2], o[8 * hf + 3]}; *(LAS f32x4*)(XL + tl * XS + col + 4) = (f32x4){o[8 * hf + 4], o[8 * hf + 5], o[8 * hf + 6], o[8 * hf + 7]}; }
;                     const float qs = q8_row16(o, XQo + (size_t)t * D, lane);
;                     if (lane == 0) TSC[nbatch * 16 + tl] = qs;
	s_lshl_b64 s[6:7], s[10:11], 10
	s_nop 0
	v_pk_fma_f32 v[128:129], v[212:213], v[2:3], v[234:235]
	v_pk_mul_f32 v[2:3], v[160:161], v[166:167] op_sel_hi:[1,0]
	s_nop 0
	v_pk_fma_f32 v[116:117], v[216:217], v[2:3], v[238:239]
	v_pk_mul_f32 v[2:3], v[164:165], v[166:167] op_sel_hi:[1,0]
	s_nop 0
	v_pk_fma_f32 v[130:131], v[214:215], v[2:3], v[236:237]
	v_pk_mul_f32 v[2:3], v[162:163], v[166:167] op_sel_hi:[1,0]
	s_nop 0
	v_pk_fma_f32 v[118:119], v[218:219], v[2:3], v[240:241]
	ds_write_b128 v1, v[120:123]
	ds_write_b128 v1, v[124:127] offset:16
	ds_write_b128 v1, v[128:131] offset:2048
	ds_write_b128 v1, v[116:119] offset:2064
	v_max3_f32 v1, |v120|, 0, |v121|
	v_max3_f32 v1, v1, |v122|, |v123|
	v_max3_f32 v1, v1, |v124|, |v125|
	v_max3_f32 v1, v1, |v126|, |v127|
	v_max3_f32 v1, v1, |v128|, |v129|
	v_max3_f32 v1, v1, |v130|, |v131|
	v_max3_f32 v1, v1, |v116|, |v117|
	v_max3_f32 v1, v1, |v118|, |v119|
	s_nop 1
	v_mov_b32_dpp v2, v1 quad_perm:[1,0,3,2] row_mask:0xf bank_mask:0xf bound_ctrl:1
	v_max_f32_e32 v2, v2, v2
	v_max_f32_e32 v1, v1, v2
	s_nop 1
	v_mov_b32_dpp v2, v1 quad_perm:[2,3,0,1] row_mask:0xf bank_mask:0xf bound_ctrl:1
	v_max_f32_e32 v2, v2, v2
	v_max_f32_e32 v1, v1, v2
	s_nop 1
	v_mov_b32_dpp v2, v1 row_half_mirror row_mask:0xf bank_mask:0xf bound_ctrl:1
	v_max_f32_e32 v2, v2, v2
	v_max_f32_e32 v1, v1, v2
	s_nop 1
	v_mov_b32_dpp v2, v1 row_mirror row_mask:0xf bank_mask:0xf bound_ctrl:1
	v_max_f32_e32 v2, v2, v2
	v_max_f32_e32 v1, v1, v2
	s_waitcnt lgkmcnt(0)
	v_mov_b32_e32 v2, v1
	s_nop 1
	v_permlane16_swap_b32_e32 v1, v2
	v_max_f32_e32 v2, v2, v2
	v_max_f32_e32 v1, v1, v2
	v_mov_b32_e32 v2, v1
	s_nop 1
	v_permlane32_swap_b32_e32 v1, v2
	v_max_f32_e32 v2, v2, v2
	v_max_f32_e32 v1, v1, v1
	v_max_f32_e32 v1, v1, v2
	v_cmp_lt_f32_e32 vcc, 0, v1
	v_mul_f32_e32 v1, 0x3c010204, v1
	s_nop 0
	v_cndmask_b32_e32 v1, 1.0, v1, vcc
	v_div_scale_f32 v2, s[16:17], v1, v1, 1.0
	v_rcp_f32_e32 v3, v2
	s_nop 0
	v_fma_f32 v132, -v2, v3, 1.0
	v_fmac_f32_e32 v3, v132, v3
	v_div_scale_f32 v132, vcc, 1.0, v1, 1.0
	v_mul_f32_e32 v133, v132, v3
	v_fma_f32 v134, -v2, v133, v132
	v_fmac_f32_e32 v133, v134, v3
	v_fma_f32 v2, -v2, v133, v132
	v_div_fmas_f32 v2, v2, v3, v133
	v_div_fixup_f32 v132, v2, v1, 1.0
	v_fmaak_f32 v120, v120, v132, 0x4b400000
	v_fmaak_f32 v121, v121, v132, 0x4b400000
	v_fmaak_f32 v122, v122, v132, 0x4b400000
	v_fmaak_f32 v123, v123, v132, 0x4b400000
	v_perm_b32 v122, v123, v122, s61
	v_perm_b32 v120, v121, v120, s61
	v_perm_b32 v120, v122, v120, s79
	v_fmaak_f32 v121, v124, v132, 0x4b400000
	v_fmaak_f32 v122, v125, v132, 0x4b400000
	v_fmaak_f32 v123, v126, v132, 0x4b400000
	v_fmaak_f32 v124, v127, v132, 0x4b400000
	v_perm_b32 v123, v124, v123, s61
	v_perm_b32 v121, v122, v121, s61
	v_lshl_add_u64 v[2:3], v[100:101], 0, s[6:7]
	v_perm_b32 v121, v123, v121, s79
	global_store_dwordx2 v[2:3], v[120:121], off
	v_fmaak_f32 v120, v128, v132, 0x4b400000
	v_fmaak_f32 v121, v129, v132, 0x4b400000
	v_fmaak_f32 v122, v130, v132, 0x4b400000
	v_fmaak_f32 v123, v131, v132, 0x4b400000
	v_fmaak_f32 v116, v116, v132, 0x4b400000
	v_fmaak_f32 v117, v117, v132, 0x4b400000
	v_fmaak_f32 v118, v118, v132, 0x4b400000
	v_fmaak_f32 v119, v119, v132, 0x4b400000
	v_perm_b32 v122, v123, v122, s61
	v_perm_b32 v120, v121, v120, s61
	v_perm_b32 v118, v119, v118, s61
	v_perm_b32 v116, v117, v116, s61
	v_perm_b32 v120, v122, v120, s79
	v_perm_b32 v121, v118, v116, s79
	global_store_dwordx2 v[2:3], v[120:121], off offset:512
	s_and_saveexec_b64 s[6:7], s[4:5]
	s_add_i32 s11, s13, -4
	v_mov_b32_e32 v2, s11
	ds_write_b32 v2, v1
	s_or_b64 exec, exec, s[6:7]
	v_lshlrev_b32_e32 v150, 16, v88
	v_and_b32_e32 v151, 0xffff0000, v88
	v_lshlrev_b32_e32 v152, 16, v89
	v_and_b32_e32 v153, 0xffff0000, v89
	v_lshlrev_b32_e32 v146, 16, v86
	v_and_b32_e32 v147, 0xffff0000, v86
	v_lshlrev_b32_e32 v148, 16, v87
	v_and_b32_e32 v149, 0xffff0000, v87
	v_add_f32_e32 v1, v153, v152
	v_add_f32_e32 v86, v151, v150
	v_add_f32_e32 v1, v86, v1
	v_add_f32_e32 v86, v149, v148
	v_add_f32_e32 v87, v147, v146
	v_lshlrev_b32_e32 v142, 16, v92
	v_and_b32_e32 v143, 0xffff0000, v92
	v_lshlrev_b32_e32 v144, 16, v93
	v_and_b32_e32 v145, 0xffff0000, v93
	v_add_f32_e32 v86, v87, v86
	s_nop 0
	s_nop 0
	s_nop 0
	s_nop 0
	v_lshlrev_b32_e32 v2, 16, v90
	v_and_b32_e32 v3, 0xffff0000, v90
	v_lshlrev_b32_e32 v140, 16, v91
	v_and_b32_e32 v141, 0xffff0000, v91
	v_add_f32_e32 v1, v86, v1
	v_add_f32_e32 v86, v145, v144
	v_add_f32_e32 v87, v143, v142
	v_add_f32_e32 v86, v87, v86
	v_add_f32_e32 v87, v141, v140
	v_add_f32_e32 v88, v3, v2
	v_add_f32_e32 v87, v88, v87
	v_add_f32_e32 v86, v87, v86
	v_add_f32_e32 v1, v86, v1
	s_nop 0
	s_nop 0
	s_nop 0
	s_nop 0
	v_add_f32_dpp v1, v1, v1 quad_perm:[1,0,3,2] row_mask:0xf bank_mask:0xf bound_ctrl:1
	s_mov_b32 s6, 0xf800000
	s_nop 0
	v_add_f32_dpp v1, v1, v1 quad_perm:[2,3,0,1] row_mask:0xf bank_mask:0xf bound_ctrl:1
	s_nop 1
	v_add_f32_dpp v1, v1, v1 row_half_mirror row_mask:0xf bank_mask:0xf bound_ctrl:1
	s_nop 1
	v_add_f32_dpp v1, v1, v1 row_mirror row_mask:0xf bank_mask:0xf bound_ctrl:1
	s_waitcnt lgkmcnt(0)
; #define LAS __attribute__((address_space(3)))
; __device__ __forceinline__ float wave_sum(float v) { v += dpp_f<0xB1>(v); v += dpp_f<0x4E>(v); v += dpp_f<0x141>(v); v += dpp_f<0x140>(v); v += xor_sw<16>(v); return sum_x32(v); }
; __device__ __forceinline__ void ln_row16(float (&v)[16], const float* lng, const float* lnb, int lane, float (&o)[16]) {
;     const float s = ((v[0] + v[1]) + (v[2] + v[3])) + ((v[4] + v[5]) + (v[6] + v[7])) + (((v[8] + v[9]) + (v[10] + v[11])) + ((v[12] + v[13]) + (v[14] + v[15])));
;     const float mean = wave_sum(s) * (1.0f / D);
; #pragma unroll
;     for (int i = 0; i < 16; ++i) v[i] -= mean;
;     const float s2 = ((v[0] * v[0] + v[1] * v[1]) + (v[2] * v[2] + v[3] * v[3])) + ((v[4] * v[4] + v[5] * v[5]) + (v[6] * v[6] + v[7] * v[7]))
;                    + (((v[8] * v[8] + v[9] * v[9]) + (v[10] * v[10] + v[11] * v[11])) + ((v[12] * v[12] + v[13] * v[13]) + (v[14] * v[14] + v[15] * v[15])));
;     const float rstd = 1.0f / sqrtf(wave_sum(s2) * (1.0f / D) + LN_EPS);
; #pragma unroll
;     for (int hf = 0; hf < 2; ++hf) { const int col = 512 * hf + 8 * lane;
;         const f32x4 g0 = *(const f32x4*)(lng + col), g1 = *(const f32x4*)(lng + col + 4), b0 = *(const f32x4*)(lnb + col), b1 = *(const f32x4*)(lnb + col + 4);
; #pragma unroll
;         for (int i = 0; i < 4; ++i) { o[8 * hf + i] = v[8 * hf + i] * rstd * g0[i] + b0[i]; o[8 * hf + 4 + i] = v[8 * hf + 4 + i] * rstd * g1[i] + b1[i]; } }
; __global__ void __launch_bounds__(NWAVES * 64, 2) mk_fwd(Args args) {
;     ...
;                 for (int ii = 0; ii < 2; ++ii) {
;                     const int tl = wave * 2 + ii, t = bi * 16 + tl;
;                     float v[16], o[16];
; #pragma unroll
;                     for (int hf = 0; hf < 2; ++hf) { float f[8]; unpack8(yc[ii][hf], f);
; #pragma unroll
;                         for (int i = 0; i < 8; ++i) v[8 * hf + i] = f[i]; }
;                     ln_row16(v, lng, lnb, lane, o);
; #pragma unroll
;                     for (int hf = 0; hf < 2; ++hf) { const int col = 512 * hf + 8 * lane;
;                         *(LAS f32x4*)(XL + tl * XS + col) = (f32x4){o[8 * hf], o[8 * hf + 1], o[8 * hf + 2], o[8 * hf + 3]}; *(LAS f32x4*)(XL + tl * XS + col + 4) = (f32x4){o[8 * hf + 4], o[8 * hf + 5], o[8 * hf + 6], o[8 * hf + 7]}; }
;                     const float qs = q8_row16(o, XQo + (size_t)t * D, lane);
	v_mov_b32_e32 v154, v1
	s_nop 1
	v_permlane16_swap_b32_e32 v1, v154
	v_add_f32_e32 v1, v1, v154
	v_mov_b32_e32 v154, v1
	s_nop 1
	v_permlane32_swap_b32_e32 v1, v154
	v_add_f32_e32 v1, v1, v154
	v_mul_f32_e32 v154, 0x3a800000, v1
	v_pk_add_f32 v[2:3], v[2:3], v[154:155] op_sel_hi:[1,0] neg_lo:[0,1] neg_hi:[0,1]
	v_pk_add_f32 v[140:141], v[140:141], v[154:155] op_sel_hi:[1,0] neg_lo:[0,1] neg_hi:[0,1]
	v_pk_add_f32 v[142:143], v[142:143], v[154:155] op_sel_hi:[1,0] neg_lo:[0,1] neg_hi:[0,1]
	v_pk_add_f32 v[144:145], v[144:145], v[154:155] op_sel_hi:[1,0] neg_lo:[0,1] neg_hi:[0,1]
	v_pk_add_f32 v[146:147], v[146:147], v[154:155] op_sel_hi:[1,0] neg_lo:[0,1] neg_hi:[0,1]
	v_pk_add_f32 v[148:149], v[148:149], v[154:155] op_sel_hi:[1,0] neg_lo:[0,1] neg_hi:[0,1]
	v_pk_add_f32 v[150:151], v[150:151], v[154:155] op_sel_hi:[1,0] neg_lo:[0,1] neg_hi:[0,1]
	v_pk_add_f32 v[152:153], v[152:153], v[154:155] op_sel_hi:[1,0] neg_lo:[0,1] neg_hi:[0,1]
	v_pk_mul_f32 v[154:155], v[2:3], v[2:3]
	v_pk_mul_f32 v[156:157], v[140:141], v[140:141]
	v_pk_mul_f32 v[158:159], v[142:143], v[142:143]
	v_pk_mul_f32 v[160:161], v[144:145], v[144:145]
	v_pk_mul_f32 v[162:163], v[146:147], v[146:147]
	v_pk_mul_f32 v[164:165], v[148:149], v[148:149]
	v_pk_mul_f32 v[166:167], v[150:151], v[150:151]
	v_pk_mul_f32 v[168:169], v[152:153], v[152:153]
	v_add_f32_e32 v166, v166, v167
	v_add_f32_e32 v1, v168, v169
	v_add_f32_e32 v164, v164, v165
	v_add_f32_e32 v162, v162, v163
	v_add_f32_e32 v160, v160, v161
	v_add_f32_e32 v158, v158, v159
	v_add_f32_e32 v156, v156, v157
	v_add_f32_e32 v154, v154, v155
	v_add_f32_e32 v1, v166, v1
	v_add_f32_e32 v162, v162, v164
	v_add_f32_e32 v158, v158, v160
	v_add_f32_e32 v154, v154, v156
	v_add_f32_e32 v1, v162, v1
	v_add_f32_e32 v154, v154, v158
	v_add_f32_e32 v1, v154, v1
	s_nop 1
	v_add_f32_dpp v1, v1, v1 quad_perm:[1,0,3,2] row_mask:0xf bank_mask:0xf bound_ctrl:1
	s_nop 1
	v_add_f32_dpp v1, v1, v1 quad_perm:[2,3,0,1] row_mask:0xf bank_mask:0xf bound_ctrl:1
	s_nop 1
	v_add_f32_dpp v1, v1, v1 row_half_mirror row_mask:0xf bank_mask:0xf bound_ctrl:1
	s_nop 1
	v_add_f32_dpp v1, v1, v1 row_mirror row_mask:0xf bank_mask:0xf bound_ctrl:1
	s_waitcnt lgkmcnt(0)
	v_mov_b32_e32 v154, v1
	s_nop 1
	v_permlane16_swap_b32_e32 v1, v154
	v_add_f32_e32 v1, v1, v154
	v_mov_b32_e32 v154, v1
	s_nop 1
	v_permlane32_swap_b32_e32 v1, v154
	v_add_f32_e32 v1, v1, v154
	v_fmamk_f32 v1, v1, 0x3a800000, v250
	v_mul_f32_e32 v154, 0x4f800000, v1
	v_cmp_gt_f32_e32 vcc, s6, v1
	s_nop 1
	v_cndmask_b32_e32 v1, v1, v154, vcc
	v_sqrt_f32_e32 v154, v1
	s_nop 0
	v_add_u32_e32 v155, -1, v154
	v_fma_f32 v156, -v155, v154, v1
	v_cmp_ge_f32_e64 s[6:7], 0, v156
	v_add_u32_e32 v156, 1, v154
	s_nop 0
	v_cndmask_b32_e64 v155, v154, v155, s[6:7]
	v_fma_f32 v154, -v156, v154, v1
	v_cmp_lt_f32_e64 s[6:7], 0, v154
	s_nop 1
	v_cndmask_b32_e64 v154, v155, v156, s[6:7]
	v_mul_f32_e32 v155, 0x37800000, v154
	v_cndmask_b32_e32 v154, v154, v155, vcc
	v_cmp_class_f32_e32 vcc, v1, v251
	s_nop 1
	v_cndmask_b32_e32 v1, v154, v1, vcc
	v_div_scale_f32 v154, s[6:7], v1, v1, 1.0
	v_rcp_f32_e32 v155, v154
	v_readlane_b32 s6, v255, 21
	v_fma_f32 v156, -v154, v155, 1.0
	v_fmac_f32_e32 v155, v156, v155
	v_div_scale_f32 v156, vcc, 1.0, v1, 1.0
	v_mul_f32_e32 v157, v156, v155
	v_fma_f32 v158, -v154, v157, v156
	v_fmac_f32_e32 v157, v158, v155
	v_fma_f32 v154, -v154, v157, v156
	v_div_fmas_f32 v154, v154, v155, v157
	v_div_fixup_f32 v154, v154, v1, 1.0
	v_pk_mul_f32 v[2:3], v[2:3], v[154:155] op_sel_hi:[1,0]
	v_add_u32_e32 v1, s6, v113
	s_nop 0
	v_pk_fma_f32 v[120:121], v[204:205], v[2:3], v[226:227]
	v_pk_mul_f32 v[2:3], v[142:143], v[154:155] op_sel_hi:[1,0]
	s_nop 0
	v_pk_fma_f32 v[116:117], v[208:209], v[2:3], v[230:231]
	v_pk_mul_f32 v[2:3], v[140:141], v[154:155] op_sel_hi:[1,0]
	s_nop 0
	v_pk_fma_f32 v[122:123], v[206:207], v[2:3], v[228:229]
	v_pk_mul_f32 v[2:3], v[144:145], v[154:155] op_sel_hi:[1,0]
	s_nop 0
	v_pk_fma_f32 v[118:119], v[210:211], v[2:3], v[232:233]
	v_pk_mul_f32 v[2:3], v[146:147], v[154:155] op_sel_hi:[1,0]
	s_nop 0
	v_pk_fma_f32 v[90:91], v[212:213], v[2:3], v[234:235]
	v_pk_mul_f32 v[2:3], v[150:151], v[154:155] op_sel_hi:[1,0]
	s_nop 0
	v_pk_fma_f32 v[86:87], v[216:217], v[2:3], v[238:239]
	v_pk_mul_f32 v[2:3], v[148:149], v[154:155] op_sel_hi:[1,0]
	s_nop 0
	v_pk_fma_f32 v[92:93], v[214:215], v[2:3], v[236:237]
	v_pk_mul_f32 v[2:3], v[152:153], v[154:155] op_sel_hi:[1,0]
	s_nop 0
	v_pk_fma_f32 v[88:89], v[218:219], v[2:3], v[240:241]
	v_max3_f32 v2, |v120|, 0, |v121|
	v_max3_f32 v2, v2, |v122|, |v123|
	v_max3_f32 v2, v2, |v116|, |v117|
	v_max3_f32 v2, v2, |v118|, |v119|
	v_max3_f32 v2, v2, |v90|, |v91|
	v_max3_f32 v2, v2, |v92|, |v93|
	v_max3_f32 v2, v2, |v86|, |v87|
	v_max3_f32 v2, v2, |v88|, |v89|
	ds_write_b128 v1, v[120:123]
	ds_write_b128 v1, v[116:119] offset:16
	ds_write_b128 v1, v[90:93] offset:2048
	ds_write_b128 v1, v[86:89] offset:2064
	v_mov_b32_dpp v3, v2 quad_perm:[1,0,3,2] row_mask:0xf bank_mask:0xf bound_ctrl:1
	v_max_f32_e32 v3, v3, v3
	v_max_f32_e32 v2, v2, v3
	s_nop 1
	v_mov_b32_dpp v3, v2 quad_perm:[2,3,0,1] row_mask:0xf bank_mask:0xf bound_ctrl:1
	v_max_f32_e32 v3, v3, v3
	v_max_f32_e32 v2, v2, v3
	s_nop 1
	v_mov_b32_dpp v3, v2 row_half_mirror row_mask:0xf bank_mask:0xf bound_ctrl:1
	v_max_f32_e32 v3, v3, v3
	v_max_f32_e32 v2, v2, v3
	s_nop 1
	v_mov_b32_dpp v3, v2 row_mirror row_mask:0xf bank_mask:0xf bound_ctrl:1
	v_max_f32_e32 v3, v3, v3
	v_max_f32_e32 v2, v2, v3
	s_waitcnt lgkmcnt(0)
; #define LAS __attribute__((address_space(3)))
; __device__ __forceinline__ float wave_max(float v) { v = fmaxf(v, dpp_f<0xB1>(v)); v = fmaxf(v, dpp_f<0x4E>(v)); v = fmaxf(v, dpp_f<0x141>(v)); v = fmaxf(v, dpp_f<0x140>(v)); v = fmaxf(v, xor_sw<16>(v)); return max_x32(v); }
; __device__ __forceinline__ float q8_row16(const float (&o)[16], unsigned char* qrow, int lane) {
;     float am = 0.f;
; #pragma unroll
;     for (int i = 0; i < 16; ++i) am = fmaxf(am, fabsf(o[i]));
;     am = wave_max(am);
;     const float qs = am > 0.f ? am * (1.0f / 127.0f) : 1.0f, qinv = 1.0f / qs;
; #pragma unroll
;     for (int hf = 0; hf < 2; ++hf) { u32x2 q; q.x = q8x4(o[8 * hf], o[8 * hf + 1], o[8 * hf + 2], o[8 * hf + 3], qinv); q.y = q8x4(o[8 * hf + 4], o[8 * hf + 5], o[8 * hf + 6], o[8 * hf + 7], qinv);
;         *(u32x2*)(qrow + 512 * hf + 8 * lane) = q; }
;     return qs;
; }
; __global__ void __launch_bounds__(NWAVES * 64, 2) mk_fwd(Args args) {
;     ...
;                 __syncthreads();
;                 {
;                     f32x4 a0 = (f32x4){0.f, 0.f, 0.f, 0.f}, a1 = (f32x4){0.f, 0.f, 0.f, 0.f};
; #pragma unroll
;                     for (int ks = 0; ks < 4; ++ks) { const LAS float* xp = XL + tk * XS + 128 * wave + 32 * ks + 8 * kq; const f32x4 p = *(const LAS f32x4*)xp, q = *(const LAS f32x4*)(xp + 4);
;                         const float f[8] = {p[0], p[1], p[2], p[3], q[0], q[1], q[2], q[3]}; bf16x8 xh, xl; split8(f, xh, xl);
;                         a0 = __builtin_amdgcn_mfma_f32_16x16x32_bf16(xh, rwh[ks][0], a0, 0, 0, 0); a1 = __builtin_amdgcn_mfma_f32_16x16x32_bf16(xh, rwh[ks][1], a1, 0, 0, 0);
;                         a0 = __builtin_amdgcn_mfma_f32_16x16x32_bf16(xh, rwl[ks][0], a0, 0, 0, 0); a1 = __builtin_amdgcn_mfma_f32_16x16x32_bf16(xh, rwl[ks][1], a1, 0, 0, 0);
;                         a0 = __builtin_amdgcn_mfma_f32_16x16x32_bf16(xl, rwh[ks][0], a0, 0, 0, 0); a1 = __builtin_amdgcn_mfma_f32_16x16x32_bf16(xl, rwh[ks][1], a1, 0, 0, 0); }
	v_mov_b32_e32 v3, v2
	s_nop 1
	v_permlane16_swap_b32_e32 v2, v3
	v_max_f32_e32 v1, v3, v3
	v_max_f32_e32 v1, v2, v1
	v_mov_b32_e32 v2, v1
	s_nop 1
	v_permlane32_swap_b32_e32 v1, v2
	v_max_f32_e32 v2, v2, v2
	v_max_f32_e32 v1, v1, v1
	v_max_f32_e32 v1, v1, v2
	v_mul_f32_e32 v2, 0x3c010204, v1
	v_cmp_lt_f32_e32 vcc, 0, v1
	s_nop 1
	v_cndmask_b32_e32 v1, 1.0, v2, vcc
	v_div_scale_f32 v2, s[6:7], v1, v1, 1.0
	v_rcp_f32_e32 v3, v2
	s_add_i32 s6, s10, 1
	s_ashr_i32 s7, s6, 31
	s_lshl_b64 s[6:7], s[6:7], 10
	v_fma_f32 v124, -v2, v3, 1.0
	v_fmac_f32_e32 v3, v124, v3
	v_div_scale_f32 v124, vcc, 1.0, v1, 1.0
	v_mul_f32_e32 v125, v124, v3
	v_fma_f32 v126, -v2, v125, v124
	v_fmac_f32_e32 v125, v126, v3
	v_fma_f32 v2, -v2, v125, v124
	v_div_fmas_f32 v2, v2, v3, v125
	v_div_fixup_f32 v124, v2, v1, 1.0
	v_fmaak_f32 v120, v120, v124, 0x4b400000
	v_fmaak_f32 v121, v121, v124, 0x4b400000
	v_fmaak_f32 v122, v122, v124, 0x4b400000
	v_fmaak_f32 v123, v123, v124, 0x4b400000
	v_fmaak_f32 v116, v116, v124, 0x4b400000
	v_fmaak_f32 v117, v117, v124, 0x4b400000
	v_fmaak_f32 v118, v118, v124, 0x4b400000
	v_fmaak_f32 v119, v119, v124, 0x4b400000
	v_fmaak_f32 v90, v90, v124, 0x4b400000
	v_fmaak_f32 v91, v91, v124, 0x4b400000
	v_fmaak_f32 v92, v92, v124, 0x4b400000
	v_fmaak_f32 v93, v93, v124, 0x4b400000
	v_fmaak_f32 v86, v86, v124, 0x4b400000
	v_fmaak_f32 v87, v87, v124, 0x4b400000
	v_fmaak_f32 v88, v88, v124, 0x4b400000
	v_fmaak_f32 v89, v89, v124, 0x4b400000
	v_perm_b32 v122, v123, v122, s61
	v_perm_b32 v120, v121, v120, s61
	v_perm_b32 v118, v119, v118, s61
	v_perm_b32 v116, v117, v116, s61
	v_perm_b32 v92, v93, v92, s61
	v_perm_b32 v90, v91, v90, s61
	v_perm_b32 v88, v89, v88, s61
	v_perm_b32 v86, v87, v86, s61
	v_lshl_add_u64 v[2:3], v[100:101], 0, s[6:7]
	v_perm_b32 v120, v122, v120, s79
	v_perm_b32 v121, v118, v116, s79
	v_perm_b32 v90, v92, v90, s79
	v_perm_b32 v91, v88, v86, s79
	global_store_dwordx2 v[2:3], v[120:121], off
	global_store_dwordx2 v[2:3], v[90:91], off offset:512
	s_and_saveexec_b64 s[6:7], s[4:5]
	v_mov_b32_e32 v2, s13
	ds_write_b32 v2, v1
	s_or_b64 exec, exec, s[6:7]
	s_waitcnt lgkmcnt(0)
	s_barrier
	ds_read_b128 v[86:89], v114
	ds_read_b128 v[90:93], v114 offset:16
	s_waitcnt lgkmcnt(1)
	v_cvt_pk_bf16_f32 v116, v86, v87
	v_cvt_pk_bf16_f32 v117, v88, v89
	s_waitcnt lgkmcnt(0)
	v_cvt_pk_bf16_f32 v118, v90, v91
	v_cvt_pk_bf16_f32 v119, v92, v93
	v_lshlrev_b32_e32 v2, 16, v116
	v_and_b32_e32 v3, 0xffff0000, v116
	v_pk_add_f32 v[2:3], v[86:87], v[2:3] neg_lo:[0,1] neg_hi:[0,1]
	v_lshlrev_b32_e32 v86, 16, v117
	v_and_b32_e32 v87, 0xffff0000, v117
	v_lshlrev_b32_e32 v120, 16, v118
	v_and_b32_e32 v121, 0xffff0000, v118
	v_pk_add_f32 v[124:125], v[88:89], v[86:87] neg_lo:[0,1] neg_hi:[0,1]
	v_mfma_f32_16x16x32_bf16 v[86:89], v[116:119], v[62:65], 0
	v_add_f32_e64 v126, v90, -v120
	v_add_f32_e64 v127, v91, -v121
	v_lshlrev_b32_e32 v90, 16, v119
	v_and_b32_e32 v91, 0xffff0000, v119
	v_mfma_f32_16x16x32_bf16 v[120:123], v[116:119], v[54:57], 0
	v_add_f32_e64 v128, v92, -v90
	v_add_f32_e64 v129, v93, -v91
	v_cvt_pk_bf16_f32 v90, v2, v3
	v_cvt_pk_bf16_f32 v91, v124, v125
	v_mfma_f32_16x16x32_bf16 v[86:89], v[116:119], v[66:69], v[86:89]
	v_cvt_pk_bf16_f32 v92, v126, v127
	v_cvt_pk_bf16_f32 v93, v128, v129
	v_mfma_f32_16x16x32_bf16 v[116:119], v[116:119], v[58:61], v[120:123]
	s_nop 2
	ds_read_b128 v[120:123], v114 offset:128
	ds_read_b128 v[124:127], v114 offset:144
	v_mfma_f32_16x16x32_bf16 v[86:89], v[90:93], v[62:65], v[86:89]
	v_mfma_f32_16x16x32_bf16 v[90:93], v[90:93], v[54:57], v[116:119]
	s_waitcnt lgkmcnt(1)
	s_nop 1
	v_cvt_pk_bf16_f32 v116, v120, v121
	v_cvt_pk_bf16_f32 v117, v122, v123
	s_waitcnt lgkmcnt(0)
	v_cvt_pk_bf16_f32 v118, v124, v125
	v_cvt_pk_bf16_f32 v119, v126, v127
	v_lshlrev_b32_e32 v2, 16, v116
	v_and_b32_e32 v3, 0xffff0000, v116
	v_pk_add_f32 v[2:3], v[120:121], v[2:3] neg_lo:[0,1] neg_hi:[0,1]
	v_lshlrev_b32_e32 v120, 16, v117
	v_and_b32_e32 v121, 0xffff0000, v117
	v_mfma_f32_16x16x32_bf16 v[86:89], v[116:119], v[46:49], v[86:89]
	v_add_f32_e64 v122, v122, -v120
	v_add_f32_e64 v123, v123, -v121
	v_lshlrev_b32_e32 v120, 16, v118
	v_and_b32_e32 v121, 0xffff0000, v118
	v_mfma_f32_16x16x32_bf16 v[90:93], v[116:119], v[38:41], v[90:93]
	v_add_f32_e64 v124, v124, -v120
	v_add_f32_e64 v125, v125, -v121
	v_lshlrev_b32_e32 v120, 16, v119
	v_and_b32_e32 v121, 0xffff0000, v119
	v_pk_add_f32 v[126:127], v[126:127], v[120:121] neg_lo:[0,1] neg_hi:[0,1]
	v_mfma_f32_16x16x32_bf16 v[86:89], v[116:119], v[50:53], v[86:89]
	v_cvt_pk_bf16_f32 v120, v2, v3
	v_cvt_pk_bf16_f32 v121, v122, v123
	v_cvt_pk_bf16_f32 v122, v124, v125
	v_mfma_f32_16x16x32_bf16 v[90:93], v[116:119], v[42:45], v[90:93]
	v_cvt_pk_bf16_f32 v123, v126, v127
	ds_read_b128 v[116:119], v114 offset:256
	ds_read_b128 v[124:127], v114 offset:272
	v_mfma_f32_16x16x32_bf16 v[86:89], v[120:123], v[46:49], v[86:89]
	v_mfma_f32_16x16x32_bf16 v[90:93], v[120:123], v[38:41], v[90:93]
	s_waitcnt lgkmcnt(1)
	v_cvt_pk_bf16_f32 v120, v116, v117
	v_cvt_pk_bf16_f32 v121, v118, v119
	s_waitcnt lgkmcnt(0)
; #define LAS __attribute__((address_space(3)))
; __global__ void __launch_bounds__(NWAVES * 64, 2) mk_fwd(Args args) {
;     ...
;                 {
;                     f32x4 a0 = (f32x4){0.f, 0.f, 0.f, 0.f}, a1 = (f32x4){0.f, 0.f, 0.f, 0.f};
; #pragma unroll
;                     for (int ks = 0; ks < 4; ++ks) { const LAS float* xp = XL + tk * XS + 128 * wave + 32 * ks + 8 * kq; const f32x4 p = *(const LAS f32x4*)xp, q = *(const LAS f32x4*)(xp + 4);
;                         const float f[8] = {p[0], p[1], p[2], p[3], q[0], q[1], q[2], q[3]}; bf16x8 xh, xl; split8(f, xh, xl);
;                         a0 = __builtin_amdgcn_mfma_f32_16x16x32_bf16(xh, rwh[ks][0], a0, 0, 0, 0); a1 = __builtin_amdgcn_mfma_f32_16x16x32_bf16(xh, rwh[ks][1], a1, 0, 0, 0);
;                         a0 = __builtin_amdgcn_mfma_f32_16x16x32_bf16(xh, rwl[ks][0], a0, 0, 0, 0); a1 = __builtin_amdgcn_mfma_f32_16x16x32_bf16(xh, rwl[ks][1], a1, 0, 0, 0);
;                         a0 = __builtin_amdgcn_mfma_f32_16x16x32_bf16(xl, rwh[ks][0], a0, 0, 0, 0); a1 = __builtin_amdgcn_mfma_f32_16x16x32_bf16(xl, rwh[ks][1], a1, 0, 0, 0); }
; #pragma unroll
;                     for (int r = 0; r < 4; ++r) { PART[(wave * 16 + 4 * kq + r) * 32 + tk] = a0[r]; PART[(wave * 16 + 4 * kq + r) * 32 + 16 + tk] = a1[r]; }
;                 }
;                 __syncthreads();
	v_cvt_pk_bf16_f32 v122, v124, v125
	v_cvt_pk_bf16_f32 v123, v126, v127
	v_lshlrev_b32_e32 v2, 16, v120
	v_and_b32_e32 v3, 0xffff0000, v120
	v_pk_add_f32 v[2:3], v[116:117], v[2:3] neg_lo:[0,1] neg_hi:[0,1]
	v_lshlrev_b32_e32 v116, 16, v121
	v_and_b32_e32 v117, 0xffff0000, v121
	v_mfma_f32_16x16x32_bf16 v[86:89], v[120:123], v[28:31], v[86:89]
	v_add_f32_e64 v118, v118, -v116
	v_add_f32_e64 v119, v119, -v117
	v_lshlrev_b32_e32 v116, 16, v122
	v_and_b32_e32 v117, 0xffff0000, v122
	v_mfma_f32_16x16x32_bf16 v[90:93], v[120:123], v[20:23], v[90:93]
	v_add_f32_e64 v124, v124, -v116
	v_add_f32_e64 v125, v125, -v117
	v_lshlrev_b32_e32 v116, 16, v123
	v_and_b32_e32 v117, 0xffff0000, v123
	v_pk_add_f32 v[126:127], v[126:127], v[116:117] neg_lo:[0,1] neg_hi:[0,1]
	v_mfma_f32_16x16x32_bf16 v[86:89], v[120:123], v[34:37], v[86:89]
	v_cvt_pk_bf16_f32 v116, v2, v3
	v_cvt_pk_bf16_f32 v117, v118, v119
	v_cvt_pk_bf16_f32 v118, v124, v125
	v_mfma_f32_16x16x32_bf16 v[90:93], v[120:123], v[24:27], v[90:93]
	v_cvt_pk_bf16_f32 v119, v126, v127
	ds_read_b128 v[120:123], v114 offset:384
	ds_read_b128 v[124:127], v114 offset:400
	v_mfma_f32_16x16x32_bf16 v[86:89], v[116:119], v[28:31], v[86:89]
	v_mfma_f32_16x16x32_bf16 v[90:93], v[116:119], v[20:23], v[90:93]
	s_waitcnt lgkmcnt(1)
	v_cvt_pk_bf16_f32 v116, v120, v121
	v_cvt_pk_bf16_f32 v117, v122, v123
	s_waitcnt lgkmcnt(0)
	v_cvt_pk_bf16_f32 v118, v124, v125
	v_cvt_pk_bf16_f32 v119, v126, v127
	v_lshlrev_b32_e32 v2, 16, v116
	v_and_b32_e32 v3, 0xffff0000, v116
	v_pk_add_f32 v[2:3], v[120:121], v[2:3] neg_lo:[0,1] neg_hi:[0,1]
	v_lshlrev_b32_e32 v120, 16, v117
	v_and_b32_e32 v121, 0xffff0000, v117
	v_pk_add_f32 v[122:123], v[122:123], v[120:121] neg_lo:[0,1] neg_hi:[0,1]
	v_mfma_f32_16x16x32_bf16 v[86:89], v[116:119], v[12:15], v[86:89]
	v_lshlrev_b32_e32 v120, 16, v118
	v_and_b32_e32 v121, 0xffff0000, v118
	v_pk_add_f32 v[124:125], v[124:125], v[120:121] neg_lo:[0,1] neg_hi:[0,1]
	v_mfma_f32_16x16x32_bf16 v[90:93], v[116:119], v[4:7], v[90:93]
	v_lshlrev_b32_e32 v120, 16, v119
	v_and_b32_e32 v121, 0xffff0000, v119
	v_pk_add_f32 v[126:127], v[126:127], v[120:121] neg_lo:[0,1] neg_hi:[0,1]
	v_cvt_pk_bf16_f32 v120, v2, v3
	v_cvt_pk_bf16_f32 v121, v122, v123
	v_cvt_pk_bf16_f32 v122, v124, v125
	v_cvt_pk_bf16_f32 v123, v126, v127
	v_mfma_f32_16x16x32_bf16 v[86:89], v[116:119], v[16:19], v[86:89]
	v_mfma_f32_16x16x32_bf16 v[90:93], v[116:119], v[8:11], v[90:93]
	v_mfma_f32_16x16x32_bf16 v[86:89], v[120:123], v[12:15], v[86:89]
	v_mfma_f32_16x16x32_bf16 v[90:93], v[120:123], v[4:7], v[90:93]
	s_nop 7
	ds_write2_b32 v115, v86, v90 offset1:16
	ds_write2_b32 v115, v87, v91 offset0:32 offset1:48
	ds_write2_b32 v115, v88, v92 offset0:64 offset1:80
	ds_write2_b32 v115, v89, v93 offset0:96 offset1:112
	s_waitcnt lgkmcnt(0)
	s_barrier
; #define LAS __attribute__((address_space(3)))
; __global__ void __launch_bounds__(NWAVES * 64, 2) mk_fwd(Args args) {
;     ...
;                 {   const int tq = tid >> 5, e = tid & 31; float s = rb[e];
; #pragma unroll
;                     for (int w = 0; w < 8; ++w) s += PART[(w * 16 + tq) * 32 + e];
;                     const unsigned ub = __float_as_uint(s), key = (((ub >> 31) ? ~ub : (ub | 0x80000000u)) & ~31u) | (unsigned)(31 - e);
;                     ((LAS unsigned*)LOG)[tq * 32 + e] = key;
;                     asm volatile("s_waitcnt lgkmcnt(0)" ::: "memory");
;                     int rank = 0;
; #pragma unroll
;                     for (int q = 0; q < 8; ++q) { const u32x4 t4 = *(const LAS u32x4*)((LAS unsigned*)LOG + tq * 32 + 4 * q);
; #pragma unroll
;                         for (int r = 0; r < 4; ++r) rank += (t4[r] > key) ? 1 : 0; }
;                     if (rank < 4) TOP[tq * 4 + rank] = s;
;                     asm volatile("s_waitcnt lgkmcnt(0)" ::: "memory");
;                     if (rank < 4) {
;                         const f32x4 tv = *(const LAS f32x4*)(TOP + tq * 4);
;                         const float es = 1.0f + __expf(tv[1] - tv[0]) + __expf(tv[2] - tv[0]) + __expf(tv[3] - tv[0]);
;                         const float wgt = __expf(s - tv[0]) * (1.0f / es);
;                         const int lp = atomicAdd((int*)(LCNT + e), 1);
;                         REC[(nbatch * 16 + tq) * 4 + rank] = (i32x4){e, lp, __float_as_int(wgt), bi * 16 + tq}; }
	ds_read2st64_b32 v[2:3], v108 offset1:8
	ds_read2st64_b32 v[86:87], v108 offset0:16 offset1:24
	ds_read2st64_b32 v[88:89], v108 offset0:32 offset1:40
	ds_read2st64_b32 v[90:91], v108 offset0:48 offset1:56
	s_waitcnt lgkmcnt(3)
	v_add_f32_e32 v1, v249, v2
	v_add_f32_e32 v1, v1, v3
	s_waitcnt lgkmcnt(2)
	v_add_f32_e32 v1, v1, v86
	v_add_f32_e32 v1, v1, v87
	s_waitcnt lgkmcnt(1)
	v_add_f32_e32 v1, v1, v88
	v_add_f32_e32 v1, v1, v89
	s_waitcnt lgkmcnt(0)
	v_add_f32_e32 v1, v1, v90
	v_add_f32_e32 v1, v1, v91
	v_not_b32_e32 v2, v1
	v_or_b32_e32 v3, 0x80000000, v1
	v_cmp_gt_i32_e32 vcc, 0, v1
	s_nop 1
	v_cndmask_b32_e32 v2, v3, v2, vcc
	v_and_b32_e32 v2, 0xffffffe0, v2
	v_bitop3_b32 v2, v2, 31, v0 bitop3:0x36
	ds_write_b32 v109, v2
	s_waitcnt lgkmcnt(0)
	ds_read_b128 v[86:89], v111
	ds_read_b128 v[90:93], v111 offset:16
	ds_read_b128 v[116:119], v111 offset:32
	ds_read_b128 v[120:123], v111 offset:48
	s_waitcnt lgkmcnt(3)
	v_cmp_gt_u32_e32 vcc, v87, v2
	s_nop 1
	v_cndmask_b32_e64 v3, 0, 1, vcc
	v_cmp_gt_u32_e32 vcc, v88, v2
	s_nop 1
	v_cndmask_b32_e64 v87, 0, 1, vcc
	s_waitcnt lgkmcnt(2)
	v_cmp_gt_u32_e32 vcc, v90, v2
	s_nop 1
	v_cndmask_b32_e64 v88, 0, 1, vcc
	v_cmp_gt_u32_e32 vcc, v86, v2
	s_nop 1
	v_addc_co_u32_e32 v3, vcc, 0, v3, vcc
	v_cmp_gt_u32_e32 vcc, v89, v2
	s_nop 1
	v_addc_co_u32_e32 v3, vcc, v3, v87, vcc
	v_cmp_gt_u32_e32 vcc, v91, v2
	s_nop 1
	v_addc_co_u32_e32 v3, vcc, v3, v88, vcc
	v_cmp_gt_u32_e32 vcc, v92, v2
	s_nop 1
	v_cndmask_b32_e64 v86, 0, 1, vcc
	v_cmp_gt_u32_e32 vcc, v93, v2
	s_nop 1
	v_addc_co_u32_e32 v3, vcc, v3, v86, vcc
	s_waitcnt lgkmcnt(1)
	v_cmp_gt_u32_e32 vcc, v116, v2
	s_nop 1
	v_cndmask_b32_e64 v86, 0, 1, vcc
	v_cmp_gt_u32_e32 vcc, v117, v2
	s_nop 1
	v_addc_co_u32_e32 v3, vcc, v3, v86, vcc
	v_cmp_gt_u32_e32 vcc, v118, v2
	s_nop 1
	v_cndmask_b32_e64 v86, 0, 1, vcc
	v_cmp_gt_u32_e32 vcc, v119, v2
	s_nop 1
	v_addc_co_u32_e32 v3, vcc, v3, v86, vcc
	s_waitcnt lgkmcnt(0)
	v_cmp_gt_u32_e32 vcc, v120, v2
	s_nop 1
	v_cndmask_b32_e64 v86, 0, 1, vcc
	v_cmp_gt_u32_e32 vcc, v121, v2
	s_nop 1
	v_addc_co_u32_e32 v3, vcc, v3, v86, vcc
	ds_read_b128 v[86:89], v111 offset:64
	v_cmp_gt_u32_e32 vcc, v122, v2
	s_nop 1
	v_cndmask_b32_e64 v90, 0, 1, vcc
	v_cmp_gt_u32_e32 vcc, v123, v2
	s_nop 1
	v_addc_co_u32_e32 v3, vcc, v3, v90, vcc
	ds_read_b128 v[90:93], v111 offset:80
	s_waitcnt lgkmcnt(1)
	v_cmp_gt_u32_e32 vcc, v86, v2
	s_nop 1
	v_cndmask_b32_e64 v86, 0, 1, vcc
	v_cmp_gt_u32_e32 vcc, v87, v2
	s_nop 1
	v_addc_co_u32_e32 v3, vcc, v3, v86, vcc
	v_cmp_gt_u32_e32 vcc, v88, v2
	s_nop 1
	v_cndmask_b32_e64 v86, 0, 1, vcc
	v_cmp_gt_u32_e32 vcc, v89, v2
	s_nop 1
	v_addc_co_u32_e32 v3, vcc, v3, v86, vcc
	s_waitcnt lgkmcnt(0)
	v_cmp_gt_u32_e32 vcc, v90, v2
	s_nop 1
	v_cndmask_b32_e64 v86, 0, 1, vcc
	v_cmp_gt_u32_e32 vcc, v91, v2
	s_nop 1
	v_addc_co_u32_e32 v3, vcc, v3, v86, vcc
	ds_read_b128 v[86:89], v111 offset:96
	v_cmp_gt_u32_e32 vcc, v92, v2
	s_nop 1
	v_cndmask_b32_e64 v90, 0, 1, vcc
	v_cmp_gt_u32_e32 vcc, v93, v2
	s_nop 1
	v_addc_co_u32_e32 v3, vcc, v3, v90, vcc
	ds_read_b128 v[90:93], v111 offset:112
	s_waitcnt lgkmcnt(1)
	v_cmp_gt_u32_e32 vcc, v86, v2
	s_nop 1
	v_cndmask_b32_e64 v86, 0, 1, vcc
	v_cmp_gt_u32_e32 vcc, v87, v2
	s_nop 1
	v_addc_co_u32_e32 v3, vcc, v3, v86, vcc
	v_cmp_gt_u32_e32 vcc, v88, v2
	s_nop 1
	v_cndmask_b32_e64 v86, 0, 1, vcc
	v_cmp_gt_u32_e32 vcc, v89, v2
	s_nop 1
	v_addc_co_u32_e32 v3, vcc, v3, v86, vcc
	s_waitcnt lgkmcnt(0)
	v_cmp_gt_u32_e32 vcc, v90, v2
	s_nop 1
	v_cndmask_b32_e64 v86, 0, 1, vcc
	v_cmp_gt_u32_e32 vcc, v91, v2
	s_nop 1
	v_addc_co_u32_e32 v3, vcc, v3, v86, vcc
	v_cmp_gt_u32_e32 vcc, v92, v2
	s_nop 1
	v_cndmask_b32_e64 v86, 0, 1, vcc
	v_cmp_gt_u32_e32 vcc, v93, v2
	s_nop 1
	v_addc_co_u32_e32 v86, vcc, v3, v86, vcc
	v_cmp_gt_u32_e32 vcc, 4, v86
	s_and_saveexec_b64 s[6:7], vcc
	v_lshl_add_u32 v2, v86, 2, v112
	ds_write_b32 v2, v1
	s_or_b64 exec, exec, s[6:7]
	s_waitcnt lgkmcnt(0)
	s_and_saveexec_b64 s[6:7], vcc
	s_cbranch_execz .LBB0_493
	ds_read_b128 v[88:91], v112
	v_lshl_add_u32 v86, v86, 4, v32
	s_waitcnt lgkmcnt(0)
	v_sub_f32_e32 v2, v89, v88
	v_sub_f32_e32 v3, v90, v88
	v_mul_f32_e32 v2, 0x3fb8aa3b, v2
	v_sub_f32_e32 v87, v91, v88
	v_mul_f32_e32 v3, 0x3fb8aa3b, v3
	v_exp_f32_e32 v2, v2
	v_mul_f32_e32 v87, 0x3fb8aa3b, v87
	v_exp_f32_e32 v3, v3
	v_exp_f32_e32 v87, v87
	v_add_f32_e32 v2, 1.0, v2
	v_sub_f32_e32 v1, v1, v88
	v_add_f32_e32 v2, v3, v2
	v_add_f32_e32 v2, v87, v2
	v_div_scale_f32 v3, s[10:11], v2, v2, 1.0
	v_rcp_f32_e32 v87, v3
	v_mul_f32_e32 v1, 0x3fb8aa3b, v1
	v_exp_f32_e32 v88, v1
	v_readlane_b32 s10, v255, 36
	v_fma_f32 v1, -v3, v87, 1.0
	v_fmac_f32_e32 v87, v1, v87
	v_div_scale_f32 v1, vcc, 1.0, v2, 1.0
	v_mul_f32_e32 v89, v1, v87
	v_fma_f32 v90, -v3, v89, v1
	v_fmac_f32_e32 v89, v90, v87
	v_fma_f32 v1, -v3, v89, v1
	v_div_fmas_f32 v3, v1, v87, v89
	ds_add_rtn_u32 v1, v110, v203
	v_div_fixup_f32 v2, v3, v2, 1.0
	v_mul_f32_e32 v2, v88, v2
	v_add_u32_e32 v3, s10, v95
	s_waitcnt lgkmcnt(0)
	ds_write_b128 v86, v[0:3]

; __global__ void __launch_bounds__(NWAVES * 64, 2) mk_fwd(Args args) {
;     ...
;             auto tok_of = [&](int t0, int j) { return (j == 0 || t0 + NGW >= T) ? t0 : t0 + NGW; };
;             auto load_raw = [&](int t0) { return INFO[(size_t)tok_of(t0, (lane >> 2) & 1) * 4 + (lane & 3)]; };
;             auto unpack_raw = [&](const i32x4& raw, int (&e)[2][4], int (&p)[2][4], float (&gq)[2][4]) {
; #pragma unroll
;                 for (int j = 0; j < 2; ++j)
; #pragma unroll
;                     for (int k = 0; k < 4; ++k) { e[j][k] = __builtin_amdgcn_readlane(raw.x, 4 * j + k); p[j][k] = __builtin_amdgcn_readlane(raw.y, 4 * j + k);
;                         gq[j][k] = __int_as_float(__builtin_amdgcn_readlane(raw.z, 4 * j + k)) * (1.0f / 16.0f); } };
;             auto load_rows = [&](int t0, const int (&e)[2][4], const int (&p)[2][4], u32x4 (&xr)[2][2], u32x2 (&yr)[2][4][2]) {
; #pragma unroll
;                 for (int j = 0; j < 2; ++j) { const int t = tok_of(t0, j);
;                     xr[j][0] = *(const u32x4*)(YB + (size_t)t * D + 8 * lane); xr[j][1] = *(const u32x4*)(YB + (size_t)t * D + 512 + 8 * lane);
; #pragma unroll
;                     for (int k = 0; k < 4; ++k) { const unsigned char* yp = (const unsigned char*)YS + ((size_t)TB[e[j][k]] * 256 + p[j][k]) * D;
;                         yr[j][k][0] = *(const u32x2*)(yp + 8 * lane); yr[j][k][1] = *(const u32x2*)(yp + 512 + 8 * lane); } } };
;             u32x4 xr[2][2], xrn[2][2]; u32x2 yr[2][4][2], yrn[2][4][2]; float gt[2][4];
;             i32x4 raw = load_raw(gw);
;             { int e0[2][4], p0[2][4]; unpack_raw(raw, e0, p0, gt); load_rows(gw, e0, p0, xr, yr); }
;             raw = load_raw((gw + 2 * NGW < T) ? gw + 2 * NGW : gw);
;             for (int t0 = gw; t0 < T; t0 += 2 * NGW) {
;                 int tt[2]; tt[0] = t0; tt[1] = tok_of(t0, 1);
;                 const int t1 = (t0 + 2 * NGW < T) ? t0 + 2 * NGW : t0, t2 = (t1 + 2 * NGW < T) ? t1 + 2 * NGW : t1;
;                 int en[2][4], pn[2][4]; float gn[2][4];
;                 unpack_raw(raw, en, pn, gn);
;                 load_rows(t1, en, pn, xrn, yrn);
;                 raw = load_raw(t2);
.LBB0_707:
	v_readlane_b32 s7, v253, 56
	s_add_i32 s6, s7, s10
	s_cmp_lt_i32 s6, 0x8000
	s_cselect_b32 s18, s6, s10
	s_add_i32 s6, s18, s7
	s_cmp_lt_i32 s6, 0x8000
	s_cselect_b32 s11, s6, s18
	v_readlane_b32 s7, v0, 0
	s_ashr_i32 s19, s18, 31
	s_lshl_b64 s[42:43], s[18:19], 11
	s_lshl_b32 s7, s7, 2
	s_waitcnt vmcnt(0)
	v_mov_b64_e32 v[30:31], v[18:19]
	v_mov_b64_e32 v[36:37], v[14:15]
	v_readlane_b32 s34, v1, 0
	v_readlane_b32 s13, v0, 1
	v_readlane_b32 s40, v1, 1
	v_readlane_b32 s15, v0, 2
	v_readlane_b32 s22, v1, 2
	v_readlane_b32 s17, v0, 3
	v_readlane_b32 s20, v1, 3
	v_readlane_b32 s33, v0, 4
	v_readlane_b32 s16, v1, 4
	v_readlane_b32 s38, v0, 5
	v_readlane_b32 s14, v1, 5
	v_readlane_b32 s44, v0, 6
	v_readlane_b32 s12, v1, 6
	v_readlane_b32 s45, v0, 7
	v_readlane_b32 s6, v1, 7
	v_lshl_add_u64 v[0:1], v[140:141], 0, s[42:43]
	s_add_i32 s7, s67, s7
	v_mov_b64_e32 v[28:29], v[16:17]
	v_mov_b64_e32 v[34:35], v[12:13]
	global_load_dwordx4 v[16:19], v[0:1], off nt
	global_load_dwordx4 v[12:15], v[0:1], off offset:1024 nt
	v_mov_b32_e32 v0, s7
	s_lshl_b32 s7, s13, 2
	s_add_i32 s7, s67, s7
	v_mov_b32_e32 v1, s7
	s_lshl_b32 s7, s15, 2
	ds_read_b32 v0, v0
	s_add_i32 s7, s67, s7
	v_mov_b32_e32 v3, s7
	s_lshl_b32 s7, s17, 2
	v_mov_b64_e32 v[26:27], v[6:7]
	s_add_i32 s7, s67, s7
	v_mov_b64_e32 v[24:25], v[4:5]
	v_mul_f32_e32 v44, s24, v224
	v_mul_f32_e32 v42, s25, v224
	v_mul_f32_e32 v40, s26, v224
	v_mul_f32_e32 v38, s27, v224
	v_mul_f32_e32 v150, s28, v224
	v_mul_f32_e32 v148, s29, v224
	v_mul_f32_e32 v146, s30, v224
	v_mul_f32_e32 v32, s31, v224
	v_readlane_b32 s24, v2, 0
	v_readlane_b32 s25, v2, 1
	v_readlane_b32 s26, v2, 2
	v_readlane_b32 s27, v2, 3
	v_readlane_b32 s28, v2, 4
	v_readlane_b32 s29, v2, 5
	v_readlane_b32 s30, v2, 6
	v_readlane_b32 s31, v2, 7
	v_mov_b32_e32 v5, s7
	ds_read_b32 v2, v1
	ds_read_b32 v4, v3
	ds_read_b32 v6, v5
	s_waitcnt lgkmcnt(3)
	v_ashrrev_i32_e32 v1, 31, v0
	s_ashr_i32 s35, s34, 31
	v_lshlrev_b64 v[0:1], 18, v[0:1]
	s_waitcnt lgkmcnt(2)
	v_ashrrev_i32_e32 v3, 31, v2
	s_lshl_b64 s[34:35], s[34:35], 10
	v_lshl_add_u64 v[0:1], s[52:53], 0, v[0:1]
	s_ashr_i32 s41, s40, 31
	v_lshlrev_b64 v[2:3], 18, v[2:3]
	v_lshl_add_u64 v[0:1], v[0:1], 0, s[34:35]
	s_lshl_b64 s[34:35], s[40:41], 10
	v_lshl_add_u64 v[2:3], s[52:53], 0, v[2:3]
	s_ashr_i32 s23, s22, 31
	s_ashr_i32 s21, s20, 31
	v_lshl_add_u64 v[0:1], v[0:1], 0, v[94:95]
	v_lshl_add_u64 v[2:3], v[2:3], 0, s[34:35]
	s_waitcnt lgkmcnt(1)
	v_ashrrev_i32_e32 v5, 31, v4
	s_lshl_b64 s[22:23], s[22:23], 10
	s_lshl_b64 s[20:21], s[20:21], 10
	s_add_i32 s7, s18, s82
	v_mov_b64_e32 v[60:61], v[144:145]
	v_mov_b64_e32 v[52:53], v[142:143]
	v_mov_b64_e32 v[58:59], v[138:139]
	v_mov_b64_e32 v[50:51], v[136:137]
	v_lshl_add_u64 v[2:3], v[2:3], 0, v[94:95]
	global_load_dwordx2 v[144:145], v[0:1], off nt
	global_load_dwordx2 v[142:143], v[0:1], off offset:512 nt
	global_load_dwordx2 v[138:139], v[2:3], off nt
	global_load_dwordx2 v[136:137], v[2:3], off offset:512 nt
	v_lshlrev_b64 v[0:1], 18, v[4:5]
	s_waitcnt lgkmcnt(0)
	v_ashrrev_i32_e32 v7, 31, v6
	s_cmpk_gt_i32 s7, 0x7fff
	v_lshl_add_u64 v[0:1], s[52:53], 0, v[0:1]
	v_lshlrev_b64 v[2:3], 18, v[6:7]
	s_cselect_b32 s18, s18, s7
	v_lshl_add_u64 v[0:1], v[0:1], 0, s[22:23]
	v_lshl_add_u64 v[2:3], s[52:53], 0, v[2:3]
	s_ashr_i32 s19, s18, 31
	v_lshl_add_u64 v[0:1], v[0:1], 0, v[94:95]
	v_lshl_add_u64 v[2:3], v[2:3], 0, s[20:21]
	s_lshl_b64 s[18:19], s[18:19], 11
	s_lshl_b32 s7, s33, 2
	v_mov_b64_e32 v[56:57], v[130:131]
	v_mov_b64_e32 v[48:49], v[128:129]
	v_mov_b64_e32 v[54:55], v[126:127]
	v_mov_b64_e32 v[46:47], v[124:125]
	v_mov_b64_e32 v[22:23], v[10:11]
	v_lshl_add_u64 v[2:3], v[2:3], 0, v[94:95]
	global_load_dwordx2 v[130:131], v[0:1], off nt
	global_load_dwordx2 v[128:129], v[0:1], off offset:512 nt
	global_load_dwordx2 v[126:127], v[2:3], off nt
	global_load_dwordx2 v[124:125], v[2:3], off offset:512 nt
	v_lshl_add_u64 v[0:1], v[140:141], 0, s[18:19]
	s_add_i32 s7, s67, s7
	v_mov_b64_e32 v[20:21], v[8:9]
	global_load_dwordx4 v[8:11], v[0:1], off nt
	global_load_dwordx4 v[4:7], v[0:1], off offset:1024 nt
	v_mov_b32_e32 v0, s7
	s_lshl_b32 s7, s38, 2
	s_add_i32 s7, s67, s7
	v_mov_b32_e32 v1, s7
	s_lshl_b32 s7, s44, 2
	ds_read_b32 v0, v0
	s_add_i32 s7, s67, s7
	v_mov_b32_e32 v3, s7
	s_lshl_b32 s7, s45, 2
	s_add_i32 s7, s67, s7
	v_mov_b32_e32 v39, s7
	ds_read_b32 v2, v1
	ds_read_b32 v62, v3
	ds_read_b32 v64, v39
	s_waitcnt lgkmcnt(3)
	v_ashrrev_i32_e32 v1, 31, v0
	s_ashr_i32 s17, s16, 31
	v_lshlrev_b64 v[0:1], 18, v[0:1]
	s_waitcnt lgkmcnt(2)
	v_ashrrev_i32_e32 v3, 31, v2
	s_lshl_b64 s[16:17], s[16:17], 10
	v_lshl_add_u64 v[0:1], s[52:53], 0, v[0:1]
	s_ashr_i32 s15, s14, 31
	v_lshlrev_b64 v[2:3], 18, v[2:3]
	v_lshl_add_u64 v[0:1], v[0:1], 0, s[16:17]
	s_lshl_b64 s[14:15], s[14:15], 10
	v_lshl_add_u64 v[2:3], s[52:53], 0, v[2:3]
	v_lshl_add_u64 v[0:1], v[0:1], 0, v[94:95]
	v_lshl_add_u64 v[2:3], v[2:3], 0, s[14:15]
	s_waitcnt lgkmcnt(1)
	v_ashrrev_i32_e32 v63, 31, v62
	v_mov_b64_e32 v[166:167], v[134:135]
	v_mov_b64_e32 v[158:159], v[132:133]
	v_mov_b64_e32 v[164:165], v[122:123]
	v_mov_b64_e32 v[156:157], v[120:121]
	v_lshl_add_u64 v[2:3], v[2:3], 0, v[94:95]
	global_load_dwordx2 v[134:135], v[0:1], off nt
	global_load_dwordx2 v[132:133], v[0:1], off offset:512 nt
	global_load_dwordx2 v[122:123], v[2:3], off nt
	global_load_dwordx2 v[120:121], v[2:3], off offset:512 nt
	s_ashr_i32 s13, s12, 31
	v_lshlrev_b64 v[0:1], 18, v[62:63]
	s_lshl_b64 s[12:13], s[12:13], 10
	v_lshl_add_u64 v[0:1], s[52:53], 0, v[0:1]
	s_waitcnt lgkmcnt(0)
; __global__ void __launch_bounds__(NWAVES * 64, 2) mk_fwd(Args args) {
;     ...
;             auto load_rows = [&](int t0, const int (&e)[2][4], const int (&p)[2][4], u32x4 (&xr)[2][2], u32x2 (&yr)[2][4][2]) {
; #pragma unroll
;                 for (int j = 0; j < 2; ++j) { const int t = tok_of(t0, j);
;                     xr[j][0] = *(const u32x4*)(YB + (size_t)t * D + 8 * lane); xr[j][1] = *(const u32x4*)(YB + (size_t)t * D + 512 + 8 * lane);
; #pragma unroll
;                     for (int k = 0; k < 4; ++k) { const unsigned char* yp = (const unsigned char*)YS + ((size_t)TB[e[j][k]] * 256 + p[j][k]) * D;
;                         yr[j][k][0] = *(const u32x2*)(yp + 8 * lane); yr[j][k][1] = *(const u32x2*)(yp + 512 + 8 * lane); } } };
;             u32x4 xr[2][2], xrn[2][2]; u32x2 yr[2][4][2], yrn[2][4][2]; float gt[2][4];
;             i32x4 raw = load_raw(gw);
;             { int e0[2][4], p0[2][4]; unpack_raw(raw, e0, p0, gt); load_rows(gw, e0, p0, xr, yr); }
;             raw = load_raw((gw + 2 * NGW < T) ? gw + 2 * NGW : gw);
;             for (int t0 = gw; t0 < T; t0 += 2 * NGW) {
;                 int tt[2]; tt[0] = t0; tt[1] = tok_of(t0, 1);
;                 const int t1 = (t0 + 2 * NGW < T) ? t0 + 2 * NGW : t0, t2 = (t1 + 2 * NGW < T) ? t1 + 2 * NGW : t1;
;                 int en[2][4], pn[2][4]; float gn[2][4];
;                 unpack_raw(raw, en, pn, gn);
;                 load_rows(t1, en, pn, xrn, yrn);
;                 raw = load_raw(t2);
;                 __builtin_amdgcn_sched_barrier(0);
;                 float o[2][16];
; #pragma unroll
;                 for (int j = 0; j < 2; ++j) {
;                     float v[16], x1[16];
; #pragma unroll
;                     for (int hf = 0; hf < 2; ++hf) { float f[8]; unpack8(xr[j][hf], f);
; #pragma unroll
;                         for (int i = 0; i < 8; ++i) v[8 * hf + i] = f[i]; }
;                     ln_row16(v, lng1, lnb1, lane, x1);
; #pragma unroll
;                     for (int hf = 0; hf < 2; ++hf) { float f[8];
; #pragma unroll
;                         for (int i = 0; i < 8; ++i) v[8 * hf + i] = ALPHA * x1[8 * hf + i];
; #pragma unroll
;                         for (int k = 0; k < 4; ++k) { unpack8_f8(yr[j][k][hf], f);
; #pragma unroll
;                             for (int i = 0; i < 8; ++i) v[8 * hf + i] += gt[j][k] * f[i]; } }
;                     ln_row16(v, lng, lnb, lane, o[j]);
	v_ashrrev_i32_e32 v65, 31, v64
	s_ashr_i32 s7, s6, 31
	v_lshl_add_u64 v[0:1], v[0:1], 0, s[12:13]
	v_lshlrev_b64 v[2:3], 18, v[64:65]
	s_lshl_b64 s[6:7], s[6:7], 10
	s_add_i32 s12, s11, s82
	v_lshl_add_u64 v[2:3], s[52:53], 0, v[2:3]
	s_cmpk_gt_i32 s12, 0x7fff
	v_lshl_add_u64 v[0:1], v[0:1], 0, v[94:95]
	v_lshl_add_u64 v[2:3], v[2:3], 0, s[6:7]
	s_cselect_b64 s[6:7], -1, 0
	v_mov_b64_e32 v[162:163], v[118:119]
	v_mov_b64_e32 v[154:155], v[116:117]
	v_mov_b64_e32 v[160:161], v[114:115]
	v_mov_b64_e32 v[152:153], v[112:113]
	v_lshl_add_u64 v[2:3], v[2:3], 0, v[94:95]
	global_load_dwordx2 v[118:119], v[0:1], off nt
	global_load_dwordx2 v[116:117], v[0:1], off offset:512 nt
	global_load_dwordx2 v[114:115], v[2:3], off nt
	global_load_dwordx2 v[112:113], v[2:3], off offset:512 nt
	v_mov_b32_e32 v0, s12
	v_mov_b32_e32 v1, s11
	s_or_b64 vcc, s[2:3], s[6:7]
	v_cndmask_b32_e32 v0, v0, v1, vcc
	v_ashrrev_i32_e32 v1, 31, v0
	v_lshlrev_b64 v[0:1], 6, v[0:1]
	v_lshl_add_u64 v[0:1], v[96:97], 0, v[0:1]
	global_load_dwordx4 v[0:3], v[0:1], off nt
	v_lshlrev_b32_e32 v62, 16, v37
	v_and_b32_e32 v63, 0xffff0000, v37
	v_lshlrev_b32_e32 v64, 16, v36
	v_and_b32_e32 v65, 0xffff0000, v36
	v_lshlrev_b32_e32 v36, 16, v35
	v_and_b32_e32 v37, 0xffff0000, v35
	v_lshlrev_b32_e32 v66, 16, v34
	v_and_b32_e32 v67, 0xffff0000, v34
	v_lshlrev_b32_e32 v70, 16, v28
	v_and_b32_e32 v71, 0xffff0000, v28
	s_waitcnt vmcnt(0)
	v_add_f32_e32 v3, v63, v62
	v_add_f32_e32 v28, v65, v64
	v_lshlrev_b32_e32 v34, 16, v31
	v_and_b32_e32 v35, 0xffff0000, v31
	v_lshlrev_b32_e32 v68, 16, v30
	v_and_b32_e32 v69, 0xffff0000, v30
	v_lshlrev_b32_e32 v30, 16, v29
	v_and_b32_e32 v31, 0xffff0000, v29
	v_add_f32_e32 v3, v28, v3
	v_add_f32_e32 v28, v37, v36
	v_add_f32_e32 v29, v67, v66
	v_add_f32_e32 v28, v29, v28
	v_add_f32_e32 v3, v28, v3
	v_add_f32_e32 v28, v35, v34
	v_add_f32_e32 v29, v69, v68
	v_add_f32_e32 v28, v29, v28
	v_add_f32_e32 v29, v31, v30
	v_add_f32_e32 v39, v71, v70
	v_add_f32_e32 v29, v39, v29
	v_add_f32_e32 v28, v29, v28
	v_add_f32_e32 v3, v28, v3
	s_mov_b32 s11, 0xf800000
	v_cvt_pk_f32_fp8_sdwa v[178:179], v60 src0_sel:WORD_1
	v_add_f32_dpp v3, v3, v3 quad_perm:[1,0,3,2] row_mask:0xf bank_mask:0xf bound_ctrl:1
	v_cvt_pk_f32_fp8_e32 v[180:181], v61
	v_cvt_pk_f32_fp8_e32 v[182:183], v58
	v_add_f32_dpp v3, v3, v3 quad_perm:[2,3,0,1] row_mask:0xf bank_mask:0xf bound_ctrl:1
	v_cvt_pk_f32_fp8_sdwa v[184:185], v58 src0_sel:WORD_1
	v_cvt_pk_f32_fp8_e32 v[186:187], v59
	v_add_f32_dpp v3, v3, v3 row_half_mirror row_mask:0xf bank_mask:0xf bound_ctrl:1
	v_cvt_pk_f32_fp8_sdwa v[58:59], v59 src0_sel:WORD_1
	v_cvt_pk_f32_fp8_e32 v[188:189], v56
	v_add_f32_dpp v3, v3, v3 row_mirror row_mask:0xf bank_mask:0xf bound_ctrl:1
	v_cvt_pk_f32_fp8_sdwa v[190:191], v56 src0_sel:WORD_1
	v_cvt_pk_f32_fp8_e32 v[192:193], v57
	v_cvt_pk_f32_fp8_sdwa v[56:57], v57 src0_sel:WORD_1
	v_cvt_pk_f32_fp8_e32 v[194:195], v54
	s_waitcnt lgkmcnt(0)
	v_mov_b32_e32 v28, v3
	s_nop 1
	v_permlane16_swap_b32_e32 v3, v28
	v_add_f32_e32 v3, v3, v28
	v_mov_b32_e32 v28, v3
	s_nop 1
	v_permlane32_swap_b32_e32 v3, v28
	v_add_f32_e32 v3, v3, v28
	v_mul_f32_e32 v28, 0x3a800000, v3
	v_pk_add_f32 v[168:169], v[70:71], v[28:29] op_sel_hi:[1,0] neg_lo:[0,1] neg_hi:[0,1]
	v_pk_add_f32 v[30:31], v[30:31], v[28:29] op_sel_hi:[1,0] neg_lo:[0,1] neg_hi:[0,1]
	v_pk_add_f32 v[170:171], v[68:69], v[28:29] op_sel_hi:[1,0] neg_lo:[0,1] neg_hi:[0,1]
	v_pk_add_f32 v[34:35], v[34:35], v[28:29] op_sel_hi:[1,0] neg_lo:[0,1] neg_hi:[0,1]
	v_pk_add_f32 v[172:173], v[66:67], v[28:29] op_sel_hi:[1,0] neg_lo:[0,1] neg_hi:[0,1]
	v_pk_add_f32 v[36:37], v[36:37], v[28:29] op_sel_hi:[1,0] neg_lo:[0,1] neg_hi:[0,1]
	v_pk_add_f32 v[174:175], v[64:65], v[28:29] op_sel_hi:[1,0] neg_lo:[0,1] neg_hi:[0,1]
	v_pk_add_f32 v[28:29], v[62:63], v[28:29] op_sel_hi:[1,0] neg_lo:[0,1] neg_hi:[0,1]
	v_pk_mul_f32 v[74:75], v[174:175], v[174:175]
	v_pk_mul_f32 v[76:77], v[28:29], v[28:29]
	v_pk_mul_f32 v[70:71], v[172:173], v[172:173]
	v_pk_mul_f32 v[72:73], v[36:37], v[36:37]
	v_add_f32_e32 v3, v76, v77
	v_add_f32_e32 v39, v74, v75
	v_add_f32_e32 v3, v39, v3
	v_add_f32_e32 v39, v72, v73
	v_add_f32_e32 v41, v70, v71
	v_pk_mul_f32 v[66:67], v[170:171], v[170:171]
	v_pk_mul_f32 v[68:69], v[34:35], v[34:35]
	v_add_f32_e32 v39, v41, v39
	v_pk_mul_f32 v[62:63], v[168:169], v[168:169]
	v_pk_mul_f32 v[64:65], v[30:31], v[30:31]
	v_add_f32_e32 v3, v39, v3
	v_add_f32_e32 v39, v68, v69
	v_add_f32_e32 v41, v66, v67
	v_add_f32_e32 v39, v41, v39
	v_add_f32_e32 v41, v64, v65
	v_add_f32_e32 v43, v62, v63
	global_load_dwordx4 v[62:65], v[98:99], off offset:16
	global_load_dwordx4 v[82:85], v[98:99], off
	global_load_dwordx4 v[86:89], v[100:101], off
	global_load_dwordx4 v[90:93], v[100:101], off offset:16
	global_load_dwordx4 v[66:69], v[98:99], off offset:2048
	global_load_dwordx4 v[70:73], v[100:101], off offset:2048
	global_load_dwordx4 v[74:77], v[98:99], off offset:2064
	global_load_dwordx4 v[78:81], v[100:101], off offset:2064
	v_add_f32_e32 v41, v43, v41
	v_add_f32_e32 v39, v41, v39
	v_add_f32_e32 v3, v39, v3
	v_cvt_pk_f32_fp8_sdwa v[196:197], v54 src0_sel:WORD_1
	v_cvt_pk_f32_fp8_e32 v[198:199], v55
	v_add_f32_dpp v3, v3, v3 quad_perm:[1,0,3,2] row_mask:0xf bank_mask:0xf bound_ctrl:1
	v_cvt_pk_f32_fp8_sdwa v[54:55], v55 src0_sel:WORD_1
	v_cvt_pk_f32_fp8_e32 v[200:201], v52
	v_add_f32_dpp v3, v3, v3 quad_perm:[2,3,0,1] row_mask:0xf bank_mask:0xf bound_ctrl:1
	v_cvt_pk_f32_fp8_sdwa v[204:205], v52 src0_sel:WORD_1
	v_cvt_pk_f32_fp8_e32 v[206:207], v53
	v_add_f32_dpp v3, v3, v3 row_half_mirror row_mask:0xf bank_mask:0xf bound_ctrl:1
	v_cvt_pk_f32_fp8_sdwa v[52:53], v53 src0_sel:WORD_1
	v_cvt_pk_f32_fp8_e32 v[208:209], v50
	v_add_f32_dpp v3, v3, v3 row_mirror row_mask:0xf bank_mask:0xf bound_ctrl:1
	v_cvt_pk_f32_fp8_sdwa v[210:211], v50 src0_sel:WORD_1
	v_cvt_pk_f32_fp8_e32 v[212:213], v51
	v_cvt_pk_f32_fp8_sdwa v[50:51], v51 src0_sel:WORD_1
	v_cvt_pk_f32_fp8_e32 v[214:215], v48
	s_waitcnt lgkmcnt(0)
; __device__ __forceinline__ void unpack8(const u32x4 w, float (&f)[8]) { f[0] = bf_lo(w.x); f[1] = bf_hi(w.x); f[2] = bf_lo(w.y); f[3] = bf_hi(w.y); f[4] = bf_lo(w.z); f[5] = bf_hi(w.z); f[6] = bf_lo(w.w); f[7] = bf_hi(w.w); }
; __device__ __forceinline__ float wave_sum(float v) { v += dpp_f<0xB1>(v); v += dpp_f<0x4E>(v); v += dpp_f<0x141>(v); v += dpp_f<0x140>(v); v += xor_sw<16>(v); return sum_x32(v); }
; __device__ __forceinline__ void ln_row16(float (&v)[16], const float* lng, const float* lnb, int lane, float (&o)[16]) {
;     ...
;     const float mean = wave_sum(s) * (1.0f / D);
; #pragma unroll
;     for (int i = 0; i < 16; ++i) v[i] -= mean;
;     const float s2 = ((v[0] * v[0] + v[1] * v[1]) + (v[2] * v[2] + v[3] * v[3])) + ((v[4] * v[4] + v[5] * v[5]) + (v[6] * v[6] + v[7] * v[7]))
;                    + (((v[8] * v[8] + v[9] * v[9]) + (v[10] * v[10] + v[11] * v[11])) + ((v[12] * v[12] + v[13] * v[13]) + (v[14] * v[14] + v[15] * v[15])));
;     const float rstd = 1.0f / sqrtf(wave_sum(s2) * (1.0f / D) + LN_EPS);
; #pragma unroll
;     for (int hf = 0; hf < 2; ++hf) { const int col = 512 * hf + 8 * lane;
;         const f32x4 g0 = *(const f32x4*)(lng + col), g1 = *(const f32x4*)(lng + col + 4), b0 = *(const f32x4*)(lnb + col), b1 = *(const f32x4*)(lnb + col + 4);
; #pragma unroll
;         for (int i = 0; i < 4; ++i) { o[8 * hf + i] = v[8 * hf + i] * rstd * g0[i] + b0[i]; o[8 * hf + 4 + i] = v[8 * hf + 4 + i] * rstd * g1[i] + b1[i]; } }
; __global__ void __launch_bounds__(NWAVES * 64, 2) mk_fwd(Args args) {
;     ...
;                 for (int j = 0; j < 2; ++j) {
;                     float v[16], x1[16];
; #pragma unroll
;                     for (int hf = 0; hf < 2; ++hf) { float f[8]; unpack8(xr[j][hf], f);
; #pragma unroll
;                         for (int i = 0; i < 8; ++i) v[8 * hf + i] = f[i]; }
;                     ln_row16(v, lng1, lnb1, lane, x1);
; #pragma unroll
;                     for (int hf = 0; hf < 2; ++hf) { float f[8];
; #pragma unroll
;                         for (int i = 0; i < 8; ++i) v[8 * hf + i] = ALPHA * x1[8 * hf + i];
; #pragma unroll
;                         for (int k = 0; k < 4; ++k) { unpack8_f8(yr[j][k][hf], f);
; #pragma unroll
;                             for (int i = 0; i < 8; ++i) v[8 * hf + i] += gt[j][k] * f[i]; } }
;                     ln_row16(v, lng, lnb, lane, o[j]);
	v_mov_b32_e32 v39, v3
	s_nop 1
	v_permlane16_swap_b32_e32 v3, v39
	v_add_f32_e32 v3, v3, v39
	v_mov_b32_e32 v39, v3
	s_nop 1
	v_permlane32_swap_b32_e32 v3, v39
	v_add_f32_e32 v3, v3, v39
	v_fmamk_f32 v3, v3, 0x3a800000, v250
	v_mul_f32_e32 v39, 0x4f800000, v3
	v_cmp_gt_f32_e32 vcc, s11, v3
	v_cvt_pk_f32_fp8_sdwa v[216:217], v48 src0_sel:WORD_1
	v_cvt_pk_f32_fp8_e32 v[218:219], v49
	v_cndmask_b32_e32 v3, v3, v39, vcc
	v_sqrt_f32_e32 v39, v3
	v_cvt_pk_f32_fp8_sdwa v[48:49], v49 src0_sel:WORD_1
	v_cvt_pk_f32_fp8_e32 v[226:227], v46
	v_cvt_pk_f32_fp8_sdwa v[228:229], v46 src0_sel:WORD_1
	v_add_u32_e32 v41, -1, v39
	v_fma_f32 v43, -v41, v39, v3
	v_cmp_ge_f32_e64 s[6:7], 0, v43
	v_add_u32_e32 v43, 1, v39
	v_cvt_pk_f32_fp8_e32 v[230:231], v47
	v_cndmask_b32_e64 v41, v39, v41, s[6:7]
	v_fma_f32 v39, -v43, v39, v3
	v_cmp_lt_f32_e64 s[6:7], 0, v39
	v_cvt_pk_f32_fp8_sdwa v[46:47], v47 src0_sel:WORD_1
	v_cvt_pk_f32_fp8_e32 v[232:233], v156
	v_cndmask_b32_e64 v39, v41, v43, s[6:7]
	v_mul_f32_e32 v41, 0x37800000, v39
	v_cndmask_b32_e32 v39, v39, v41, vcc
	v_cmp_class_f32_e32 vcc, v3, v251
	v_cvt_pk_f32_fp8_e32 v[238:239], v154
	v_cvt_pk_f32_fp8_e32 v[244:245], v152
	v_cndmask_b32_e32 v3, v39, v3, vcc
	v_div_scale_f32 v39, s[6:7], v3, v3, 1.0
	v_rcp_f32_e32 v41, v39
	v_cvt_pk_f32_fp8_sdwa v[234:235], v156 src0_sel:WORD_1
	v_cvt_pk_f32_fp8_sdwa v[240:241], v154 src0_sel:WORD_1
	v_cvt_pk_f32_fp8_sdwa v[246:247], v152 src0_sel:WORD_1
	v_fma_f32 v43, -v39, v41, 1.0
	v_fmac_f32_e32 v41, v43, v41
	v_div_scale_f32 v43, vcc, 1.0, v3, 1.0
	v_mul_f32_e32 v45, v43, v41
	v_fma_f32 v147, -v39, v45, v43
	v_fmac_f32_e32 v45, v147, v41
	v_fma_f32 v39, -v39, v45, v43
	v_div_fmas_f32 v39, v39, v41, v45
	v_div_fixup_f32 v176, v39, v3, 1.0
	v_pk_mul_f32 v[168:169], v[168:169], v[176:177] op_sel_hi:[1,0]
	v_pk_mul_f32 v[170:171], v[170:171], v[176:177] op_sel_hi:[1,0]
	v_pk_mul_f32 v[30:31], v[30:31], v[176:177] op_sel_hi:[1,0]
	v_pk_mul_f32 v[34:35], v[34:35], v[176:177] op_sel_hi:[1,0]
	v_pk_mul_f32 v[172:173], v[172:173], v[176:177] op_sel_hi:[1,0]
	v_pk_mul_f32 v[174:175], v[174:175], v[176:177] op_sel_hi:[1,0]
	v_pk_mul_f32 v[36:37], v[36:37], v[176:177] op_sel_hi:[1,0]
	v_pk_mul_f32 v[28:29], v[28:29], v[176:177] op_sel_hi:[1,0]
	v_cvt_pk_f32_fp8_e32 v[176:177], v60
	v_cvt_pk_f32_fp8_sdwa v[60:61], v61 src0_sel:WORD_1
	s_waitcnt vmcnt(4)
	v_pk_fma_f32 v[34:35], v[64:65], v[34:35], v[92:93]
	v_pk_fma_f32 v[168:169], v[82:83], v[168:169], v[86:87]
	v_pk_mul_f32 v[176:177], v[44:45], v[176:177] op_sel_hi:[0,1]
	v_pk_mul_f32 v[60:61], v[44:45], v[60:61] op_sel_hi:[0,1]
	v_pk_fma_f32 v[34:35], v[34:35], s[60:61], v[60:61] op_sel_hi:[1,0,1]
	v_pk_fma_f32 v[168:169], v[168:169], s[60:61], v[176:177] op_sel_hi:[1,0,1]
	v_pk_fma_f32 v[34:35], v[42:43], v[58:59], v[34:35] op_sel_hi:[0,1,1]
	v_pk_fma_f32 v[34:35], v[40:41], v[56:57], v[34:35] op_sel_hi:[0,1,1]
	v_pk_fma_f32 v[34:35], v[38:39], v[54:55], v[34:35] op_sel_hi:[0,1,1]
	s_waitcnt vmcnt(2)
	v_pk_fma_f32 v[54:55], v[172:173], v[66:67], v[70:71]
	v_pk_mul_f32 v[56:57], v[44:45], v[200:201] op_sel_hi:[0,1]
	v_pk_fma_f32 v[30:31], v[84:85], v[30:31], v[88:89]
	v_pk_mul_f32 v[176:177], v[44:45], v[178:179] op_sel_hi:[0,1]
	v_pk_fma_f32 v[54:55], v[54:55], s[60:61], v[56:57] op_sel_hi:[1,0,1]
	v_pk_fma_f32 v[36:37], v[36:37], v[68:69], v[72:73]
	v_pk_mul_f32 v[56:57], v[44:45], v[204:205] op_sel_hi:[0,1]
	v_pk_fma_f32 v[30:31], v[30:31], s[60:61], v[176:177] op_sel_hi:[1,0,1]
	v_pk_mul_f32 v[176:177], v[44:45], v[180:181] op_sel_hi:[0,1]
	v_pk_fma_f32 v[36:37], v[36:37], s[60:61], v[56:57] op_sel_hi:[1,0,1]
	s_waitcnt vmcnt(0)
	v_pk_fma_f32 v[56:57], v[174:175], v[74:75], v[78:79]
	v_pk_mul_f32 v[58:59], v[44:45], v[206:207] op_sel_hi:[0,1]
	v_pk_fma_f32 v[28:29], v[28:29], v[76:77], v[80:81]
	v_pk_mul_f32 v[44:45], v[44:45], v[52:53] op_sel_hi:[0,1]
	v_pk_fma_f32 v[170:171], v[62:63], v[170:171], v[90:91]
	v_pk_fma_f32 v[56:57], v[56:57], s[60:61], v[58:59] op_sel_hi:[1,0,1]
	v_pk_fma_f32 v[28:29], v[28:29], s[60:61], v[44:45] op_sel_hi:[1,0,1]
	v_pk_fma_f32 v[170:171], v[170:171], s[60:61], v[176:177] op_sel_hi:[1,0,1]
	v_pk_fma_f32 v[56:57], v[42:43], v[212:213], v[56:57] op_sel_hi:[0,1,1]
	v_pk_fma_f32 v[28:29], v[42:43], v[50:51], v[28:29] op_sel_hi:[0,1,1]
	v_pk_fma_f32 v[168:169], v[42:43], v[182:183], v[168:169] op_sel_hi:[0,1,1]
	v_pk_fma_f32 v[30:31], v[42:43], v[184:185], v[30:31] op_sel_hi:[0,1,1]
	v_pk_fma_f32 v[170:171], v[42:43], v[186:187], v[170:171] op_sel_hi:[0,1,1]
	v_pk_fma_f32 v[54:55], v[42:43], v[208:209], v[54:55] op_sel_hi:[0,1,1]
	v_pk_fma_f32 v[36:37], v[42:43], v[210:211], v[36:37] op_sel_hi:[0,1,1]
	v_pk_fma_f32 v[56:57], v[40:41], v[218:219], v[56:57] op_sel_hi:[0,1,1]
	v_pk_fma_f32 v[28:29], v[40:41], v[48:49], v[28:29] op_sel_hi:[0,1,1]
	v_pk_fma_f32 v[168:169], v[40:41], v[188:189], v[168:169] op_sel_hi:[0,1,1]
	v_pk_fma_f32 v[30:31], v[40:41], v[190:191], v[30:31] op_sel_hi:[0,1,1]
	v_pk_fma_f32 v[170:171], v[40:41], v[192:193], v[170:171] op_sel_hi:[0,1,1]
	v_pk_fma_f32 v[54:55], v[40:41], v[214:215], v[54:55] op_sel_hi:[0,1,1]
	v_pk_fma_f32 v[36:37], v[40:41], v[216:217], v[36:37] op_sel_hi:[0,1,1]
	v_pk_fma_f32 v[56:57], v[38:39], v[230:231], v[56:57] op_sel_hi:[0,1,1]
	v_pk_fma_f32 v[28:29], v[38:39], v[46:47], v[28:29] op_sel_hi:[0,1,1]
	v_pk_fma_f32 v[168:169], v[38:39], v[194:195], v[168:169] op_sel_hi:[0,1,1]
	v_pk_fma_f32 v[30:31], v[38:39], v[196:197], v[30:31] op_sel_hi:[0,1,1]
	v_pk_fma_f32 v[170:171], v[38:39], v[198:199], v[170:171] op_sel_hi:[0,1,1]
	v_pk_fma_f32 v[54:55], v[38:39], v[226:227], v[54:55] op_sel_hi:[0,1,1]
	v_pk_fma_f32 v[36:37], v[38:39], v[228:229], v[36:37] op_sel_hi:[0,1,1]
	v_add_f32_e32 v3, v28, v29
	v_add_f32_e32 v38, v56, v57
	v_add_f32_e32 v3, v38, v3
	v_add_f32_e32 v38, v36, v37
	v_add_f32_e32 v39, v54, v55
	v_add_f32_e32 v38, v39, v38
	v_add_f32_e32 v3, v38, v3
	v_add_f32_e32 v38, v34, v35
	v_add_f32_e32 v39, v170, v171
	v_add_f32_e32 v38, v39, v38
	v_add_f32_e32 v39, v30, v31
	v_add_f32_e32 v40, v168, v169
	v_add_f32_e32 v39, v40, v39
	v_add_f32_e32 v38, v39, v38
	v_add_f32_e32 v3, v38, v3
	v_lshlrev_b32_e32 v184, 16, v27
	v_and_b32_e32 v185, 0xffff0000, v27
	v_add_f32_dpp v3, v3, v3 quad_perm:[1,0,3,2] row_mask:0xf bank_mask:0xf bound_ctrl:1
	v_lshlrev_b32_e32 v186, 16, v26
	v_and_b32_e32 v187, 0xffff0000, v26
	v_add_f32_dpp v3, v3, v3 quad_perm:[2,3,0,1] row_mask:0xf bank_mask:0xf bound_ctrl:1
	v_lshlrev_b32_e32 v26, 16, v25
	v_and_b32_e32 v27, 0xffff0000, v25
	v_add_f32_dpp v3, v3, v3 row_half_mirror row_mask:0xf bank_mask:0xf bound_ctrl:1
	v_lshlrev_b32_e32 v188, 16, v24
	v_and_b32_e32 v189, 0xffff0000, v24
	v_add_f32_dpp v3, v3, v3 row_mirror row_mask:0xf bank_mask:0xf bound_ctrl:1
	v_lshlrev_b32_e32 v24, 16, v23
	v_and_b32_e32 v25, 0xffff0000, v23
	v_lshlrev_b32_e32 v190, 16, v22
	v_and_b32_e32 v191, 0xffff0000, v22
	s_waitcnt lgkmcnt(0)
; __device__ __forceinline__ void unpack8(const u32x4 w, float (&f)[8]) { f[0] = bf_lo(w.x); f[1] = bf_hi(w.x); f[2] = bf_lo(w.y); f[3] = bf_hi(w.y); f[4] = bf_lo(w.z); f[5] = bf_hi(w.z); f[6] = bf_lo(w.w); f[7] = bf_hi(w.w); }
; __device__ __forceinline__ float wave_sum(float v) { v += dpp_f<0xB1>(v); v += dpp_f<0x4E>(v); v += dpp_f<0x141>(v); v += dpp_f<0x140>(v); v += xor_sw<16>(v); return sum_x32(v); }
; __device__ __forceinline__ void ln_row16(float (&v)[16], const float* lng, const float* lnb, int lane, float (&o)[16]) {
;     const float s = ((v[0] + v[1]) + (v[2] + v[3])) + ((v[4] + v[5]) + (v[6] + v[7])) + (((v[8] + v[9]) + (v[10] + v[11])) + ((v[12] + v[13]) + (v[14] + v[15])));
;     const float mean = wave_sum(s) * (1.0f / D);
; #pragma unroll
;     for (int i = 0; i < 16; ++i) v[i] -= mean;
;     const float s2 = ((v[0] * v[0] + v[1] * v[1]) + (v[2] * v[2] + v[3] * v[3])) + ((v[4] * v[4] + v[5] * v[5]) + (v[6] * v[6] + v[7] * v[7]))
;                    + (((v[8] * v[8] + v[9] * v[9]) + (v[10] * v[10] + v[11] * v[11])) + ((v[12] * v[12] + v[13] * v[13]) + (v[14] * v[14] + v[15] * v[15])));
;     const float rstd = 1.0f / sqrtf(wave_sum(s2) * (1.0f / D) + LN_EPS);
; __global__ void __launch_bounds__(NWAVES * 64, 2) mk_fwd(Args args) {
;     ...
;                 for (int j = 0; j < 2; ++j) {
;                     float v[16], x1[16];
; #pragma unroll
;                     for (int hf = 0; hf < 2; ++hf) { float f[8]; unpack8(xr[j][hf], f);
; #pragma unroll
;                         for (int i = 0; i < 8; ++i) v[8 * hf + i] = f[i]; }
;                     ln_row16(v, lng1, lnb1, lane, x1);
; #pragma unroll
;                     for (int hf = 0; hf < 2; ++hf) { float f[8];
; #pragma unroll
;                         for (int i = 0; i < 8; ++i) v[8 * hf + i] = ALPHA * x1[8 * hf + i];
; #pragma unroll
;                         for (int k = 0; k < 4; ++k) { unpack8_f8(yr[j][k][hf], f);
; #pragma unroll
;                             for (int i = 0; i < 8; ++i) v[8 * hf + i] += gt[j][k] * f[i]; } }
;                     ln_row16(v, lng, lnb, lane, o[j]);
	v_mov_b32_e32 v38, v3
	s_nop 1
	v_permlane16_swap_b32_e32 v3, v38
	v_add_f32_e32 v3, v3, v38
	v_mov_b32_e32 v38, v3
	s_nop 1
	v_permlane32_swap_b32_e32 v3, v38
	v_add_f32_e32 v3, v3, v38
	v_mul_f32_e32 v38, 0x3a800000, v3
	v_pk_add_f32 v[176:177], v[168:169], v[38:39] op_sel_hi:[1,0] neg_lo:[0,1] neg_hi:[0,1]
	v_pk_add_f32 v[178:179], v[30:31], v[38:39] op_sel_hi:[1,0] neg_lo:[0,1] neg_hi:[0,1]
	v_pk_add_f32 v[180:181], v[170:171], v[38:39] op_sel_hi:[1,0] neg_lo:[0,1] neg_hi:[0,1]
	v_pk_add_f32 v[182:183], v[34:35], v[38:39] op_sel_hi:[1,0] neg_lo:[0,1] neg_hi:[0,1]
	v_pk_add_f32 v[172:173], v[54:55], v[38:39] op_sel_hi:[1,0] neg_lo:[0,1] neg_hi:[0,1]
	v_pk_add_f32 v[168:169], v[36:37], v[38:39] op_sel_hi:[1,0] neg_lo:[0,1] neg_hi:[0,1]
	v_pk_add_f32 v[174:175], v[56:57], v[38:39] op_sel_hi:[1,0] neg_lo:[0,1] neg_hi:[0,1]
	v_pk_add_f32 v[170:171], v[28:29], v[38:39] op_sel_hi:[1,0] neg_lo:[0,1] neg_hi:[0,1]
	v_pk_mul_f32 v[28:29], v[176:177], v[176:177]
	v_pk_mul_f32 v[30:31], v[178:179], v[178:179]
	v_pk_mul_f32 v[34:35], v[180:181], v[180:181]
	v_pk_mul_f32 v[36:37], v[182:183], v[182:183]
	v_pk_mul_f32 v[38:39], v[172:173], v[172:173]
	v_pk_mul_f32 v[40:41], v[168:169], v[168:169]
	v_pk_mul_f32 v[42:43], v[174:175], v[174:175]
	v_pk_mul_f32 v[44:45], v[170:171], v[170:171]
	v_add_f32_e32 v42, v42, v43
	v_add_f32_e32 v3, v44, v45
	v_add_f32_e32 v40, v40, v41
	v_add_f32_e32 v38, v38, v39
	v_add_f32_e32 v36, v36, v37
	v_add_f32_e32 v34, v34, v35
	v_add_f32_e32 v30, v30, v31
	v_add_f32_e32 v28, v28, v29
	v_add_f32_e32 v3, v42, v3
	v_add_f32_e32 v38, v38, v40
	v_add_f32_e32 v34, v34, v36
	v_add_f32_e32 v28, v28, v30
	v_add_f32_e32 v3, v38, v3
	v_add_f32_e32 v28, v28, v34
	v_add_f32_e32 v3, v28, v3
	v_lshlrev_b32_e32 v22, 16, v21
	v_and_b32_e32 v23, 0xffff0000, v21
	v_add_f32_dpp v3, v3, v3 quad_perm:[1,0,3,2] row_mask:0xf bank_mask:0xf bound_ctrl:1
	v_lshlrev_b32_e32 v192, 16, v20
	v_and_b32_e32 v193, 0xffff0000, v20
	v_add_f32_dpp v3, v3, v3 quad_perm:[2,3,0,1] row_mask:0xf bank_mask:0xf bound_ctrl:1
	v_add_f32_e32 v20, v185, v184
	v_add_f32_e32 v21, v187, v186
	v_add_f32_dpp v3, v3, v3 row_half_mirror row_mask:0xf bank_mask:0xf bound_ctrl:1
	v_add_f32_e32 v20, v21, v20
	v_add_f32_e32 v21, v27, v26
	v_add_f32_dpp v3, v3, v3 row_mirror row_mask:0xf bank_mask:0xf bound_ctrl:1
	v_add_f32_e32 v194, v189, v188
	v_add_f32_e32 v21, v194, v21
	v_add_f32_e32 v20, v21, v20
	v_add_f32_e32 v21, v25, v24
	s_waitcnt lgkmcnt(0)
	v_mov_b32_e32 v28, v3
	s_nop 1
	v_permlane16_swap_b32_e32 v3, v28
	v_add_f32_e32 v3, v3, v28
	v_mov_b32_e32 v28, v3
	s_nop 1
	v_permlane32_swap_b32_e32 v3, v28
	v_add_f32_e32 v3, v3, v28
	v_fmamk_f32 v3, v3, 0x3a800000, v250
	v_mul_f32_e32 v28, 0x4f800000, v3
	v_cmp_gt_f32_e32 vcc, s11, v3
	v_add_f32_e32 v194, v191, v190
	v_add_f32_e32 v21, v194, v21
	v_cndmask_b32_e32 v3, v3, v28, vcc
	global_load_dwordx4 v[28:31], v[102:103], off offset:16
	global_load_dwordx4 v[38:41], v[102:103], off
	global_load_dwordx4 v[34:37], v[104:105], off offset:16
	global_load_dwordx4 v[42:45], v[104:105], off
	v_sqrt_f32_e32 v46, v3
	v_add_f32_e32 v194, v23, v22
	v_add_f32_e32 v195, v193, v192
	v_add_f32_e32 v194, v195, v194
	v_add_u32_e32 v47, -1, v46
	v_fma_f32 v48, -v47, v46, v3
	v_cmp_ge_f32_e64 s[6:7], 0, v48
	v_add_u32_e32 v48, 1, v46
	v_add_f32_e32 v21, v194, v21
	v_cndmask_b32_e64 v47, v46, v47, s[6:7]
	v_fma_f32 v46, -v48, v46, v3
	v_add_f32_e32 v20, v21, v20
	v_cmp_lt_f32_e64 s[6:7], 0, v46
	v_cvt_pk_f32_fp8_e32 v[212:213], v163
	v_add_f32_dpp v20, v20, v20 quad_perm:[1,0,3,2] row_mask:0xf bank_mask:0xf bound_ctrl:1
	v_cndmask_b32_e64 v46, v47, v48, s[6:7]
	v_mul_f32_e32 v47, 0x37800000, v46
	v_add_f32_dpp v20, v20, v20 quad_perm:[2,3,0,1] row_mask:0xf bank_mask:0xf bound_ctrl:1
	v_cndmask_b32_e32 v46, v46, v47, vcc
	v_cmp_class_f32_e32 vcc, v3, v251
	v_add_f32_dpp v20, v20, v20 row_half_mirror row_mask:0xf bank_mask:0xf bound_ctrl:1
	v_cvt_pk_f32_fp8_e32 v[218:219], v161
	v_cndmask_b32_e32 v3, v46, v3, vcc
	v_add_f32_dpp v20, v20, v20 row_mirror row_mask:0xf bank_mask:0xf bound_ctrl:1
	v_div_scale_f32 v147, s[6:7], v3, v3, 1.0
	v_rcp_f32_e32 v149, v147
	global_load_dwordx4 v[46:49], v[102:103], off offset:2064
	global_load_dwordx4 v[54:57], v[102:103], off offset:2048
	global_load_dwordx4 v[50:53], v[104:105], off offset:2064
	global_load_dwordx4 v[58:61], v[104:105], off offset:2048
	s_waitcnt lgkmcnt(0)
; __device__ __forceinline__ void unpack8(const u32x4 w, float (&f)[8]) { f[0] = bf_lo(w.x); f[1] = bf_hi(w.x); f[2] = bf_lo(w.y); f[3] = bf_hi(w.y); f[4] = bf_lo(w.z); f[5] = bf_hi(w.z); f[6] = bf_lo(w.w); f[7] = bf_hi(w.w); }
; __device__ __forceinline__ void ln_row16(float (&v)[16], const float* lng, const float* lnb, int lane, float (&o)[16]) {
;     const float s = ((v[0] + v[1]) + (v[2] + v[3])) + ((v[4] + v[5]) + (v[6] + v[7])) + (((v[8] + v[9]) + (v[10] + v[11])) + ((v[12] + v[13]) + (v[14] + v[15])));
;     const float mean = wave_sum(s) * (1.0f / D);
; #pragma unroll
;     for (int i = 0; i < 16; ++i) v[i] -= mean;
;     const float s2 = ((v[0] * v[0] + v[1] * v[1]) + (v[2] * v[2] + v[3] * v[3])) + ((v[4] * v[4] + v[5] * v[5]) + (v[6] * v[6] + v[7] * v[7]))
;                    + (((v[8] * v[8] + v[9] * v[9]) + (v[10] * v[10] + v[11] * v[11])) + ((v[12] * v[12] + v[13] * v[13]) + (v[14] * v[14] + v[15] * v[15])));
;     const float rstd = 1.0f / sqrtf(wave_sum(s2) * (1.0f / D) + LN_EPS);
; #pragma unroll
;     for (int hf = 0; hf < 2; ++hf) { const int col = 512 * hf + 8 * lane;
;         const f32x4 g0 = *(const f32x4*)(lng + col), g1 = *(const f32x4*)(lng + col + 4), b0 = *(const f32x4*)(lnb + col), b1 = *(const f32x4*)(lnb + col + 4);
; #pragma unroll
;         for (int i = 0; i < 4; ++i) { o[8 * hf + i] = v[8 * hf + i] * rstd * g0[i] + b0[i]; o[8 * hf + 4 + i] = v[8 * hf + 4 + i] * rstd * g1[i] + b1[i]; } }
; __global__ void __launch_bounds__(NWAVES * 64, 2) mk_fwd(Args args) {
;     ...
;                 for (int j = 0; j < 2; ++j) {
;                     float v[16], x1[16];
; #pragma unroll
;                     for (int hf = 0; hf < 2; ++hf) { float f[8]; unpack8(xr[j][hf], f);
; #pragma unroll
;                         for (int i = 0; i < 8; ++i) v[8 * hf + i] = f[i]; }
;                     ln_row16(v, lng1, lnb1, lane, x1);
; #pragma unroll
;                     for (int hf = 0; hf < 2; ++hf) { float f[8];
; #pragma unroll
;                         for (int i = 0; i < 8; ++i) v[8 * hf + i] = ALPHA * x1[8 * hf + i];
; #pragma unroll
;                         for (int k = 0; k < 4; ++k) { unpack8_f8(yr[j][k][hf], f);
; #pragma unroll
;                             for (int i = 0; i < 8; ++i) v[8 * hf + i] += gt[j][k] * f[i]; } }
;                     ln_row16(v, lng, lnb, lane, o[j]);
	v_mov_b32_e32 v21, v20
	s_nop 1
	v_permlane16_swap_b32_e32 v20, v21
	v_add_f32_e32 v20, v20, v21
	v_mov_b32_e32 v21, v20
	v_fma_f32 v151, -v147, v149, 1.0
	v_fmac_f32_e32 v149, v151, v149
	v_div_scale_f32 v151, vcc, 1.0, v3, 1.0
	v_permlane32_swap_b32_e32 v20, v21
	v_mul_f32_e32 v202, v151, v149
	v_add_f32_e32 v20, v20, v21
	v_fma_f32 v194, -v147, v202, v151
	v_mul_f32_e32 v20, 0x3a800000, v20
	v_fmac_f32_e32 v202, v194, v149
	v_pk_add_f32 v[192:193], v[192:193], v[20:21] op_sel_hi:[1,0] neg_lo:[0,1] neg_hi:[0,1]
	v_pk_add_f32 v[194:195], v[22:23], v[20:21] op_sel_hi:[1,0] neg_lo:[0,1] neg_hi:[0,1]
	v_pk_add_f32 v[190:191], v[190:191], v[20:21] op_sel_hi:[1,0] neg_lo:[0,1] neg_hi:[0,1]
	v_pk_add_f32 v[196:197], v[24:25], v[20:21] op_sel_hi:[1,0] neg_lo:[0,1] neg_hi:[0,1]
	v_pk_add_f32 v[188:189], v[188:189], v[20:21] op_sel_hi:[1,0] neg_lo:[0,1] neg_hi:[0,1]
	v_pk_add_f32 v[198:199], v[26:27], v[20:21] op_sel_hi:[1,0] neg_lo:[0,1] neg_hi:[0,1]
	v_pk_add_f32 v[186:187], v[186:187], v[20:21] op_sel_hi:[1,0] neg_lo:[0,1] neg_hi:[0,1]
	v_pk_add_f32 v[184:185], v[184:185], v[20:21] op_sel_hi:[1,0] neg_lo:[0,1] neg_hi:[0,1]
	v_pk_mul_f32 v[20:21], v[192:193], v[192:193]
	v_pk_mul_f32 v[22:23], v[194:195], v[194:195]
	v_pk_mul_f32 v[24:25], v[190:191], v[190:191]
	v_pk_mul_f32 v[26:27], v[196:197], v[196:197]
	v_pk_mul_f32 v[200:201], v[188:189], v[188:189]
	v_pk_mul_f32 v[204:205], v[198:199], v[198:199]
	v_pk_mul_f32 v[206:207], v[186:187], v[186:187]
	v_pk_mul_f32 v[208:209], v[184:185], v[184:185]
	v_fma_f32 v147, -v147, v202, v151
	v_add_f32_e32 v151, v208, v209
	v_add_f32_e32 v206, v206, v207
	v_add_f32_e32 v204, v204, v205
	v_add_f32_e32 v200, v200, v201
	v_add_f32_e32 v26, v26, v27
	v_add_f32_e32 v24, v24, v25
	v_add_f32_e32 v22, v22, v23
	v_add_f32_e32 v20, v20, v21
	v_add_f32_e32 v151, v206, v151
	v_add_f32_e32 v200, v200, v204
	v_add_f32_e32 v24, v24, v26
	v_add_f32_e32 v20, v20, v22
	v_add_f32_e32 v151, v200, v151
	v_add_f32_e32 v20, v20, v24
	v_add_f32_e32 v20, v20, v151
	v_cvt_pk_f32_fp8_e32 v[206:207], v165
	v_cvt_pk_f32_fp8_sdwa v[204:205], v164 src0_sel:WORD_1
	v_add_f32_dpp v20, v20, v20 quad_perm:[1,0,3,2] row_mask:0xf bank_mask:0xf bound_ctrl:1
	v_cvt_pk_f32_fp8_e32 v[208:209], v162
	v_cvt_pk_f32_fp8_sdwa v[210:211], v162 src0_sel:WORD_1
	v_add_f32_dpp v20, v20, v20 quad_perm:[2,3,0,1] row_mask:0xf bank_mask:0xf bound_ctrl:1
	v_cvt_pk_f32_fp8_sdwa v[162:163], v163 src0_sel:WORD_1
	v_cvt_pk_f32_fp8_e32 v[214:215], v160
	v_add_f32_dpp v20, v20, v20 row_half_mirror row_mask:0xf bank_mask:0xf bound_ctrl:1
	v_cvt_pk_f32_fp8_sdwa v[216:217], v160 src0_sel:WORD_1
	v_cvt_pk_f32_fp8_sdwa v[160:161], v161 src0_sel:WORD_1
	v_add_f32_dpp v24, v20, v20 row_mirror row_mask:0xf bank_mask:0xf bound_ctrl:1
	v_div_fmas_f32 v20, v147, v149, v202
	v_div_fixup_f32 v200, v20, v3, 1.0
	v_pk_mul_f32 v[20:21], v[176:177], v[200:201] op_sel_hi:[1,0]
	v_pk_mul_f32 v[22:23], v[180:181], v[200:201] op_sel_hi:[1,0]
	s_waitcnt lgkmcnt(0)
	v_mov_b32_e32 v25, v24
	s_nop 1
	v_permlane16_swap_b32_e32 v24, v25
	v_add_f32_e32 v3, v24, v25
	v_mov_b32_e32 v24, v3
	s_nop 1
	v_permlane32_swap_b32_e32 v3, v24
	v_add_f32_e32 v3, v3, v24
	v_fmamk_f32 v3, v3, 0x3a800000, v250
	v_mul_f32_e32 v24, 0x4f800000, v3
	v_cmp_gt_f32_e32 vcc, s11, v3
	v_pk_mul_f32 v[176:177], v[182:183], v[200:201] op_sel_hi:[1,0]
	v_cvt_pk_f32_fp8_e32 v[226:227], v158
	v_cndmask_b32_e32 v3, v3, v24, vcc
	v_sqrt_f32_e32 v26, v3
	s_waitcnt vmcnt(4)
	v_pk_fma_f32 v[24:25], v[38:39], v[20:21], v[42:43]
	v_pk_fma_f32 v[20:21], v[28:29], v[22:23], v[34:35]
	v_pk_mul_f32 v[22:23], v[178:179], v[200:201] op_sel_hi:[1,0]
	v_add_u32_e32 v27, -1, v26
	v_fma_f32 v147, -v27, v26, v3
	v_cmp_ge_f32_e64 s[6:7], 0, v147
	v_add_u32_e32 v147, 1, v26
	v_cvt_pk_f32_fp8_sdwa v[228:229], v158 src0_sel:WORD_1
	v_cndmask_b32_e64 v27, v26, v27, s[6:7]
	v_fma_f32 v26, -v147, v26, v3
	v_cmp_lt_f32_e64 s[6:7], 0, v26
	v_cvt_pk_f32_fp8_e32 v[230:231], v159
	v_cvt_pk_f32_fp8_e32 v[236:237], v157
	v_cndmask_b32_e64 v26, v27, v147, s[6:7]
	v_mul_f32_e32 v27, 0x37800000, v26
	v_cndmask_b32_e32 v26, v26, v27, vcc
	v_cmp_class_f32_e32 vcc, v3, v251
	v_cvt_pk_f32_fp8_e32 v[242:243], v155
	v_cvt_pk_f32_fp8_sdwa v[158:159], v159 src0_sel:WORD_1
	v_cndmask_b32_e32 v3, v26, v3, vcc
	v_div_scale_f32 v147, s[6:7], v3, v3, 1.0
	v_rcp_f32_e32 v149, v147
	v_pk_fma_f32 v[26:27], v[40:41], v[22:23], v[44:45]
	v_pk_fma_f32 v[22:23], v[30:31], v[176:177], v[36:37]
	v_cvt_pk_f32_fp8_e32 v[248:249], v153
	v_fma_f32 v151, -v147, v149, 1.0
	v_fmac_f32_e32 v149, v151, v149
	v_div_scale_f32 v151, vcc, 1.0, v3, 1.0
	v_mul_f32_e32 v176, v151, v149
	v_fma_f32 v177, -v147, v176, v151
	v_fmac_f32_e32 v176, v177, v149
	v_fma_f32 v147, -v147, v176, v151
	v_div_fmas_f32 v147, v147, v149, v176
	v_div_fixup_f32 v176, v147, v3, 1.0
	v_pk_mul_f32 v[178:179], v[192:193], v[176:177] op_sel_hi:[1,0]
	v_pk_mul_f32 v[180:181], v[190:191], v[176:177] op_sel_hi:[1,0]
	v_pk_mul_f32 v[182:183], v[194:195], v[176:177] op_sel_hi:[1,0]
	v_pk_mul_f32 v[190:191], v[196:197], v[176:177] op_sel_hi:[1,0]
	v_pk_mul_f32 v[188:189], v[188:189], v[176:177] op_sel_hi:[1,0]
	v_pk_mul_f32 v[186:187], v[186:187], v[176:177] op_sel_hi:[1,0]
	v_pk_mul_f32 v[192:193], v[198:199], v[176:177] op_sel_hi:[1,0]
	v_pk_mul_f32 v[176:177], v[184:185], v[176:177] op_sel_hi:[1,0]
	v_cvt_pk_f32_fp8_e32 v[184:185], v166
	v_cvt_pk_f32_fp8_sdwa v[194:195], v166 src0_sel:WORD_1
	v_cvt_pk_f32_fp8_e32 v[196:197], v167
	v_pk_fma_f32 v[82:83], v[82:83], v[178:179], v[86:87]
	v_pk_mul_f32 v[86:87], v[150:151], v[184:185] op_sel_hi:[0,1]
	v_pk_fma_f32 v[82:83], v[82:83], s[60:61], v[86:87] op_sel_hi:[1,0,1]
; __device__ __forceinline__ void unpack8(const u32x4 w, float (&f)[8]) { f[0] = bf_lo(w.x); f[1] = bf_hi(w.x); f[2] = bf_lo(w.y); f[3] = bf_hi(w.y); f[4] = bf_lo(w.z); f[5] = bf_hi(w.z); f[6] = bf_lo(w.w); f[7] = bf_hi(w.w); }
; __global__ void __launch_bounds__(NWAVES * 64, 2) mk_fwd(Args args) {
;     ...
;                 for (int j = 0; j < 2; ++j) {
;                     float v[16], x1[16];
; #pragma unroll
;                     for (int hf = 0; hf < 2; ++hf) { float f[8]; unpack8(xr[j][hf], f);
; #pragma unroll
;                         for (int i = 0; i < 8; ++i) v[8 * hf + i] = f[i]; }
;                     ln_row16(v, lng1, lnb1, lane, x1);
; #pragma unroll
;                     for (int hf = 0; hf < 2; ++hf) { float f[8];
; #pragma unroll
;                         for (int i = 0; i < 8; ++i) v[8 * hf + i] = ALPHA * x1[8 * hf + i];
; #pragma unroll
;                         for (int k = 0; k < 4; ++k) { unpack8_f8(yr[j][k][hf], f);
; #pragma unroll
;                             for (int i = 0; i < 8; ++i) v[8 * hf + i] += gt[j][k] * f[i]; } }
;                     ln_row16(v, lng, lnb, lane, o[j]);
;                 }
; #pragma unroll
;                 for (int j = 0; j < 2; ++j) {
;                     const int t = tt[j];
;                     if (layer == DEPTH - 1) {
	v_pk_fma_f32 v[84:85], v[84:85], v[182:183], v[88:89]
	v_pk_mul_f32 v[86:87], v[150:151], v[194:195] op_sel_hi:[0,1]
	v_cvt_pk_f32_fp8_sdwa v[166:167], v167 src0_sel:WORD_1
	v_pk_fma_f32 v[84:85], v[84:85], s[60:61], v[86:87] op_sel_hi:[1,0,1]
	v_pk_fma_f32 v[62:63], v[62:63], v[180:181], v[90:91]
	v_pk_mul_f32 v[86:87], v[150:151], v[196:197] op_sel_hi:[0,1]
	v_pk_fma_f32 v[62:63], v[62:63], s[60:61], v[86:87] op_sel_hi:[1,0,1]
	v_cvt_pk_f32_fp8_e32 v[198:199], v164
	v_cvt_pk_f32_fp8_sdwa v[164:165], v165 src0_sel:WORD_1
	v_pk_fma_f32 v[62:63], v[148:149], v[206:207], v[62:63] op_sel_hi:[0,1,1]
	v_pk_fma_f32 v[62:63], v[146:147], v[212:213], v[62:63] op_sel_hi:[0,1,1]
	v_pk_fma_f32 v[86:87], v[32:33], v[218:219], v[62:63] op_sel_hi:[0,1,1]
	v_pk_fma_f32 v[62:63], v[64:65], v[190:191], v[92:93]
	v_pk_mul_f32 v[64:65], v[150:151], v[166:167] op_sel_hi:[0,1]
	v_pk_fma_f32 v[62:63], v[62:63], s[60:61], v[64:65] op_sel_hi:[1,0,1]
	v_cvt_pk_f32_fp8_sdwa v[156:157], v157 src0_sel:WORD_1
	v_pk_fma_f32 v[62:63], v[148:149], v[164:165], v[62:63] op_sel_hi:[0,1,1]
	v_pk_fma_f32 v[62:63], v[146:147], v[162:163], v[62:63] op_sel_hi:[0,1,1]
	v_pk_fma_f32 v[64:65], v[32:33], v[160:161], v[62:63] op_sel_hi:[0,1,1]
	v_pk_fma_f32 v[62:63], v[188:189], v[66:67], v[70:71]
	v_pk_mul_f32 v[66:67], v[150:151], v[226:227] op_sel_hi:[0,1]
	v_pk_fma_f32 v[62:63], v[62:63], s[60:61], v[66:67] op_sel_hi:[1,0,1]
	v_pk_mul_f32 v[66:67], v[150:151], v[228:229] op_sel_hi:[0,1]
	v_pk_fma_f32 v[62:63], v[148:149], v[232:233], v[62:63] op_sel_hi:[0,1,1]
	v_pk_fma_f32 v[62:63], v[146:147], v[238:239], v[62:63] op_sel_hi:[0,1,1]
	v_pk_fma_f32 v[70:71], v[32:33], v[244:245], v[62:63] op_sel_hi:[0,1,1]
	v_pk_fma_f32 v[62:63], v[192:193], v[68:69], v[72:73]
	v_cvt_pk_f32_fp8_sdwa v[154:155], v155 src0_sel:WORD_1
	v_pk_fma_f32 v[62:63], v[62:63], s[60:61], v[66:67] op_sel_hi:[1,0,1]
	v_pk_mul_f32 v[66:67], v[150:151], v[230:231] op_sel_hi:[0,1]
	v_pk_fma_f32 v[62:63], v[148:149], v[234:235], v[62:63] op_sel_hi:[0,1,1]
	v_pk_fma_f32 v[62:63], v[146:147], v[240:241], v[62:63] op_sel_hi:[0,1,1]
	v_pk_fma_f32 v[68:69], v[32:33], v[246:247], v[62:63] op_sel_hi:[0,1,1]
	v_pk_fma_f32 v[62:63], v[186:187], v[74:75], v[78:79]
	v_cvt_pk_f32_fp8_sdwa v[152:153], v153 src0_sel:WORD_1
	v_pk_fma_f32 v[62:63], v[62:63], s[60:61], v[66:67] op_sel_hi:[1,0,1]
	v_pk_mul_f32 v[66:67], v[150:151], v[158:159] op_sel_hi:[0,1]
	v_pk_fma_f32 v[62:63], v[148:149], v[236:237], v[62:63] op_sel_hi:[0,1,1]
	v_pk_fma_f32 v[62:63], v[146:147], v[242:243], v[62:63] op_sel_hi:[0,1,1]
	v_pk_fma_f32 v[72:73], v[32:33], v[248:249], v[62:63] op_sel_hi:[0,1,1]
	v_pk_fma_f32 v[62:63], v[176:177], v[76:77], v[80:81]
	v_pk_fma_f32 v[82:83], v[148:149], v[198:199], v[82:83] op_sel_hi:[0,1,1]
	v_pk_fma_f32 v[62:63], v[62:63], s[60:61], v[66:67] op_sel_hi:[1,0,1]
	v_pk_fma_f32 v[84:85], v[148:149], v[204:205], v[84:85] op_sel_hi:[0,1,1]
	v_pk_fma_f32 v[62:63], v[148:149], v[156:157], v[62:63] op_sel_hi:[0,1,1]
	v_pk_fma_f32 v[62:63], v[146:147], v[154:155], v[62:63] op_sel_hi:[0,1,1]
	v_pk_fma_f32 v[82:83], v[146:147], v[208:209], v[82:83] op_sel_hi:[0,1,1]
	v_pk_fma_f32 v[84:85], v[146:147], v[210:211], v[84:85] op_sel_hi:[0,1,1]
	v_pk_fma_f32 v[88:89], v[32:33], v[152:153], v[62:63] op_sel_hi:[0,1,1]
	v_pk_fma_f32 v[82:83], v[32:33], v[214:215], v[82:83] op_sel_hi:[0,1,1]
	v_pk_fma_f32 v[84:85], v[32:33], v[216:217], v[84:85] op_sel_hi:[0,1,1]
	v_add_f32_e32 v3, v88, v89
	v_add_f32_e32 v32, v72, v73
	v_add_f32_e32 v3, v32, v3
	v_add_f32_e32 v32, v68, v69
	v_add_f32_e32 v62, v70, v71
	v_add_f32_e32 v32, v62, v32
	v_add_f32_e32 v3, v32, v3
	v_add_f32_e32 v32, v64, v65
	v_add_f32_e32 v62, v86, v87
	v_add_f32_e32 v32, v62, v32
	v_add_f32_e32 v62, v84, v85
	v_add_f32_e32 v63, v82, v83
	v_add_f32_e32 v62, v63, v62
	v_add_f32_e32 v32, v62, v32
	v_add_f32_e32 v3, v32, v3
	v_pk_mul_f32 v[62:63], v[172:173], v[200:201] op_sel_hi:[1,0]
	v_pk_mul_f32 v[74:75], v[174:175], v[200:201] op_sel_hi:[1,0]
	v_add_f32_dpp v3, v3, v3 quad_perm:[1,0,3,2] row_mask:0xf bank_mask:0xf bound_ctrl:1
	s_waitcnt vmcnt(0)
	v_pk_fma_f32 v[66:67], v[62:63], v[54:55], v[58:59]
	v_pk_fma_f32 v[62:63], v[74:75], v[46:47], v[50:51]
	v_add_f32_dpp v3, v3, v3 quad_perm:[2,3,0,1] row_mask:0xf bank_mask:0xf bound_ctrl:1
	s_mov_b64 s[6:7], -1
	s_and_b64 vcc, exec, s[8:9]
	v_add_f32_dpp v3, v3, v3 row_half_mirror row_mask:0xf bank_mask:0xf bound_ctrl:1
	s_nop 1
	v_add_f32_dpp v3, v3, v3 row_mirror row_mask:0xf bank_mask:0xf bound_ctrl:1
	s_waitcnt lgkmcnt(0)
	v_mov_b32_e32 v32, v3
	s_nop 1
	v_permlane16_swap_b32_e32 v3, v32
	v_add_f32_e32 v3, v3, v32
	v_mov_b32_e32 v32, v3
	s_nop 1
	v_permlane32_swap_b32_e32 v3, v32
	v_add_f32_e32 v3, v3, v32
	v_mul_f32_e32 v32, 0x3a800000, v3
	v_pk_add_f32 v[76:77], v[72:73], v[32:33] op_sel_hi:[1,0] neg_lo:[0,1] neg_hi:[0,1]
	v_pk_add_f32 v[72:73], v[88:89], v[32:33] op_sel_hi:[1,0] neg_lo:[0,1] neg_hi:[0,1]
	v_pk_add_f32 v[74:75], v[70:71], v[32:33] op_sel_hi:[1,0] neg_lo:[0,1] neg_hi:[0,1]
	v_pk_add_f32 v[70:71], v[68:69], v[32:33] op_sel_hi:[1,0] neg_lo:[0,1] neg_hi:[0,1]
	v_pk_mul_f32 v[146:147], v[76:77], v[76:77]
	v_pk_mul_f32 v[148:149], v[72:73], v[72:73]
	v_pk_add_f32 v[82:83], v[82:83], v[32:33] op_sel_hi:[1,0] neg_lo:[0,1] neg_hi:[0,1]
	v_pk_add_f32 v[78:79], v[84:85], v[32:33] op_sel_hi:[1,0] neg_lo:[0,1] neg_hi:[0,1]
	v_pk_add_f32 v[84:85], v[86:87], v[32:33] op_sel_hi:[1,0] neg_lo:[0,1] neg_hi:[0,1]
	v_pk_add_f32 v[80:81], v[64:65], v[32:33] op_sel_hi:[1,0] neg_lo:[0,1] neg_hi:[0,1]
	v_pk_mul_f32 v[90:91], v[74:75], v[74:75]
	v_pk_mul_f32 v[92:93], v[70:71], v[70:71]
	v_add_f32_e32 v3, v148, v149
	v_add_f32_e32 v32, v146, v147
	v_add_f32_e32 v3, v32, v3
	v_add_f32_e32 v32, v92, v93
	v_add_f32_e32 v90, v90, v91
	v_pk_mul_f32 v[64:65], v[82:83], v[82:83]
	v_pk_mul_f32 v[68:69], v[78:79], v[78:79]
	v_pk_mul_f32 v[86:87], v[84:85], v[84:85]
	v_pk_mul_f32 v[88:89], v[80:81], v[80:81]
	v_add_f32_e32 v32, v90, v32
	v_add_f32_e32 v3, v32, v3
	v_add_f32_e32 v32, v88, v89
	v_add_f32_e32 v86, v86, v87
	v_add_f32_e32 v68, v68, v69
	v_add_f32_e32 v64, v64, v65
	v_add_f32_e32 v32, v86, v32
	v_add_f32_e32 v64, v64, v68
	v_add_f32_e32 v32, v64, v32
	v_add_f32_e32 v3, v32, v3
	v_pk_mul_f32 v[64:65], v[168:169], v[200:201] op_sel_hi:[1,0]
	v_pk_mul_f32 v[86:87], v[170:171], v[200:201] op_sel_hi:[1,0]
	v_add_f32_dpp v3, v3, v3 quad_perm:[1,0,3,2] row_mask:0xf bank_mask:0xf bound_ctrl:1
	v_pk_fma_f32 v[68:69], v[64:65], v[56:57], v[60:61]
	v_pk_fma_f32 v[64:65], v[86:87], v[48:49], v[52:53]
	v_add_f32_dpp v3, v3, v3 quad_perm:[2,3,0,1] row_mask:0xf bank_mask:0xf bound_ctrl:1
	s_nop 1
	v_add_f32_dpp v3, v3, v3 row_half_mirror row_mask:0xf bank_mask:0xf bound_ctrl:1
	s_nop 1
	v_add_f32_dpp v3, v3, v3 row_mirror row_mask:0xf bank_mask:0xf bound_ctrl:1
	s_waitcnt lgkmcnt(0)
	v_mov_b32_e32 v32, v3
	s_nop 1
	v_permlane16_swap_b32_e32 v3, v32
	v_add_f32_e32 v3, v3, v32
	v_mov_b32_e32 v32, v3
	s_nop 1
	v_permlane32_swap_b32_e32 v3, v32
	s_cbranch_vccz .LBB0_711
; __device__ __forceinline__ u32x4 pack8(const float (&f)[8]) { u32x4 o; o.x = cvt_pk_bf16(f[0], f[1]); o.y = cvt_pk_bf16(f[2], f[3]); o.z = cvt_pk_bf16(f[4], f[5]); o.w = cvt_pk_bf16(f[6], f[7]); return o; }
; __device__ __forceinline__ float wave_max(float v) { v = fmaxf(v, dpp_f<0xB1>(v)); v = fmaxf(v, dpp_f<0x4E>(v)); v = fmaxf(v, dpp_f<0x141>(v)); v = fmaxf(v, dpp_f<0x140>(v)); v = fmaxf(v, xor_sw<16>(v)); return max_x32(v); }
; __device__ __forceinline__ float q8_row16(const float (&o)[16], unsigned char* qrow, int lane) {
;     float am = 0.f;
; #pragma unroll
;     for (int i = 0; i < 16; ++i) am = fmaxf(am, fabsf(o[i]));
;     am = wave_max(am);
;     const float qs = am > 0.f ? am * (1.0f / 127.0f) : 1.0f, qinv = 1.0f / qs;
; #pragma unroll
;     for (int hf = 0; hf < 2; ++hf) { u32x2 q; q.x = q8x4(o[8 * hf], o[8 * hf + 1], o[8 * hf + 2], o[8 * hf + 3], qinv); q.y = q8x4(o[8 * hf + 4], o[8 * hf + 5], o[8 * hf + 6], o[8 * hf + 7], qinv);
;         *(u32x2*)(qrow + 512 * hf + 8 * lane) = q; }
;     return qs;
; }
; __device__ __forceinline__ void store_bf16_row16(const float (&o)[16], bf16_t* row, int lane) {
; #pragma unroll
;     for (int hf = 0; hf < 2; ++hf) { const float (&oh)[8] = *(const float (*)[8])(o + 8 * hf); *(u32x4*)(row + 512 * hf + 8 * lane) = pack8(oh); }
; __global__ void __launch_bounds__(NWAVES * 64, 2) mk_fwd(Args args) {
;     ...
;                     } else {
;                         store_bf16_row16(o[j], XBo + (size_t)t * D, lane);
;                         const float qs = q8_row16(o[j], XQo + (size_t)t * D, lane);
;                         if (lane == 0) SXo[t] = qs;
	v_max3_f32 v89, |v24|, 0, |v25|
	v_max3_f32 v89, v89, |v26|, |v27|
	v_max3_f32 v89, v89, |v20|, |v21|
	v_max3_f32 v89, v89, |v22|, |v23|
	v_max3_f32 v89, v89, |v66|, |v67|
	v_max3_f32 v89, v89, |v68|, |v69|
	v_max3_f32 v89, v89, |v62|, |v63|
	v_max3_f32 v89, v89, |v64|, |v65|
	s_ashr_i32 s11, s10, 31
	s_lshl_b64 s[12:13], s[10:11], 11
	v_mov_b32_dpp v90, v89 quad_perm:[1,0,3,2] row_mask:0xf bank_mask:0xf bound_ctrl:1
	v_max_f32_e32 v90, v90, v90
	v_max_f32_e32 v89, v89, v90
	v_lshl_add_u64 v[92:93], v[106:107], 0, s[12:13]
	v_cvt_pk_bf16_f32 v86, v24, v25
	v_mov_b32_dpp v90, v89 quad_perm:[2,3,0,1] row_mask:0xf bank_mask:0xf bound_ctrl:1
	v_max_f32_e32 v90, v90, v90
	v_max_f32_e32 v89, v89, v90
	v_cvt_pk_bf16_f32 v87, v26, v27
	v_cvt_pk_bf16_f32 v88, v20, v21
	v_mov_b32_dpp v90, v89 row_half_mirror row_mask:0xf bank_mask:0xf bound_ctrl:1
	v_max_f32_e32 v90, v90, v90
	v_max_f32_e32 v89, v89, v90
	s_lshl_b64 s[6:7], s[10:11], 10
	s_nop 0
	v_mov_b32_dpp v90, v89 row_mirror row_mask:0xf bank_mask:0xf bound_ctrl:1
	v_max_f32_e32 v90, v90, v90
	v_max_f32_e32 v90, v89, v90
	v_cvt_pk_bf16_f32 v89, v22, v23
	global_store_dwordx4 v[92:93], v[86:89], off
	s_waitcnt lgkmcnt(0)
	s_nop 0
	v_mov_b32_e32 v91, v90
	s_nop 1
	v_permlane16_swap_b32_e32 v90, v91
	v_max_f32_e32 v86, v91, v91
	v_max_f32_e32 v86, v90, v86
	v_mov_b32_e32 v87, v86
	s_nop 1
	v_permlane32_swap_b32_e32 v86, v87
	v_max_f32_e32 v87, v87, v87
	v_max_f32_e32 v86, v86, v86
	v_max_f32_e32 v86, v86, v87
	v_mul_f32_e32 v87, 0x3c010204, v86
	v_cmp_lt_f32_e32 vcc, 0, v86
	v_cvt_pk_bf16_f32 v88, v66, v67
	v_cvt_pk_bf16_f32 v89, v68, v69
	v_cndmask_b32_e32 v86, 1.0, v87, vcc
	v_div_scale_f32 v87, s[12:13], v86, v86, 1.0
	v_rcp_f32_e32 v146, v87
	v_cvt_pk_bf16_f32 v90, v62, v63
	v_cvt_pk_bf16_f32 v91, v64, v65
	global_store_dwordx4 v[92:93], v[88:91], off offset:1024
	s_nop 1
	v_fma_f32 v88, -v87, v146, 1.0
	v_fmac_f32_e32 v146, v88, v146
	v_div_scale_f32 v88, vcc, 1.0, v86, 1.0
	v_mul_f32_e32 v89, v88, v146
	v_fma_f32 v90, -v87, v89, v88
	v_fmac_f32_e32 v89, v90, v146
	v_fma_f32 v87, -v87, v89, v88
	v_div_fmas_f32 v87, v87, v146, v89
	v_div_fixup_f32 v87, v87, v86, 1.0
	v_fmaak_f32 v90, v24, v87, 0x4b400000
	v_fmaak_f32 v91, v25, v87, 0x4b400000
	v_fmaak_f32 v92, v26, v87, 0x4b400000
	v_fmaak_f32 v93, v27, v87, 0x4b400000
	v_perm_b32 v92, v93, v92, s61
	v_perm_b32 v90, v91, v90, s61
	v_perm_b32 v90, v92, v90, s79
	v_fmaak_f32 v91, v20, v87, 0x4b400000
	v_fmaak_f32 v92, v21, v87, 0x4b400000
	v_fmaak_f32 v93, v22, v87, 0x4b400000
	v_fmaak_f32 v146, v23, v87, 0x4b400000
	v_perm_b32 v93, v146, v93, s61
	v_perm_b32 v91, v92, v91, s61
	v_lshl_add_u64 v[88:89], v[108:109], 0, s[6:7]
	v_perm_b32 v91, v93, v91, s79
	global_store_dwordx2 v[88:89], v[90:91], off
	v_fmaak_f32 v90, v66, v87, 0x4b400000
	v_fmaak_f32 v91, v67, v87, 0x4b400000
	v_fmaak_f32 v92, v68, v87, 0x4b400000
	v_fmaak_f32 v93, v69, v87, 0x4b400000
	v_perm_b32 v92, v93, v92, s61
	v_perm_b32 v90, v91, v90, s61
	v_perm_b32 v90, v92, v90, s79
	v_fmaak_f32 v91, v62, v87, 0x4b400000
	v_fmaak_f32 v92, v63, v87, 0x4b400000
	v_fmaak_f32 v93, v64, v87, 0x4b400000
	v_fmaak_f32 v87, v65, v87, 0x4b400000
	v_perm_b32 v87, v87, v93, s61
	v_perm_b32 v91, v92, v91, s61
	v_perm_b32 v91, v87, v91, s79
	global_store_dwordx2 v[88:89], v[90:91], off offset:512
	s_and_saveexec_b64 s[6:7], s[4:5]
	s_cbranch_execz .LBB0_710
	s_lshl_b64 s[12:13], s[10:11], 2
	v_readlane_b32 s14, v254, 11
	v_readlane_b32 s15, v254, 12
	s_add_u32 s12, s14, s12
	s_addc_u32 s13, s15, s13
	global_store_dword v33, v86, s[12:13]

; __device__ __forceinline__ u32x4 pack8(const float (&f)[8]) { u32x4 o; o.x = cvt_pk_bf16(f[0], f[1]); o.y = cvt_pk_bf16(f[2], f[3]); o.z = cvt_pk_bf16(f[4], f[5]); o.w = cvt_pk_bf16(f[6], f[7]); return o; }
; __device__ __forceinline__ float wave_max(float v) { v = fmaxf(v, dpp_f<0xB1>(v)); v = fmaxf(v, dpp_f<0x4E>(v)); v = fmaxf(v, dpp_f<0x141>(v)); v = fmaxf(v, dpp_f<0x140>(v)); v = fmaxf(v, xor_sw<16>(v)); return max_x32(v); }
; __device__ __forceinline__ float q8_row16(const float (&o)[16], unsigned char* qrow, int lane) {
;     float am = 0.f;
; #pragma unroll
;     for (int i = 0; i < 16; ++i) am = fmaxf(am, fabsf(o[i]));
;     am = wave_max(am);
;     const float qs = am > 0.f ? am * (1.0f / 127.0f) : 1.0f, qinv = 1.0f / qs;
; #pragma unroll
;     for (int hf = 0; hf < 2; ++hf) { u32x2 q; q.x = q8x4(o[8 * hf], o[8 * hf + 1], o[8 * hf + 2], o[8 * hf + 3], qinv); q.y = q8x4(o[8 * hf + 4], o[8 * hf + 5], o[8 * hf + 6], o[8 * hf + 7], qinv);
;         *(u32x2*)(qrow + 512 * hf + 8 * lane) = q; }
;     return qs;
; }
; __device__ __forceinline__ void store_bf16_row16(const float (&o)[16], bf16_t* row, int lane) {
; #pragma unroll
;     for (int hf = 0; hf < 2; ++hf) { const float (&oh)[8] = *(const float (*)[8])(o + 8 * hf); *(u32x4*)(row + 512 * hf + 8 * lane) = pack8(oh); }
; __global__ void __launch_bounds__(NWAVES * 64, 2) mk_fwd(Args args) {
;     ...
;                     } else {
;                         store_bf16_row16(o[j], XBo + (size_t)t * D, lane);
;                         const float qs = q8_row16(o[j], XQo + (size_t)t * D, lane);
;                         if (lane == 0) SXo[t] = qs;
.LBB0_715:
	v_max3_f32 v3, |v38|, 0, |v39|
	v_max3_f32 v3, v3, |v40|, |v41|
	v_max3_f32 v3, v3, |v24|, |v25|
	v_max3_f32 v3, v3, |v26|, |v27|
	v_max3_f32 v3, v3, |v28|, |v29|
	v_max3_f32 v3, v3, |v30|, |v31|
	v_max3_f32 v3, v3, |v20|, |v21|
	v_max3_f32 v3, v3, |v22|, |v23|
	s_lshl_b64 s[14:15], s[6:7], 11
	v_lshl_add_u64 v[42:43], v[106:107], 0, s[14:15]
	v_mov_b32_dpp v32, v3 quad_perm:[1,0,3,2] row_mask:0xf bank_mask:0xf bound_ctrl:1
	v_max_f32_e32 v32, v32, v32
	v_max_f32_e32 v3, v3, v32
	v_cvt_pk_bf16_f32 v34, v38, v39
	v_cvt_pk_bf16_f32 v35, v40, v41
	v_mov_b32_dpp v32, v3 quad_perm:[2,3,0,1] row_mask:0xf bank_mask:0xf bound_ctrl:1
	v_max_f32_e32 v32, v32, v32
	v_max_f32_e32 v3, v3, v32
	v_cvt_pk_bf16_f32 v36, v24, v25
	v_cvt_pk_bf16_f32 v37, v26, v27
	v_mov_b32_dpp v32, v3 row_half_mirror row_mask:0xf bank_mask:0xf bound_ctrl:1
	v_max_f32_e32 v32, v32, v32
	v_max_f32_e32 v3, v3, v32
	global_store_dwordx4 v[42:43], v[34:37], off
	s_lshl_b64 s[10:11], s[6:7], 10
	v_mov_b32_dpp v32, v3 row_mirror row_mask:0xf bank_mask:0xf bound_ctrl:1
	v_max_f32_e32 v32, v32, v32
	v_max_f32_e32 v3, v3, v32
	v_cvt_pk_bf16_f32 v34, v28, v29
	v_cvt_pk_bf16_f32 v35, v30, v31
	v_cvt_pk_bf16_f32 v36, v20, v21
	v_cvt_pk_bf16_f32 v37, v22, v23
	s_waitcnt lgkmcnt(0)
	v_mov_b32_e32 v32, v3
	s_nop 1
	v_permlane16_swap_b32_e32 v3, v32
	v_max_f32_e32 v32, v32, v32
	v_max_f32_e32 v3, v3, v32
	v_mov_b32_e32 v32, v3
	s_nop 1
	v_permlane32_swap_b32_e32 v3, v32
	v_max_f32_e32 v32, v32, v32
	v_max_f32_e32 v3, v3, v3
	v_max_f32_e32 v3, v3, v32
	v_mul_f32_e32 v32, 0x3c010204, v3
	v_cmp_lt_f32_e32 vcc, 0, v3
	global_store_dwordx4 v[42:43], v[34:37], off offset:1024
	s_nop 0
	v_cndmask_b32_e32 v3, 1.0, v32, vcc
	v_div_scale_f32 v32, s[14:15], v3, v3, 1.0
	v_rcp_f32_e32 v44, v32
	s_nop 0
	v_fma_f32 v34, -v32, v44, 1.0
	v_fmac_f32_e32 v44, v34, v44
	v_div_scale_f32 v34, vcc, 1.0, v3, 1.0
	v_mul_f32_e32 v35, v34, v44
	v_fma_f32 v36, -v32, v35, v34
	v_fmac_f32_e32 v35, v36, v44
	v_fma_f32 v32, -v32, v35, v34
	v_div_fmas_f32 v32, v32, v44, v35
	v_div_fixup_f32 v32, v32, v3, 1.0
	v_fmaak_f32 v36, v38, v32, 0x4b400000
	v_fmaak_f32 v37, v39, v32, 0x4b400000
	v_fmaak_f32 v42, v40, v32, 0x4b400000
	v_fmaak_f32 v43, v41, v32, 0x4b400000
	v_perm_b32 v42, v43, v42, s61
	v_perm_b32 v36, v37, v36, s61
	v_perm_b32 v36, v42, v36, s79
	v_fmaak_f32 v37, v24, v32, 0x4b400000
	v_fmaak_f32 v42, v25, v32, 0x4b400000
	v_fmaak_f32 v43, v26, v32, 0x4b400000
	v_fmaak_f32 v44, v27, v32, 0x4b400000
	v_perm_b32 v43, v44, v43, s61
	v_perm_b32 v37, v42, v37, s61
	v_lshl_add_u64 v[34:35], v[108:109], 0, s[10:11]
	v_perm_b32 v37, v43, v37, s79
	global_store_dwordx2 v[34:35], v[36:37], off
	v_fmaak_f32 v36, v28, v32, 0x4b400000
	v_fmaak_f32 v37, v29, v32, 0x4b400000
	v_fmaak_f32 v42, v30, v32, 0x4b400000
	v_fmaak_f32 v43, v31, v32, 0x4b400000
	v_perm_b32 v42, v43, v42, s61
	v_perm_b32 v36, v37, v36, s61
	v_perm_b32 v36, v42, v36, s79
	v_fmaak_f32 v37, v20, v32, 0x4b400000
	v_fmaak_f32 v42, v21, v32, 0x4b400000
	v_fmaak_f32 v43, v22, v32, 0x4b400000
	v_fmaak_f32 v32, v23, v32, 0x4b400000
	v_perm_b32 v32, v32, v43, s61
	v_perm_b32 v37, v42, v37, s61
	v_perm_b32 v37, v32, v37, s79
	global_store_dwordx2 v[34:35], v[36:37], off offset:512
	s_and_saveexec_b64 s[10:11], s[4:5]
	s_cbranch_execz .LBB0_717
	s_lshl_b64 s[14:15], s[6:7], 2
	v_readlane_b32 s16, v254, 11
	v_readlane_b32 s17, v254, 12
	s_add_u32 s14, s16, s14
	s_addc_u32 s15, s17, s15
	global_store_dword v33, v3, s[14:15]
